# T12 MFMA issue order inside the bf16 GEMM blocks: snake order so consecutive MFMAs share one source fragment (pure reorder of independent MFMAs, on top of v10)
# speedup vs baseline: 1.0085x; 1.0085x over previous
; #define PG8_STAGE(bufoff, gbase, voff) do { _Pragma("unroll") for (int _i = 0; _i < 2; ++_i) \
;         __builtin_amdgcn_global_load_lds((const unsigned*)((const char*)(gbase) + (voff)[_i]), (PG8_LAS unsigned*)(lds + (bufoff) + ldsw + _i * 8192), 16, 0, 0); } while (0)
; #define PG8_LDA(dst, b, h) do { _Pragma("unroll") for (int m = 0; m < 4; ++m) _Pragma("unroll") for (int k = 0; k < 2; ++k) dst[m][k] = *(const PG8_LAS bf16x8*)(lds + PG8_SA(b, h) + aoff + m * 2048 + k * 1024); } while (0)
; #define PG8_LDB(dst, b, h) do { _Pragma("unroll") for (int n = 0; n < 2; ++n) _Pragma("unroll") for (int k = 0; k < 2; ++k) dst[n][k] = *(const PG8_LAS bf16x8*)(lds + PG8_SB(b, h) + boff + n * 2048 + k * 1024); } while (0)
; #define PG8_WAIT_V(n) asm volatile("s_waitcnt vmcnt(" #n ")" ::: "memory")
; #define PG8_WAIT_L(n) asm volatile("s_waitcnt lgkmcnt(" #n ")" ::: "memory")
; #define PG8_BAR __builtin_amdgcn_s_barrier()
; #define PG8_SCHED __builtin_amdgcn_sched_barrier(0)
; template <class Epi, class Sched, bool ALIGN_EPI = false, bool SP2 = false>
; __device__ __forceinline__ void gemm_phase(PG8_LAS unsigned char* lds, const Gemm g, const Sched& S, const Epi& E) {
;     ...
;         const bool has_next = S.next(ui + 1, nxt);
;         const char* nA = has_next ? (const char*)g.A + (size_t)nxt.pm * tstep : cA; const char* nB = has_next ? (const char*)g.Bt + (size_t)nxt.pn * tstep : cB;
;         for (int t = 0; t < nt; t += 2) {
;             const bool last = (t == nt - 2);
;             const char* a1 = cA + (size_t)(t + 1) * kstep;
;             const char* a2 = last ? nA : cA + (size_t)(t + 2) * kstep; const char* b2 = last ? nB : cB + (size_t)(t + 2) * kstep;
;             const char* a3 = a2 + kstep; const char* b3 = b2 + kstep;
;             if (last && has_next) S.a_ready(nxt);
;             if constexpr (SP2) {
;             PG8_LDB(B0, 0, 0); PG8_LDB(B1, 0, 1); PG8_SCHED; PG8_LDA(At, 0, 0); PG8_STAGE(PG8_SA(1, 1), a1 + hstep, voffA);
;             PG8_WAIT_V(8); PG8_WAIT_L(0); PG8_BAR; PG8_MMA(0, 0, At, B0); PG8_MMA(0, 1, At, B1); PG8_BAR; PG8_SCHED;
;             PG8_LDA(At, 0, 1); PG8_STAGE(PG8_SB(0, 0), b2, voffB); PG8_STAGE(PG8_SB(0, 1), b2 + hstep, voffB); PG8_STAGE(PG8_SA(0, 0), a2, voffA);
;             PG8_WAIT_V(8); PG8_WAIT_L(0); PG8_BAR; PG8_MMA(1, 0, At, B0); PG8_MMA(1, 1, At, B1); PG8_BAR; PG8_SCHED;
.LBB0_366:
	s_ashr_i32 s23, s22, 31
	s_lshl_b64 s[24:25], s[22:23], 20
	s_add_u32 s24, s70, s24
	s_addc_u32 s25, s71, s25
	s_and_b64 s[26:27], s[2:3], exec
	s_cselect_b32 s23, s25, s31
	s_cselect_b32 s29, s24, s30
	s_ashr_i32 s21, s20, 31
	s_lshl_b64 s[26:27], s[20:21], 20
	s_add_u32 s26, s33, s26
	s_addc_u32 s27, s38, s27
	s_and_b64 s[36:37], s[2:3], exec
	s_cselect_b32 s21, s27, s35
	s_cselect_b32 s55, s26, s34
	s_add_u32 s30, s30, 0x80080
	s_addc_u32 s31, s31, 0
	s_add_u32 s56, s34, 0x100
	s_addc_u32 s57, s35, 0
	s_mov_b32 s58, -2
	v_add_u32_e32 v248, 0x18000, v154
	v_add_u32_e32 v249, 0x1c000, v154
	ds_read_b128 v[148:151], v156
	ds_read_b128 v[160:163], v156 offset:1024
	ds_read_b128 v[164:167], v156 offset:2048
	ds_read_b128 v[168:171], v156 offset:3072
	ds_read_b128 v[172:175], v157
	ds_read_b128 v[176:179], v157 offset:1024
	ds_read_b128 v[180:183], v157 offset:2048
	ds_read_b128 v[188:191], v157 offset:3072
	s_add_u32 s34, s30, 0xfff80080
	s_addc_u32 s35, s31, -1
	s_cmp_eq_u32 s58, 28
	s_cselect_b32 s37, s23, s35
	s_cselect_b32 s36, s29, s34
	s_cselect_b32 s35, s21, s57
	s_cselect_b32 s34, s55, s56
	s_add_i32 m0, s42, 0xc000
	ds_read_b128 v[192:195], v158
	ds_read_b128 v[196:199], v158 offset:1024
	ds_read_b128 v[200:203], v158 offset:2048
	ds_read_b128 v[204:207], v158 offset:3072
	ds_read_b128 v[212:215], v158 offset:4096
	ds_read_b128 v[216:219], v158 offset:5120
	ds_read_b128 v[220:223], v158 offset:6144
	ds_read_b128 v[224:227], v158 offset:7168
	global_load_lds_dwordx4 v140, s[30:31]
	s_add_i32 m0, s42, 0xe000
	s_nop 0
	global_load_lds_dwordx4 v142, s[30:31]
	s_waitcnt vmcnt(8)
	s_waitcnt lgkmcnt(0)
	s_barrier
	s_setprio 1
	s_waitcnt lgkmcnt(0)
	v_mfma_f32_16x16x32_bf16 v[126:129], v[148:151], v[192:195], 0
	v_mfma_f32_16x16x32_bf16 v[122:125], v[164:167], v[192:195], 0
	v_mfma_f32_16x16x32_bf16 v[110:113], v[164:167], v[200:203], 0
	v_mfma_f32_16x16x32_bf16 v[118:121], v[148:151], v[200:203], 0
	v_mfma_f32_16x16x32_bf16 v[102:105], v[148:151], v[212:215], 0
	v_mfma_f32_16x16x32_bf16 v[94:97], v[164:167], v[212:215], 0
	v_mfma_f32_16x16x32_bf16 v[78:81], v[164:167], v[220:223], 0
	v_mfma_f32_16x16x32_bf16 v[86:89], v[148:151], v[220:223], 0
	v_mfma_f32_16x16x32_bf16 v[126:129], v[160:163], v[196:199], v[126:129]
	v_mfma_f32_16x16x32_bf16 v[122:125], v[168:171], v[196:199], v[122:125]
	v_mfma_f32_16x16x32_bf16 v[110:113], v[168:171], v[204:207], v[110:113]
	v_mfma_f32_16x16x32_bf16 v[118:121], v[160:163], v[204:207], v[118:121]
	v_mfma_f32_16x16x32_bf16 v[102:105], v[160:163], v[216:219], v[102:105]
	v_mfma_f32_16x16x32_bf16 v[94:97], v[168:171], v[216:219], v[94:97]
	v_mfma_f32_16x16x32_bf16 v[78:81], v[168:171], v[224:227], v[78:81]
	v_mfma_f32_16x16x32_bf16 v[86:89], v[160:163], v[224:227], v[86:89]
	s_setprio 0
	s_setprio 1
	v_mfma_f32_16x16x32_bf16 v[114:117], v[172:175], v[192:195], 0
	v_mfma_f32_16x16x32_bf16 v[106:109], v[180:183], v[192:195], 0
	v_mfma_f32_16x16x32_bf16 v[90:93], v[180:183], v[200:203], 0
	v_mfma_f32_16x16x32_bf16 v[98:101], v[172:175], v[200:203], 0
	v_mfma_f32_16x16x32_bf16 v[82:85], v[172:175], v[212:215], 0
	v_mfma_f32_16x16x32_bf16 v[74:77], v[180:183], v[212:215], 0
	v_mfma_f32_16x16x32_bf16 v[66:69], v[180:183], v[220:223], 0
	v_mfma_f32_16x16x32_bf16 v[70:73], v[172:175], v[220:223], 0
	v_mfma_f32_16x16x32_bf16 v[114:117], v[176:179], v[196:199], v[114:117]
	v_mfma_f32_16x16x32_bf16 v[106:109], v[188:191], v[196:199], v[106:109]
	v_mfma_f32_16x16x32_bf16 v[90:93], v[188:191], v[204:207], v[90:93]
	v_mfma_f32_16x16x32_bf16 v[98:101], v[176:179], v[204:207], v[98:101]
	v_mfma_f32_16x16x32_bf16 v[82:85], v[176:179], v[216:219], v[82:85]
	v_mfma_f32_16x16x32_bf16 v[74:77], v[188:191], v[216:219], v[74:77]
	v_mfma_f32_16x16x32_bf16 v[66:69], v[188:191], v[224:227], v[66:69]
	v_mfma_f32_16x16x32_bf16 v[70:73], v[176:179], v[224:227], v[70:73]
	s_setprio 0
	s_barrier
	s_add_i32 s59, s51, s39
	s_mov_b32 m0, s59
	ds_read_b128 v[192:195], v158 offset:16384
	ds_read_b128 v[196:199], v158 offset:17408
	ds_read_b128 v[200:203], v158 offset:18432
	ds_read_b128 v[204:207], v158 offset:19456
	ds_read_b128 v[212:215], v158 offset:20480
	ds_read_b128 v[216:219], v158 offset:21504
	ds_read_b128 v[220:223], v158 offset:22528
	ds_read_b128 v[224:227], v158 offset:23552
	global_load_lds_dwordx4 v134, s[34:35]
	s_add_i32 m0, s59, 0x2000
	s_add_u32 s60, s34, 0x80000
	s_addc_u32 s61, s35, 0
	s_add_i32 s59, s52, s39
	global_load_lds_dwordx4 v130, s[34:35]
	s_mov_b32 m0, s59
	s_nop 0
	global_load_lds_dwordx4 v134, s[60:61]
	s_add_i32 m0, s59, 0x2000
	s_nop 0
	global_load_lds_dwordx4 v130, s[60:61]
	s_mov_b32 m0, s42
	s_nop 0
	global_load_lds_dwordx4 v136, s[36:37]
	s_mov_b32 m0, s43
	s_nop 0
	global_load_lds_dwordx4 v132, s[36:37]
	s_waitcnt vmcnt(8)
	s_waitcnt lgkmcnt(0)
	s_barrier
; #define PG8_STAGE(bufoff, gbase, voff) do { _Pragma("unroll") for (int _i = 0; _i < 2; ++_i) \
;         __builtin_amdgcn_global_load_lds((const unsigned*)((const char*)(gbase) + (voff)[_i]), (PG8_LAS unsigned*)(lds + (bufoff) + ldsw + _i * 8192), 16, 0, 0); } while (0)
; #define PG8_LDA(dst, b, h) do { _Pragma("unroll") for (int m = 0; m < 4; ++m) _Pragma("unroll") for (int k = 0; k < 2; ++k) dst[m][k] = *(const PG8_LAS bf16x8*)(lds + PG8_SA(b, h) + aoff + m * 2048 + k * 1024); } while (0)
; #define PG8_LDB(dst, b, h) do { _Pragma("unroll") for (int n = 0; n < 2; ++n) _Pragma("unroll") for (int k = 0; k < 2; ++k) dst[n][k] = *(const PG8_LAS bf16x8*)(lds + PG8_SB(b, h) + boff + n * 2048 + k * 1024); } while (0)
; #define PG8_WAIT_V(n) asm volatile("s_waitcnt vmcnt(" #n ")" ::: "memory")
; #define PG8_WAIT_L(n) asm volatile("s_waitcnt lgkmcnt(" #n ")" ::: "memory")
; #define PG8_BAR __builtin_amdgcn_s_barrier()
; #define PG8_SCHED __builtin_amdgcn_sched_barrier(0)
; template <class Epi, class Sched, bool ALIGN_EPI = false, bool SP2 = false>
; __device__ __forceinline__ void gemm_phase(PG8_LAS unsigned char* lds, const Gemm g, const Sched& S, const Epi& E) {
;     ...
;             PG8_WAIT_V(8); PG8_WAIT_L(0); PG8_BAR; PG8_MMA(1, 0, At, B0); PG8_MMA(1, 1, At, B1); PG8_BAR; PG8_SCHED;
;             PG8_LDB(B0, 1, 0); PG8_LDB(B1, 1, 1); PG8_SCHED; PG8_LDA(At, 1, 0); PG8_STAGE(PG8_SA(0, 1), a2 + hstep, voffA);
;             PG8_WAIT_V(8); PG8_WAIT_L(0); PG8_BAR; PG8_MMA(0, 0, At, B0); PG8_MMA(0, 1, At, B1); PG8_BAR; PG8_SCHED;
	s_setprio 1
	s_waitcnt lgkmcnt(0)
	v_mfma_f32_16x16x32_bf16 v[62:65], v[148:151], v[192:195], 0
	v_mfma_f32_16x16x32_bf16 v[58:61], v[164:167], v[192:195], 0
	v_mfma_f32_16x16x32_bf16 v[46:49], v[164:167], v[200:203], 0
	v_mfma_f32_16x16x32_bf16 v[54:57], v[148:151], v[200:203], 0
	v_mfma_f32_16x16x32_bf16 v[38:41], v[148:151], v[212:215], 0
	v_mfma_f32_16x16x32_bf16 v[30:33], v[164:167], v[212:215], 0
	v_mfma_f32_16x16x32_bf16 v[14:17], v[164:167], v[220:223], 0
	v_mfma_f32_16x16x32_bf16 v[22:25], v[148:151], v[220:223], 0
	v_mfma_f32_16x16x32_bf16 v[62:65], v[160:163], v[196:199], v[62:65]
	v_mfma_f32_16x16x32_bf16 v[58:61], v[168:171], v[196:199], v[58:61]
	v_mfma_f32_16x16x32_bf16 v[46:49], v[168:171], v[204:207], v[46:49]
	v_mfma_f32_16x16x32_bf16 v[54:57], v[160:163], v[204:207], v[54:57]
	v_mfma_f32_16x16x32_bf16 v[38:41], v[160:163], v[216:219], v[38:41]
	v_mfma_f32_16x16x32_bf16 v[30:33], v[168:171], v[216:219], v[30:33]
	v_mfma_f32_16x16x32_bf16 v[14:17], v[168:171], v[224:227], v[14:17]
	v_mfma_f32_16x16x32_bf16 v[22:25], v[160:163], v[224:227], v[22:25]
	s_setprio 0
	s_setprio 1
	v_mfma_f32_16x16x32_bf16 v[50:53], v[172:175], v[192:195], 0
	v_mfma_f32_16x16x32_bf16 v[42:45], v[180:183], v[192:195], 0
	v_mfma_f32_16x16x32_bf16 v[26:29], v[180:183], v[200:203], 0
	v_mfma_f32_16x16x32_bf16 v[34:37], v[172:175], v[200:203], 0
	v_mfma_f32_16x16x32_bf16 v[18:21], v[172:175], v[212:215], 0
	v_mfma_f32_16x16x32_bf16 v[10:13], v[180:183], v[212:215], 0
	v_mfma_f32_16x16x32_bf16 v[2:5], v[180:183], v[220:223], 0
	v_mfma_f32_16x16x32_bf16 v[6:9], v[172:175], v[220:223], 0
	v_mfma_f32_16x16x32_bf16 v[50:53], v[176:179], v[196:199], v[50:53]
	v_mfma_f32_16x16x32_bf16 v[42:45], v[188:191], v[196:199], v[42:45]
	v_mfma_f32_16x16x32_bf16 v[26:29], v[188:191], v[204:207], v[26:29]
	v_mfma_f32_16x16x32_bf16 v[34:37], v[176:179], v[204:207], v[34:37]
	v_mfma_f32_16x16x32_bf16 v[18:21], v[176:179], v[216:219], v[18:21]
	v_mfma_f32_16x16x32_bf16 v[10:13], v[188:191], v[216:219], v[10:13]
	v_mfma_f32_16x16x32_bf16 v[2:5], v[188:191], v[224:227], v[2:5]
	v_mfma_f32_16x16x32_bf16 v[6:9], v[176:179], v[224:227], v[6:9]
	s_setprio 0
	s_barrier
	s_add_i32 s59, 0, 0x18000
	s_add_i32 s60, 0, 0x1c000
	ds_read_b128 v[148:151], v248
	ds_read_b128 v[160:163], v248 offset:1024
	ds_read_b128 v[164:167], v248 offset:2048
	ds_read_b128 v[168:171], v248 offset:3072
	ds_read_b128 v[172:175], v249
	ds_read_b128 v[176:179], v249 offset:1024
	ds_read_b128 v[180:183], v249 offset:2048
	ds_read_b128 v[188:191], v249 offset:3072
	s_add_u32 s36, s36, 0x80000
	s_addc_u32 s37, s37, 0
	s_mov_b32 m0, s44
	ds_read_b128 v[192:195], v158 offset:32768
	ds_read_b128 v[196:199], v158 offset:33792
	ds_read_b128 v[200:203], v158 offset:34816
	ds_read_b128 v[204:207], v158 offset:35840
	ds_read_b128 v[212:215], v158 offset:36864
	ds_read_b128 v[216:219], v158 offset:37888
	ds_read_b128 v[220:223], v158 offset:38912
	ds_read_b128 v[224:227], v158 offset:39936
	global_load_lds_dwordx4 v136, s[36:37]
	s_mov_b32 m0, s45
	s_nop 0
	global_load_lds_dwordx4 v132, s[36:37]
	s_waitcnt vmcnt(8)
	s_waitcnt lgkmcnt(0)
	s_barrier
	s_setprio 1
	s_waitcnt lgkmcnt(0)
	v_mfma_f32_16x16x32_bf16 v[126:129], v[148:151], v[192:195], v[126:129]
	v_mfma_f32_16x16x32_bf16 v[122:125], v[164:167], v[192:195], v[122:125]
	v_mfma_f32_16x16x32_bf16 v[110:113], v[164:167], v[200:203], v[110:113]
	v_mfma_f32_16x16x32_bf16 v[118:121], v[148:151], v[200:203], v[118:121]
	v_mfma_f32_16x16x32_bf16 v[102:105], v[148:151], v[212:215], v[102:105]
	v_mfma_f32_16x16x32_bf16 v[94:97], v[164:167], v[212:215], v[94:97]
	v_mfma_f32_16x16x32_bf16 v[78:81], v[164:167], v[220:223], v[78:81]
	v_mfma_f32_16x16x32_bf16 v[86:89], v[148:151], v[220:223], v[86:89]
	v_mfma_f32_16x16x32_bf16 v[126:129], v[160:163], v[196:199], v[126:129]
	v_mfma_f32_16x16x32_bf16 v[122:125], v[168:171], v[196:199], v[122:125]
	v_mfma_f32_16x16x32_bf16 v[110:113], v[168:171], v[204:207], v[110:113]
	v_mfma_f32_16x16x32_bf16 v[118:121], v[160:163], v[204:207], v[118:121]
	v_mfma_f32_16x16x32_bf16 v[102:105], v[160:163], v[216:219], v[102:105]
	v_mfma_f32_16x16x32_bf16 v[94:97], v[168:171], v[216:219], v[94:97]
	v_mfma_f32_16x16x32_bf16 v[78:81], v[168:171], v[224:227], v[78:81]
	v_mfma_f32_16x16x32_bf16 v[86:89], v[160:163], v[224:227], v[86:89]
	s_setprio 0
	s_setprio 1
	v_mfma_f32_16x16x32_bf16 v[114:117], v[172:175], v[192:195], v[114:117]
	v_mfma_f32_16x16x32_bf16 v[106:109], v[180:183], v[192:195], v[106:109]
	v_mfma_f32_16x16x32_bf16 v[90:93], v[180:183], v[200:203], v[90:93]
	v_mfma_f32_16x16x32_bf16 v[98:101], v[172:175], v[200:203], v[98:101]
	v_mfma_f32_16x16x32_bf16 v[82:85], v[172:175], v[212:215], v[82:85]
	v_mfma_f32_16x16x32_bf16 v[74:77], v[180:183], v[212:215], v[74:77]
	v_mfma_f32_16x16x32_bf16 v[66:69], v[180:183], v[220:223], v[66:69]
	v_mfma_f32_16x16x32_bf16 v[70:73], v[172:175], v[220:223], v[70:73]
	v_mfma_f32_16x16x32_bf16 v[114:117], v[176:179], v[196:199], v[114:117]
	v_mfma_f32_16x16x32_bf16 v[106:109], v[188:191], v[196:199], v[106:109]
	v_mfma_f32_16x16x32_bf16 v[90:93], v[188:191], v[204:207], v[90:93]
	v_mfma_f32_16x16x32_bf16 v[98:101], v[176:179], v[204:207], v[98:101]
	v_mfma_f32_16x16x32_bf16 v[82:85], v[176:179], v[216:219], v[82:85]
	v_mfma_f32_16x16x32_bf16 v[74:77], v[188:191], v[216:219], v[74:77]
	v_mfma_f32_16x16x32_bf16 v[66:69], v[188:191], v[224:227], v[66:69]
	v_mfma_f32_16x16x32_bf16 v[70:73], v[176:179], v[224:227], v[70:73]
	s_setprio 0
	s_barrier
; #define PG8_STAGE(bufoff, gbase, voff) do { _Pragma("unroll") for (int _i = 0; _i < 2; ++_i) \
;         __builtin_amdgcn_global_load_lds((const unsigned*)((const char*)(gbase) + (voff)[_i]), (PG8_LAS unsigned*)(lds + (bufoff) + ldsw + _i * 8192), 16, 0, 0); } while (0)
; #define PG8_LDA(dst, b, h) do { _Pragma("unroll") for (int m = 0; m < 4; ++m) _Pragma("unroll") for (int k = 0; k < 2; ++k) dst[m][k] = *(const PG8_LAS bf16x8*)(lds + PG8_SA(b, h) + aoff + m * 2048 + k * 1024); } while (0)
; #define PG8_LDB(dst, b, h) do { _Pragma("unroll") for (int n = 0; n < 2; ++n) _Pragma("unroll") for (int k = 0; k < 2; ++k) dst[n][k] = *(const PG8_LAS bf16x8*)(lds + PG8_SB(b, h) + boff + n * 2048 + k * 1024); } while (0)
; #define PG8_WAIT_V(n) asm volatile("s_waitcnt vmcnt(" #n ")" ::: "memory")
; #define PG8_WAIT_L(n) asm volatile("s_waitcnt lgkmcnt(" #n ")" ::: "memory")
; #define PG8_BAR __builtin_amdgcn_s_barrier()
; #define PG8_SCHED __builtin_amdgcn_sched_barrier(0)
; template <class Epi, class Sched, bool ALIGN_EPI = false, bool SP2 = false>
; __device__ __forceinline__ void gemm_phase(PG8_LAS unsigned char* lds, const Gemm g, const Sched& S, const Epi& E) {
;     ...
;             PG8_LDB(B0, 0, 0); PG8_LDB(B1, 0, 1); PG8_SCHED; PG8_LDA(At, 0, 0); PG8_STAGE(PG8_SA(1, 1), a1 + hstep, voffA);
;             PG8_WAIT_V(8); PG8_WAIT_L(0); PG8_BAR; PG8_MMA(0, 0, At, B0); PG8_MMA(0, 1, At, B1); PG8_BAR; PG8_SCHED;
;     ...
;             PG8_LDA(At, 1, 1); PG8_STAGE(PG8_SB(1, 0), b3, voffB); PG8_STAGE(PG8_SB(1, 1), b3 + hstep, voffB); PG8_STAGE(PG8_SA(1, 0), a3, voffA);
;             PG8_WAIT_V(8); PG8_WAIT_L(0); PG8_BAR; PG8_MMA(1, 0, At, B0); PG8_MMA(1, 1, At, B1); PG8_BAR; PG8_SCHED;
	s_add_u32 s98, s34, 0x80
	s_addc_u32 s99, s35, 0
	s_add_u32 s100, s36, 0xfff80080
	s_addc_u32 s101, s37, -1
	s_add_i32 s36, s59, s39
	s_mov_b32 m0, s36
	ds_read_b128 v[192:195], v158 offset:49152
	ds_read_b128 v[196:199], v158 offset:50176
	ds_read_b128 v[200:203], v158 offset:51200
	ds_read_b128 v[204:207], v158 offset:52224
	ds_read_b128 v[212:215], v158 offset:53248
	ds_read_b128 v[216:219], v158 offset:54272
	ds_read_b128 v[220:223], v158 offset:55296
	ds_read_b128 v[224:227], v158 offset:56320
	global_load_lds_dwordx4 v134, s[98:99]
	s_add_i32 m0, s36, 0x2000
	s_add_u32 s34, s34, 0x80080
	s_addc_u32 s35, s35, 0
	s_add_i32 s36, s60, s39
	global_load_lds_dwordx4 v130, s[98:99]
	s_mov_b32 m0, s36
	s_nop 0
	global_load_lds_dwordx4 v134, s[34:35]
	s_add_i32 m0, s36, 0x2000
	s_nop 0
	global_load_lds_dwordx4 v130, s[34:35]
	s_mov_b32 m0, s48
	s_nop 0
	global_load_lds_dwordx4 v136, s[100:101]
	s_mov_b32 m0, s49
	s_nop 0
	global_load_lds_dwordx4 v132, s[100:101]
	s_waitcnt vmcnt(8)
	s_waitcnt lgkmcnt(0)
	s_barrier
	s_setprio 1
	s_waitcnt lgkmcnt(0)
	v_mfma_f32_16x16x32_bf16 v[62:65], v[148:151], v[192:195], v[62:65]
	v_mfma_f32_16x16x32_bf16 v[58:61], v[164:167], v[192:195], v[58:61]
	v_mfma_f32_16x16x32_bf16 v[46:49], v[164:167], v[200:203], v[46:49]
	v_mfma_f32_16x16x32_bf16 v[54:57], v[148:151], v[200:203], v[54:57]
	v_mfma_f32_16x16x32_bf16 v[38:41], v[148:151], v[212:215], v[38:41]
	v_mfma_f32_16x16x32_bf16 v[30:33], v[164:167], v[212:215], v[30:33]
	v_mfma_f32_16x16x32_bf16 v[14:17], v[164:167], v[220:223], v[14:17]
	v_mfma_f32_16x16x32_bf16 v[22:25], v[148:151], v[220:223], v[22:25]
	v_mfma_f32_16x16x32_bf16 v[62:65], v[160:163], v[196:199], v[62:65]
	v_mfma_f32_16x16x32_bf16 v[58:61], v[168:171], v[196:199], v[58:61]
	v_mfma_f32_16x16x32_bf16 v[46:49], v[168:171], v[204:207], v[46:49]
	v_mfma_f32_16x16x32_bf16 v[54:57], v[160:163], v[204:207], v[54:57]
	v_mfma_f32_16x16x32_bf16 v[38:41], v[160:163], v[216:219], v[38:41]
	v_mfma_f32_16x16x32_bf16 v[30:33], v[168:171], v[216:219], v[30:33]
	v_mfma_f32_16x16x32_bf16 v[14:17], v[168:171], v[224:227], v[14:17]
	v_mfma_f32_16x16x32_bf16 v[22:25], v[160:163], v[224:227], v[22:25]
	s_setprio 0
	s_setprio 1
	v_mfma_f32_16x16x32_bf16 v[50:53], v[172:175], v[192:195], v[50:53]
	v_mfma_f32_16x16x32_bf16 v[42:45], v[180:183], v[192:195], v[42:45]
	v_mfma_f32_16x16x32_bf16 v[26:29], v[180:183], v[200:203], v[26:29]
	v_mfma_f32_16x16x32_bf16 v[34:37], v[172:175], v[200:203], v[34:37]
	v_mfma_f32_16x16x32_bf16 v[18:21], v[172:175], v[212:215], v[18:21]
	v_mfma_f32_16x16x32_bf16 v[10:13], v[180:183], v[212:215], v[10:13]
	v_mfma_f32_16x16x32_bf16 v[2:5], v[180:183], v[220:223], v[2:5]
	v_mfma_f32_16x16x32_bf16 v[6:9], v[172:175], v[220:223], v[6:9]
	v_mfma_f32_16x16x32_bf16 v[50:53], v[176:179], v[196:199], v[50:53]
	v_mfma_f32_16x16x32_bf16 v[42:45], v[188:191], v[196:199], v[42:45]
	v_mfma_f32_16x16x32_bf16 v[26:29], v[188:191], v[204:207], v[26:29]
	v_mfma_f32_16x16x32_bf16 v[34:37], v[176:179], v[204:207], v[34:37]
	v_mfma_f32_16x16x32_bf16 v[18:21], v[176:179], v[216:219], v[18:21]
	v_mfma_f32_16x16x32_bf16 v[10:13], v[188:191], v[216:219], v[10:13]
	v_mfma_f32_16x16x32_bf16 v[2:5], v[188:191], v[224:227], v[2:5]
	v_mfma_f32_16x16x32_bf16 v[6:9], v[176:179], v[224:227], v[6:9]
	s_setprio 0
	s_barrier
	s_add_i32 s58, s58, 2
	s_add_u32 s30, s30, 0x100
	s_addc_u32 s31, s31, 0
	s_add_u32 s56, s56, 0x100
	s_addc_u32 s57, s57, 0
	s_cmp_gt_u32 s58, 29
.LBB0_367:
	ds_read_b128 v[148:151], v156
	ds_read_b128 v[160:163], v156 offset:1024
	ds_read_b128 v[164:167], v156 offset:2048
	ds_read_b128 v[168:171], v156 offset:3072
	ds_read_b128 v[172:175], v157
	ds_read_b128 v[176:179], v157 offset:1024
	ds_read_b128 v[180:183], v157 offset:2048
	ds_read_b128 v[188:191], v157 offset:3072
	s_add_u32 s34, s30, 0xfff80080
	s_addc_u32 s35, s31, -1
	s_cmp_eq_u32 s58, 28
	s_cselect_b32 s37, s23, s35
	s_cselect_b32 s36, s29, s34
	s_cselect_b32 s35, s21, s57
	s_cselect_b32 s34, s55, s56
	s_add_i32 m0, s42, 0xc000
	ds_read_b128 v[192:195], v158
	ds_read_b128 v[196:199], v158 offset:1024
	ds_read_b128 v[200:203], v158 offset:2048
	ds_read_b128 v[204:207], v158 offset:3072
	ds_read_b128 v[212:215], v158 offset:4096
	ds_read_b128 v[216:219], v158 offset:5120
	ds_read_b128 v[220:223], v158 offset:6144
	ds_read_b128 v[224:227], v158 offset:7168
	global_load_lds_dwordx4 v140, s[30:31]
	s_add_i32 m0, s42, 0xe000
	s_nop 0
	global_load_lds_dwordx4 v142, s[30:31]
	s_waitcnt vmcnt(8)
	s_waitcnt lgkmcnt(0)
	s_barrier
; #define PG8_STAGE(bufoff, gbase, voff) do { _Pragma("unroll") for (int _i = 0; _i < 2; ++_i) \
;         __builtin_amdgcn_global_load_lds((const unsigned*)((const char*)(gbase) + (voff)[_i]), (PG8_LAS unsigned*)(lds + (bufoff) + ldsw + _i * 8192), 16, 0, 0); } while (0)
; #define PG8_LDA(dst, b, h) do { _Pragma("unroll") for (int m = 0; m < 4; ++m) _Pragma("unroll") for (int k = 0; k < 2; ++k) dst[m][k] = *(const PG8_LAS bf16x8*)(lds + PG8_SA(b, h) + aoff + m * 2048 + k * 1024); } while (0)
; #define PG8_WAIT_V(n) asm volatile("s_waitcnt vmcnt(" #n ")" ::: "memory")
; #define PG8_WAIT_L(n) asm volatile("s_waitcnt lgkmcnt(" #n ")" ::: "memory")
; #define PG8_BAR __builtin_amdgcn_s_barrier()
; #define PG8_SCHED __builtin_amdgcn_sched_barrier(0)
; template <class Epi, class Sched, bool ALIGN_EPI = false, bool SP2 = false>
; __device__ __forceinline__ void gemm_phase(PG8_LAS unsigned char* lds, const Gemm g, const Sched& S, const Epi& E) {
;     ...
;             PG8_WAIT_V(8); PG8_WAIT_L(0); PG8_BAR; PG8_MMA(0, 0, At, B0); PG8_MMA(0, 1, At, B1); PG8_BAR; PG8_SCHED;
;             PG8_LDA(At, 0, 1); PG8_STAGE(PG8_SB(0, 0), b2, voffB); PG8_STAGE(PG8_SB(0, 1), b2 + hstep, voffB); PG8_STAGE(PG8_SA(0, 0), a2, voffA);
;             PG8_WAIT_V(8); PG8_WAIT_L(0); PG8_BAR; PG8_MMA(1, 0, At, B0); PG8_MMA(1, 1, At, B1); PG8_BAR; PG8_SCHED;
	s_setprio 1
	s_waitcnt lgkmcnt(0)
	v_mfma_f32_16x16x32_bf16 v[126:129], v[148:151], v[192:195], v[126:129]
	v_mfma_f32_16x16x32_bf16 v[122:125], v[164:167], v[192:195], v[122:125]
	v_mfma_f32_16x16x32_bf16 v[110:113], v[164:167], v[200:203], v[110:113]
	v_mfma_f32_16x16x32_bf16 v[118:121], v[148:151], v[200:203], v[118:121]
	v_mfma_f32_16x16x32_bf16 v[102:105], v[148:151], v[212:215], v[102:105]
	v_mfma_f32_16x16x32_bf16 v[94:97], v[164:167], v[212:215], v[94:97]
	v_mfma_f32_16x16x32_bf16 v[78:81], v[164:167], v[220:223], v[78:81]
	v_mfma_f32_16x16x32_bf16 v[86:89], v[148:151], v[220:223], v[86:89]
	v_mfma_f32_16x16x32_bf16 v[126:129], v[160:163], v[196:199], v[126:129]
	v_mfma_f32_16x16x32_bf16 v[122:125], v[168:171], v[196:199], v[122:125]
	v_mfma_f32_16x16x32_bf16 v[110:113], v[168:171], v[204:207], v[110:113]
	v_mfma_f32_16x16x32_bf16 v[118:121], v[160:163], v[204:207], v[118:121]
	v_mfma_f32_16x16x32_bf16 v[102:105], v[160:163], v[216:219], v[102:105]
	v_mfma_f32_16x16x32_bf16 v[94:97], v[168:171], v[216:219], v[94:97]
	v_mfma_f32_16x16x32_bf16 v[78:81], v[168:171], v[224:227], v[78:81]
	v_mfma_f32_16x16x32_bf16 v[86:89], v[160:163], v[224:227], v[86:89]
	s_setprio 0
	s_setprio 1
	v_mfma_f32_16x16x32_bf16 v[114:117], v[172:175], v[192:195], v[114:117]
	v_mfma_f32_16x16x32_bf16 v[106:109], v[180:183], v[192:195], v[106:109]
	v_mfma_f32_16x16x32_bf16 v[90:93], v[180:183], v[200:203], v[90:93]
	v_mfma_f32_16x16x32_bf16 v[98:101], v[172:175], v[200:203], v[98:101]
	v_mfma_f32_16x16x32_bf16 v[82:85], v[172:175], v[212:215], v[82:85]
	v_mfma_f32_16x16x32_bf16 v[74:77], v[180:183], v[212:215], v[74:77]
	v_mfma_f32_16x16x32_bf16 v[66:69], v[180:183], v[220:223], v[66:69]
	v_mfma_f32_16x16x32_bf16 v[70:73], v[172:175], v[220:223], v[70:73]
	v_mfma_f32_16x16x32_bf16 v[114:117], v[176:179], v[196:199], v[114:117]
	v_mfma_f32_16x16x32_bf16 v[106:109], v[188:191], v[196:199], v[106:109]
	v_mfma_f32_16x16x32_bf16 v[90:93], v[188:191], v[204:207], v[90:93]
	v_mfma_f32_16x16x32_bf16 v[98:101], v[176:179], v[204:207], v[98:101]
	v_mfma_f32_16x16x32_bf16 v[82:85], v[176:179], v[216:219], v[82:85]
	v_mfma_f32_16x16x32_bf16 v[74:77], v[188:191], v[216:219], v[74:77]
	v_mfma_f32_16x16x32_bf16 v[66:69], v[188:191], v[224:227], v[66:69]
	v_mfma_f32_16x16x32_bf16 v[70:73], v[176:179], v[224:227], v[70:73]
	s_setprio 0
	s_barrier
	s_add_i32 s59, s51, s39
	s_mov_b32 m0, s59
	ds_read_b128 v[192:195], v158 offset:16384
	ds_read_b128 v[196:199], v158 offset:17408
	ds_read_b128 v[200:203], v158 offset:18432
	ds_read_b128 v[204:207], v158 offset:19456
	ds_read_b128 v[212:215], v158 offset:20480
	ds_read_b128 v[216:219], v158 offset:21504
	ds_read_b128 v[220:223], v158 offset:22528
	ds_read_b128 v[224:227], v158 offset:23552
	global_load_lds_dwordx4 v134, s[34:35]
	s_add_i32 m0, s59, 0x2000
	s_add_u32 s60, s34, 0x80000
	s_addc_u32 s61, s35, 0
	s_add_i32 s59, s52, s39
	global_load_lds_dwordx4 v130, s[34:35]
	s_mov_b32 m0, s59
	s_nop 0
	global_load_lds_dwordx4 v134, s[60:61]
	s_add_i32 m0, s59, 0x2000
	s_nop 0
	global_load_lds_dwordx4 v130, s[60:61]
	s_mov_b32 m0, s42
	s_nop 0
	global_load_lds_dwordx4 v136, s[36:37]
	s_mov_b32 m0, s43
	s_nop 0
	global_load_lds_dwordx4 v132, s[36:37]
	s_waitcnt vmcnt(8)
	s_waitcnt lgkmcnt(0)
	s_barrier
	s_setprio 1
	s_waitcnt lgkmcnt(0)
	v_mfma_f32_16x16x32_bf16 v[62:65], v[148:151], v[192:195], v[62:65]
	v_mfma_f32_16x16x32_bf16 v[58:61], v[164:167], v[192:195], v[58:61]
	v_mfma_f32_16x16x32_bf16 v[46:49], v[164:167], v[200:203], v[46:49]
	v_mfma_f32_16x16x32_bf16 v[54:57], v[148:151], v[200:203], v[54:57]
	v_mfma_f32_16x16x32_bf16 v[38:41], v[148:151], v[212:215], v[38:41]
	v_mfma_f32_16x16x32_bf16 v[30:33], v[164:167], v[212:215], v[30:33]
	v_mfma_f32_16x16x32_bf16 v[14:17], v[164:167], v[220:223], v[14:17]
	v_mfma_f32_16x16x32_bf16 v[22:25], v[148:151], v[220:223], v[22:25]
	v_mfma_f32_16x16x32_bf16 v[62:65], v[160:163], v[196:199], v[62:65]
	v_mfma_f32_16x16x32_bf16 v[58:61], v[168:171], v[196:199], v[58:61]
	v_mfma_f32_16x16x32_bf16 v[46:49], v[168:171], v[204:207], v[46:49]
	v_mfma_f32_16x16x32_bf16 v[54:57], v[160:163], v[204:207], v[54:57]
	v_mfma_f32_16x16x32_bf16 v[38:41], v[160:163], v[216:219], v[38:41]
	v_mfma_f32_16x16x32_bf16 v[30:33], v[168:171], v[216:219], v[30:33]
	v_mfma_f32_16x16x32_bf16 v[14:17], v[168:171], v[224:227], v[14:17]
	v_mfma_f32_16x16x32_bf16 v[22:25], v[160:163], v[224:227], v[22:25]
	s_setprio 0
	s_setprio 1
	v_mfma_f32_16x16x32_bf16 v[50:53], v[172:175], v[192:195], v[50:53]
	v_mfma_f32_16x16x32_bf16 v[42:45], v[180:183], v[192:195], v[42:45]
	v_mfma_f32_16x16x32_bf16 v[26:29], v[180:183], v[200:203], v[26:29]
	v_mfma_f32_16x16x32_bf16 v[34:37], v[172:175], v[200:203], v[34:37]
	v_mfma_f32_16x16x32_bf16 v[18:21], v[172:175], v[212:215], v[18:21]
	v_mfma_f32_16x16x32_bf16 v[10:13], v[180:183], v[212:215], v[10:13]
	v_mfma_f32_16x16x32_bf16 v[2:5], v[180:183], v[220:223], v[2:5]
	v_mfma_f32_16x16x32_bf16 v[6:9], v[172:175], v[220:223], v[6:9]
	v_mfma_f32_16x16x32_bf16 v[50:53], v[176:179], v[196:199], v[50:53]
	v_mfma_f32_16x16x32_bf16 v[42:45], v[188:191], v[196:199], v[42:45]
	v_mfma_f32_16x16x32_bf16 v[26:29], v[188:191], v[204:207], v[26:29]
	v_mfma_f32_16x16x32_bf16 v[34:37], v[176:179], v[204:207], v[34:37]
	v_mfma_f32_16x16x32_bf16 v[18:21], v[176:179], v[216:219], v[18:21]
	v_mfma_f32_16x16x32_bf16 v[10:13], v[188:191], v[216:219], v[10:13]
	v_mfma_f32_16x16x32_bf16 v[2:5], v[188:191], v[224:227], v[2:5]
	v_mfma_f32_16x16x32_bf16 v[6:9], v[176:179], v[224:227], v[6:9]
	s_setprio 0
	s_barrier
; #define PG8_STAGE(bufoff, gbase, voff) do { _Pragma("unroll") for (int _i = 0; _i < 2; ++_i) \
;         __builtin_amdgcn_global_load_lds((const unsigned*)((const char*)(gbase) + (voff)[_i]), (PG8_LAS unsigned*)(lds + (bufoff) + ldsw + _i * 8192), 16, 0, 0); } while (0)
; #define PG8_LDA(dst, b, h) do { _Pragma("unroll") for (int m = 0; m < 4; ++m) _Pragma("unroll") for (int k = 0; k < 2; ++k) dst[m][k] = *(const PG8_LAS bf16x8*)(lds + PG8_SA(b, h) + aoff + m * 2048 + k * 1024); } while (0)
; #define PG8_LDB(dst, b, h) do { _Pragma("unroll") for (int n = 0; n < 2; ++n) _Pragma("unroll") for (int k = 0; k < 2; ++k) dst[n][k] = *(const PG8_LAS bf16x8*)(lds + PG8_SB(b, h) + boff + n * 2048 + k * 1024); } while (0)
; #define PG8_WAIT_V(n) asm volatile("s_waitcnt vmcnt(" #n ")" ::: "memory")
; #define PG8_WAIT_L(n) asm volatile("s_waitcnt lgkmcnt(" #n ")" ::: "memory")
; #define PG8_BAR __builtin_amdgcn_s_barrier()
; #define PG8_SCHED __builtin_amdgcn_sched_barrier(0)
; template <class Epi, class Sched, bool ALIGN_EPI = false, bool SP2 = false>
; __device__ __forceinline__ void gemm_phase(PG8_LAS unsigned char* lds, const Gemm g, const Sched& S, const Epi& E) {
;     ...
;             PG8_LDB(B0, 1, 0); PG8_LDB(B1, 1, 1); PG8_SCHED; PG8_LDA(At, 1, 0); PG8_STAGE(PG8_SA(0, 1), a2 + hstep, voffA);
;             PG8_WAIT_V(8); PG8_WAIT_L(0); PG8_BAR; PG8_MMA(0, 0, At, B0); PG8_MMA(0, 1, At, B1); PG8_BAR; PG8_SCHED;
;             PG8_LDA(At, 1, 1); PG8_STAGE(PG8_SB(1, 0), b3, voffB); PG8_STAGE(PG8_SB(1, 1), b3 + hstep, voffB); PG8_STAGE(PG8_SA(1, 0), a3, voffA);
;             PG8_WAIT_V(8); PG8_WAIT_L(0); PG8_BAR; PG8_MMA(1, 0, At, B0); PG8_MMA(1, 1, At, B1); PG8_BAR; PG8_SCHED;
	s_add_i32 s59, 0, 0x18000
	s_add_i32 s60, 0, 0x1c000
	ds_read_b128 v[148:151], v248
	ds_read_b128 v[160:163], v248 offset:1024
	ds_read_b128 v[164:167], v248 offset:2048
	ds_read_b128 v[168:171], v248 offset:3072
	ds_read_b128 v[172:175], v249
	ds_read_b128 v[176:179], v249 offset:1024
	ds_read_b128 v[180:183], v249 offset:2048
	ds_read_b128 v[188:191], v249 offset:3072
	s_add_u32 s36, s36, 0x80000
	s_addc_u32 s37, s37, 0
	s_mov_b32 m0, s44
	ds_read_b128 v[192:195], v158 offset:32768
	ds_read_b128 v[196:199], v158 offset:33792
	ds_read_b128 v[200:203], v158 offset:34816
	ds_read_b128 v[204:207], v158 offset:35840
	ds_read_b128 v[212:215], v158 offset:36864
	ds_read_b128 v[216:219], v158 offset:37888
	ds_read_b128 v[220:223], v158 offset:38912
	ds_read_b128 v[224:227], v158 offset:39936
	global_load_lds_dwordx4 v136, s[36:37]
	s_mov_b32 m0, s45
	s_nop 0
	global_load_lds_dwordx4 v132, s[36:37]
	s_waitcnt vmcnt(8)
	s_waitcnt lgkmcnt(0)
	s_barrier
	s_setprio 1
	s_waitcnt lgkmcnt(0)
	v_mfma_f32_16x16x32_bf16 v[126:129], v[148:151], v[192:195], v[126:129]
	v_mfma_f32_16x16x32_bf16 v[122:125], v[164:167], v[192:195], v[122:125]
	v_mfma_f32_16x16x32_bf16 v[110:113], v[164:167], v[200:203], v[110:113]
	v_mfma_f32_16x16x32_bf16 v[118:121], v[148:151], v[200:203], v[118:121]
	v_mfma_f32_16x16x32_bf16 v[102:105], v[148:151], v[212:215], v[102:105]
	v_mfma_f32_16x16x32_bf16 v[94:97], v[164:167], v[212:215], v[94:97]
	v_mfma_f32_16x16x32_bf16 v[78:81], v[164:167], v[220:223], v[78:81]
	v_mfma_f32_16x16x32_bf16 v[86:89], v[148:151], v[220:223], v[86:89]
	v_mfma_f32_16x16x32_bf16 v[126:129], v[160:163], v[196:199], v[126:129]
	v_mfma_f32_16x16x32_bf16 v[122:125], v[168:171], v[196:199], v[122:125]
	v_mfma_f32_16x16x32_bf16 v[110:113], v[168:171], v[204:207], v[110:113]
	v_mfma_f32_16x16x32_bf16 v[118:121], v[160:163], v[204:207], v[118:121]
	v_mfma_f32_16x16x32_bf16 v[102:105], v[160:163], v[216:219], v[102:105]
	v_mfma_f32_16x16x32_bf16 v[94:97], v[168:171], v[216:219], v[94:97]
	v_mfma_f32_16x16x32_bf16 v[78:81], v[168:171], v[224:227], v[78:81]
	v_mfma_f32_16x16x32_bf16 v[86:89], v[160:163], v[224:227], v[86:89]
	s_setprio 0
	s_setprio 1
	v_mfma_f32_16x16x32_bf16 v[114:117], v[172:175], v[192:195], v[114:117]
	v_mfma_f32_16x16x32_bf16 v[106:109], v[180:183], v[192:195], v[106:109]
	v_mfma_f32_16x16x32_bf16 v[90:93], v[180:183], v[200:203], v[90:93]
	v_mfma_f32_16x16x32_bf16 v[98:101], v[172:175], v[200:203], v[98:101]
	v_mfma_f32_16x16x32_bf16 v[82:85], v[172:175], v[212:215], v[82:85]
	v_mfma_f32_16x16x32_bf16 v[74:77], v[180:183], v[212:215], v[74:77]
	v_mfma_f32_16x16x32_bf16 v[66:69], v[180:183], v[220:223], v[66:69]
	v_mfma_f32_16x16x32_bf16 v[70:73], v[172:175], v[220:223], v[70:73]
	v_mfma_f32_16x16x32_bf16 v[114:117], v[176:179], v[196:199], v[114:117]
	v_mfma_f32_16x16x32_bf16 v[106:109], v[188:191], v[196:199], v[106:109]
	v_mfma_f32_16x16x32_bf16 v[90:93], v[188:191], v[204:207], v[90:93]
	v_mfma_f32_16x16x32_bf16 v[98:101], v[176:179], v[204:207], v[98:101]
	v_mfma_f32_16x16x32_bf16 v[82:85], v[176:179], v[216:219], v[82:85]
	v_mfma_f32_16x16x32_bf16 v[74:77], v[188:191], v[216:219], v[74:77]
	v_mfma_f32_16x16x32_bf16 v[66:69], v[188:191], v[224:227], v[66:69]
	v_mfma_f32_16x16x32_bf16 v[70:73], v[176:179], v[224:227], v[70:73]
	s_setprio 0
	s_barrier
	s_add_u32 s98, s34, 0x80
	s_addc_u32 s99, s35, 0
	s_add_u32 s100, s36, 0xfff80080
	s_addc_u32 s101, s37, -1
	s_add_i32 s36, s59, s39
	s_mov_b32 m0, s36
	ds_read_b128 v[192:195], v158 offset:49152
	ds_read_b128 v[196:199], v158 offset:50176
	ds_read_b128 v[200:203], v158 offset:51200
	ds_read_b128 v[204:207], v158 offset:52224
	ds_read_b128 v[212:215], v158 offset:53248
	ds_read_b128 v[216:219], v158 offset:54272
	ds_read_b128 v[220:223], v158 offset:55296
	ds_read_b128 v[224:227], v158 offset:56320
	global_load_lds_dwordx4 v134, s[98:99]
	s_add_i32 m0, s36, 0x2000
	s_add_u32 s34, s34, 0x80080
	s_addc_u32 s35, s35, 0
	s_add_i32 s36, s60, s39
	global_load_lds_dwordx4 v130, s[98:99]
	s_mov_b32 m0, s36
	s_nop 0
	global_load_lds_dwordx4 v134, s[34:35]
	s_add_i32 m0, s36, 0x2000
	s_nop 0
	global_load_lds_dwordx4 v130, s[34:35]
	s_mov_b32 m0, s48
	s_nop 0
	global_load_lds_dwordx4 v136, s[100:101]
	s_mov_b32 m0, s49
	s_nop 0
	global_load_lds_dwordx4 v132, s[100:101]
	s_waitcnt vmcnt(8)
	s_waitcnt lgkmcnt(0)
	s_barrier
	s_setprio 1
	s_waitcnt lgkmcnt(0)
	v_mfma_f32_16x16x32_bf16 v[62:65], v[148:151], v[192:195], v[62:65]
	v_mfma_f32_16x16x32_bf16 v[58:61], v[164:167], v[192:195], v[58:61]
	v_mfma_f32_16x16x32_bf16 v[46:49], v[164:167], v[200:203], v[46:49]
	v_mfma_f32_16x16x32_bf16 v[54:57], v[148:151], v[200:203], v[54:57]
	v_mfma_f32_16x16x32_bf16 v[38:41], v[148:151], v[212:215], v[38:41]
	v_mfma_f32_16x16x32_bf16 v[30:33], v[164:167], v[212:215], v[30:33]
	v_mfma_f32_16x16x32_bf16 v[14:17], v[164:167], v[220:223], v[14:17]
	v_mfma_f32_16x16x32_bf16 v[22:25], v[148:151], v[220:223], v[22:25]
	v_mfma_f32_16x16x32_bf16 v[62:65], v[160:163], v[196:199], v[62:65]
	v_mfma_f32_16x16x32_bf16 v[58:61], v[168:171], v[196:199], v[58:61]
	v_mfma_f32_16x16x32_bf16 v[46:49], v[168:171], v[204:207], v[46:49]
	v_mfma_f32_16x16x32_bf16 v[54:57], v[160:163], v[204:207], v[54:57]
	v_mfma_f32_16x16x32_bf16 v[38:41], v[160:163], v[216:219], v[38:41]
	v_mfma_f32_16x16x32_bf16 v[30:33], v[168:171], v[216:219], v[30:33]
	v_mfma_f32_16x16x32_bf16 v[14:17], v[168:171], v[224:227], v[14:17]
	v_mfma_f32_16x16x32_bf16 v[22:25], v[160:163], v[224:227], v[22:25]
	s_setprio 0
	s_setprio 1
	v_mfma_f32_16x16x32_bf16 v[50:53], v[172:175], v[192:195], v[50:53]
	v_mfma_f32_16x16x32_bf16 v[42:45], v[180:183], v[192:195], v[42:45]
	v_mfma_f32_16x16x32_bf16 v[26:29], v[180:183], v[200:203], v[26:29]
	v_mfma_f32_16x16x32_bf16 v[34:37], v[172:175], v[200:203], v[34:37]
	v_mfma_f32_16x16x32_bf16 v[18:21], v[172:175], v[212:215], v[18:21]
	v_mfma_f32_16x16x32_bf16 v[10:13], v[180:183], v[212:215], v[10:13]
	v_mfma_f32_16x16x32_bf16 v[2:5], v[180:183], v[220:223], v[2:5]
	v_mfma_f32_16x16x32_bf16 v[6:9], v[172:175], v[220:223], v[6:9]
	v_mfma_f32_16x16x32_bf16 v[50:53], v[176:179], v[196:199], v[50:53]
	v_mfma_f32_16x16x32_bf16 v[42:45], v[188:191], v[196:199], v[42:45]
	v_mfma_f32_16x16x32_bf16 v[26:29], v[188:191], v[204:207], v[26:29]
	v_mfma_f32_16x16x32_bf16 v[34:37], v[176:179], v[204:207], v[34:37]
	v_mfma_f32_16x16x32_bf16 v[18:21], v[176:179], v[216:219], v[18:21]
	v_mfma_f32_16x16x32_bf16 v[10:13], v[188:191], v[216:219], v[10:13]
	v_mfma_f32_16x16x32_bf16 v[2:5], v[188:191], v[224:227], v[2:5]
	v_mfma_f32_16x16x32_bf16 v[6:9], v[176:179], v[224:227], v[6:9]
	s_setprio 0
	s_barrier
	s_add_i32 s58, s58, 2
	s_add_u32 s30, s30, 0x100
	s_addc_u32 s31, s31, 0
	s_add_u32 s56, s56, 0x100
	s_addc_u32 s57, s57, 0
	s_cmp_gt_u32 s58, 29
	s_cbranch_scc0 .LBB0_367
	s_and_b64 vcc, exec, s[8:9]
	s_cbranch_vccnz .LBB0_372
	v_lshl_add_u32 v148, s28, 8, v1
	s_cmp_gt_i32 s54, 16
	s_mov_b64 s[28:29], -1
	s_cbranch_scc1 .LBB0_373

; #define PG8_STAGE(bufoff, gbase, voff) do { _Pragma("unroll") for (int _i = 0; _i < 2; ++_i) \
;         __builtin_amdgcn_global_load_lds((const unsigned*)((const char*)(gbase) + (voff)[_i]), (PG8_LAS unsigned*)(lds + (bufoff) + ldsw + _i * 8192), 16, 0, 0); } while (0)
; #define PG8_LDA(dst, b, h) do { _Pragma("unroll") for (int m = 0; m < 4; ++m) _Pragma("unroll") for (int k = 0; k < 2; ++k) dst[m][k] = *(const PG8_LAS bf16x8*)(lds + PG8_SA(b, h) + aoff + m * 2048 + k * 1024); } while (0)
; #define PG8_LDB(dst, b, h) do { _Pragma("unroll") for (int n = 0; n < 2; ++n) _Pragma("unroll") for (int k = 0; k < 2; ++k) dst[n][k] = *(const PG8_LAS bf16x8*)(lds + PG8_SB(b, h) + boff + n * 2048 + k * 1024); } while (0)
; #define PG8_WAIT_V(n) asm volatile("s_waitcnt vmcnt(" #n ")" ::: "memory")
; #define PG8_WAIT_L(n) asm volatile("s_waitcnt lgkmcnt(" #n ")" ::: "memory")
; #define PG8_BAR __builtin_amdgcn_s_barrier()
; #define PG8_SCHED __builtin_amdgcn_sched_barrier(0)
; template <class Epi, class Sched, bool ALIGN_EPI = false, bool SP2 = false>
; __device__ __forceinline__ void gemm_phase(PG8_LAS unsigned char* lds, const Gemm g, const Sched& S, const Epi& E) {
;     ...
;         const bool has_next = S.next(ui + 1, nxt);
;         const char* nA = has_next ? (const char*)g.A + (size_t)nxt.pm * tstep : cA; const char* nB = has_next ? (const char*)g.Bt + (size_t)nxt.pn * tstep : cB;
;         for (int t = 0; t < nt; t += 2) {
;             const bool last = (t == nt - 2);
;             const char* a1 = cA + (size_t)(t + 1) * kstep;
;             const char* a2 = last ? nA : cA + (size_t)(t + 2) * kstep; const char* b2 = last ? nB : cB + (size_t)(t + 2) * kstep;
;             const char* a3 = a2 + kstep; const char* b3 = b2 + kstep;
;             if (last && has_next) S.a_ready(nxt);
;             if constexpr (SP2) {
;             PG8_LDB(B0, 0, 0); PG8_LDB(B1, 0, 1); PG8_SCHED; PG8_LDA(At, 0, 0); PG8_STAGE(PG8_SA(1, 1), a1 + hstep, voffA);
;             PG8_WAIT_V(8); PG8_WAIT_L(0); PG8_BAR; PG8_MMA(0, 0, At, B0); PG8_MMA(0, 1, At, B1); PG8_BAR; PG8_SCHED;
;             PG8_LDA(At, 0, 1); PG8_STAGE(PG8_SB(0, 0), b2, voffB); PG8_STAGE(PG8_SB(0, 1), b2 + hstep, voffB); PG8_STAGE(PG8_SA(0, 0), a2, voffA);
;             PG8_WAIT_V(8); PG8_WAIT_L(0); PG8_BAR; PG8_MMA(1, 0, At, B0); PG8_MMA(1, 1, At, B1); PG8_BAR; PG8_SCHED;
.LBB0_746:
	s_ashr_i32 s21, s20, 31
	s_lshl_b64 s[22:23], s[20:21], 20
	v_readlane_b32 s24, v247, 17
	v_readlane_b32 s25, v247, 18
	s_add_u32 s22, s24, s22
	s_addc_u32 s23, s25, s23
	s_and_b64 s[24:25], s[2:3], exec
	s_cselect_b32 s21, s23, s29
	s_cselect_b32 s58, s22, s28
	s_ashr_i32 s19, s18, 31
	s_lshl_b64 s[24:25], s[18:19], 20
	s_add_u32 s24, s36, s24
	s_addc_u32 s25, s37, s25
	s_and_b64 s[34:35], s[2:3], exec
	s_cselect_b32 s19, s25, s31
	s_cselect_b32 s59, s24, s30
	s_add_u32 s28, s28, 0x80080
	s_addc_u32 s29, s29, 0
	s_add_u32 s60, s30, 0x100
	s_addc_u32 s61, s31, 0
	s_mov_b32 s62, -2
	v_add_u32_e32 v248, 0x18000, v216
	v_add_u32_e32 v249, 0x1c000, v216
	ds_read_b128 v[130:133], v218
	ds_read_b128 v[134:137], v218 offset:1024
	ds_read_b128 v[138:141], v218 offset:2048
	ds_read_b128 v[142:145], v218 offset:3072
	ds_read_b128 v[146:149], v219
	ds_read_b128 v[150:153], v219 offset:1024
	ds_read_b128 v[154:157], v219 offset:2048
	ds_read_b128 v[158:161], v219 offset:3072
	s_add_u32 s30, s28, 0xfff80080
	s_addc_u32 s31, s29, -1
	s_cmp_eq_u32 s62, 28
	s_cselect_b32 s35, s21, s31
	s_cselect_b32 s34, s58, s30
	s_cselect_b32 s31, s19, s61
	s_cselect_b32 s30, s59, s60
	s_add_i32 m0, s27, 0xc000
	ds_read_b128 v[162:165], v220
	ds_read_b128 v[166:169], v220 offset:1024
	ds_read_b128 v[170:173], v220 offset:2048
	ds_read_b128 v[174:177], v220 offset:3072
	ds_read_b128 v[178:181], v220 offset:4096
	ds_read_b128 v[182:185], v220 offset:5120
	ds_read_b128 v[206:209], v220 offset:6144
	ds_read_b128 v[222:225], v220 offset:7168
	global_load_lds_dwordx4 v198, s[28:29]
	s_add_i32 m0, s27, 0xe000
	s_nop 0
	global_load_lds_dwordx4 v200, s[28:29]
	s_waitcnt vmcnt(8)
	s_waitcnt lgkmcnt(0)
	s_barrier
	s_setprio 1
	s_waitcnt lgkmcnt(0)
	v_mfma_f32_16x16x32_bf16 v[126:129], v[130:133], v[162:165], 0
	v_mfma_f32_16x16x32_bf16 v[122:125], v[138:141], v[162:165], 0
	v_mfma_f32_16x16x32_bf16 v[110:113], v[138:141], v[170:173], 0
	v_mfma_f32_16x16x32_bf16 v[118:121], v[130:133], v[170:173], 0
	v_mfma_f32_16x16x32_bf16 v[94:97], v[130:133], v[178:181], 0
	v_mfma_f32_16x16x32_bf16 v[90:93], v[138:141], v[178:181], 0
	v_mfma_f32_16x16x32_bf16 v[74:77], v[138:141], v[206:209], 0
	v_mfma_f32_16x16x32_bf16 v[82:85], v[130:133], v[206:209], 0
	v_mfma_f32_16x16x32_bf16 v[126:129], v[134:137], v[166:169], v[126:129]
	v_mfma_f32_16x16x32_bf16 v[122:125], v[142:145], v[166:169], v[122:125]
	v_mfma_f32_16x16x32_bf16 v[110:113], v[142:145], v[174:177], v[110:113]
	v_mfma_f32_16x16x32_bf16 v[118:121], v[134:137], v[174:177], v[118:121]
	v_mfma_f32_16x16x32_bf16 v[94:97], v[134:137], v[182:185], v[94:97]
	v_mfma_f32_16x16x32_bf16 v[90:93], v[142:145], v[182:185], v[90:93]
	v_mfma_f32_16x16x32_bf16 v[74:77], v[142:145], v[222:225], v[74:77]
	v_mfma_f32_16x16x32_bf16 v[82:85], v[134:137], v[222:225], v[82:85]
	s_setprio 0
	s_setprio 1
	v_mfma_f32_16x16x32_bf16 v[114:117], v[146:149], v[162:165], 0
	v_mfma_f32_16x16x32_bf16 v[106:109], v[154:157], v[162:165], 0
	v_mfma_f32_16x16x32_bf16 v[98:101], v[154:157], v[170:173], 0
	v_mfma_f32_16x16x32_bf16 v[102:105], v[146:149], v[170:173], 0
	v_mfma_f32_16x16x32_bf16 v[86:89], v[146:149], v[178:181], 0
	v_mfma_f32_16x16x32_bf16 v[78:81], v[154:157], v[178:181], 0
	v_mfma_f32_16x16x32_bf16 v[66:69], v[154:157], v[206:209], 0
	v_mfma_f32_16x16x32_bf16 v[70:73], v[146:149], v[206:209], 0
	v_mfma_f32_16x16x32_bf16 v[114:117], v[150:153], v[166:169], v[114:117]
	v_mfma_f32_16x16x32_bf16 v[106:109], v[158:161], v[166:169], v[106:109]
	v_mfma_f32_16x16x32_bf16 v[98:101], v[158:161], v[174:177], v[98:101]
	v_mfma_f32_16x16x32_bf16 v[102:105], v[150:153], v[174:177], v[102:105]
	v_mfma_f32_16x16x32_bf16 v[86:89], v[150:153], v[182:185], v[86:89]
	v_mfma_f32_16x16x32_bf16 v[78:81], v[158:161], v[182:185], v[78:81]
	v_mfma_f32_16x16x32_bf16 v[66:69], v[158:161], v[222:225], v[66:69]
	v_mfma_f32_16x16x32_bf16 v[70:73], v[150:153], v[222:225], v[70:73]
	s_setprio 0
	s_barrier
	s_add_i32 s63, s48, s38
	s_mov_b32 m0, s63
	ds_read_b128 v[162:165], v220 offset:16384
	ds_read_b128 v[166:169], v220 offset:17408
	ds_read_b128 v[170:173], v220 offset:18432
	ds_read_b128 v[174:177], v220 offset:19456
	ds_read_b128 v[178:181], v220 offset:20480
	ds_read_b128 v[182:185], v220 offset:21504
	ds_read_b128 v[206:209], v220 offset:22528
	ds_read_b128 v[222:225], v220 offset:23552
	global_load_lds_dwordx4 v192, s[30:31]
	s_add_i32 m0, s63, 0x2000
	s_add_u32 s64, s30, 0x80000
	s_addc_u32 s65, s31, 0
	s_add_i32 s63, s49, s38
	global_load_lds_dwordx4 v196, s[30:31]
	s_mov_b32 m0, s63
	s_nop 0
	global_load_lds_dwordx4 v192, s[64:65]
	s_add_i32 m0, s63, 0x2000
	s_nop 0
	global_load_lds_dwordx4 v196, s[64:65]
	s_mov_b32 m0, s27
	s_nop 0
	global_load_lds_dwordx4 v190, s[34:35]
	s_mov_b32 m0, s39
	s_nop 0
	global_load_lds_dwordx4 v194, s[34:35]
	s_waitcnt vmcnt(8)
	s_waitcnt lgkmcnt(0)
	s_barrier
; #define PG8_STAGE(bufoff, gbase, voff) do { _Pragma("unroll") for (int _i = 0; _i < 2; ++_i) \
;         __builtin_amdgcn_global_load_lds((const unsigned*)((const char*)(gbase) + (voff)[_i]), (PG8_LAS unsigned*)(lds + (bufoff) + ldsw + _i * 8192), 16, 0, 0); } while (0)
; #define PG8_LDA(dst, b, h) do { _Pragma("unroll") for (int m = 0; m < 4; ++m) _Pragma("unroll") for (int k = 0; k < 2; ++k) dst[m][k] = *(const PG8_LAS bf16x8*)(lds + PG8_SA(b, h) + aoff + m * 2048 + k * 1024); } while (0)
; #define PG8_LDB(dst, b, h) do { _Pragma("unroll") for (int n = 0; n < 2; ++n) _Pragma("unroll") for (int k = 0; k < 2; ++k) dst[n][k] = *(const PG8_LAS bf16x8*)(lds + PG8_SB(b, h) + boff + n * 2048 + k * 1024); } while (0)
; #define PG8_WAIT_V(n) asm volatile("s_waitcnt vmcnt(" #n ")" ::: "memory")
; #define PG8_WAIT_L(n) asm volatile("s_waitcnt lgkmcnt(" #n ")" ::: "memory")
; #define PG8_BAR __builtin_amdgcn_s_barrier()
; #define PG8_SCHED __builtin_amdgcn_sched_barrier(0)
; template <class Epi, class Sched, bool ALIGN_EPI = false, bool SP2 = false>
; __device__ __forceinline__ void gemm_phase(PG8_LAS unsigned char* lds, const Gemm g, const Sched& S, const Epi& E) {
;     ...
;             PG8_WAIT_V(8); PG8_WAIT_L(0); PG8_BAR; PG8_MMA(1, 0, At, B0); PG8_MMA(1, 1, At, B1); PG8_BAR; PG8_SCHED;
;             PG8_LDB(B0, 1, 0); PG8_LDB(B1, 1, 1); PG8_SCHED; PG8_LDA(At, 1, 0); PG8_STAGE(PG8_SA(0, 1), a2 + hstep, voffA);
;             PG8_WAIT_V(8); PG8_WAIT_L(0); PG8_BAR; PG8_MMA(0, 0, At, B0); PG8_MMA(0, 1, At, B1); PG8_BAR; PG8_SCHED;
	s_setprio 1
	s_waitcnt lgkmcnt(0)
	v_mfma_f32_16x16x32_bf16 v[62:65], v[130:133], v[162:165], 0
	v_mfma_f32_16x16x32_bf16 v[58:61], v[138:141], v[162:165], 0
	v_mfma_f32_16x16x32_bf16 v[42:45], v[138:141], v[170:173], 0
	v_mfma_f32_16x16x32_bf16 v[50:53], v[130:133], v[170:173], 0
	v_mfma_f32_16x16x32_bf16 v[34:37], v[130:133], v[178:181], 0
	v_mfma_f32_16x16x32_bf16 v[26:29], v[138:141], v[178:181], 0
	v_mfma_f32_16x16x32_bf16 v[10:13], v[138:141], v[206:209], 0
	v_mfma_f32_16x16x32_bf16 v[18:21], v[130:133], v[206:209], 0
	v_mfma_f32_16x16x32_bf16 v[62:65], v[134:137], v[166:169], v[62:65]
	v_mfma_f32_16x16x32_bf16 v[58:61], v[142:145], v[166:169], v[58:61]
	v_mfma_f32_16x16x32_bf16 v[42:45], v[142:145], v[174:177], v[42:45]
	v_mfma_f32_16x16x32_bf16 v[50:53], v[134:137], v[174:177], v[50:53]
	v_mfma_f32_16x16x32_bf16 v[34:37], v[134:137], v[182:185], v[34:37]
	v_mfma_f32_16x16x32_bf16 v[26:29], v[142:145], v[182:185], v[26:29]
	v_mfma_f32_16x16x32_bf16 v[10:13], v[142:145], v[222:225], v[10:13]
	v_mfma_f32_16x16x32_bf16 v[18:21], v[134:137], v[222:225], v[18:21]
	s_setprio 0
	s_setprio 1
	v_mfma_f32_16x16x32_bf16 v[54:57], v[146:149], v[162:165], 0
	v_mfma_f32_16x16x32_bf16 v[46:49], v[154:157], v[162:165], 0
	v_mfma_f32_16x16x32_bf16 v[30:33], v[154:157], v[170:173], 0
	v_mfma_f32_16x16x32_bf16 v[38:41], v[146:149], v[170:173], 0
	v_mfma_f32_16x16x32_bf16 v[22:25], v[146:149], v[178:181], 0
	v_mfma_f32_16x16x32_bf16 v[14:17], v[154:157], v[178:181], 0
	v_mfma_f32_16x16x32_bf16 v[2:5], v[154:157], v[206:209], 0
	v_mfma_f32_16x16x32_bf16 v[6:9], v[146:149], v[206:209], 0
	v_mfma_f32_16x16x32_bf16 v[54:57], v[150:153], v[166:169], v[54:57]
	v_mfma_f32_16x16x32_bf16 v[46:49], v[158:161], v[166:169], v[46:49]
	v_mfma_f32_16x16x32_bf16 v[30:33], v[158:161], v[174:177], v[30:33]
	v_mfma_f32_16x16x32_bf16 v[38:41], v[150:153], v[174:177], v[38:41]
	v_mfma_f32_16x16x32_bf16 v[22:25], v[150:153], v[182:185], v[22:25]
	v_mfma_f32_16x16x32_bf16 v[14:17], v[158:161], v[182:185], v[14:17]
	v_mfma_f32_16x16x32_bf16 v[2:5], v[158:161], v[222:225], v[2:5]
	v_mfma_f32_16x16x32_bf16 v[6:9], v[150:153], v[222:225], v[6:9]
	s_setprio 0
	s_barrier
	s_add_i32 s63, 0, 0x18000
	s_add_i32 s64, 0, 0x1c000
	ds_read_b128 v[130:133], v248
	ds_read_b128 v[134:137], v248 offset:1024
	ds_read_b128 v[138:141], v248 offset:2048
	ds_read_b128 v[142:145], v248 offset:3072
	ds_read_b128 v[146:149], v249
	ds_read_b128 v[150:153], v249 offset:1024
	ds_read_b128 v[154:157], v249 offset:2048
	ds_read_b128 v[158:161], v249 offset:3072
	s_add_u32 s34, s34, 0x80000
	s_addc_u32 s35, s35, 0
	s_mov_b32 m0, s40
	ds_read_b128 v[162:165], v220 offset:32768
	ds_read_b128 v[166:169], v220 offset:33792
	ds_read_b128 v[170:173], v220 offset:34816
	ds_read_b128 v[174:177], v220 offset:35840
	ds_read_b128 v[178:181], v220 offset:36864
	ds_read_b128 v[182:185], v220 offset:37888
	ds_read_b128 v[206:209], v220 offset:38912
	ds_read_b128 v[222:225], v220 offset:39936
	global_load_lds_dwordx4 v190, s[34:35]
	s_mov_b32 m0, s41
	s_nop 0
	global_load_lds_dwordx4 v194, s[34:35]
	s_waitcnt vmcnt(8)
	s_waitcnt lgkmcnt(0)
	s_barrier
	s_setprio 1
	s_waitcnt lgkmcnt(0)
	v_mfma_f32_16x16x32_bf16 v[126:129], v[130:133], v[162:165], v[126:129]
	v_mfma_f32_16x16x32_bf16 v[122:125], v[138:141], v[162:165], v[122:125]
	v_mfma_f32_16x16x32_bf16 v[110:113], v[138:141], v[170:173], v[110:113]
	v_mfma_f32_16x16x32_bf16 v[118:121], v[130:133], v[170:173], v[118:121]
	v_mfma_f32_16x16x32_bf16 v[94:97], v[130:133], v[178:181], v[94:97]
	v_mfma_f32_16x16x32_bf16 v[90:93], v[138:141], v[178:181], v[90:93]
	v_mfma_f32_16x16x32_bf16 v[74:77], v[138:141], v[206:209], v[74:77]
	v_mfma_f32_16x16x32_bf16 v[82:85], v[130:133], v[206:209], v[82:85]
	v_mfma_f32_16x16x32_bf16 v[126:129], v[134:137], v[166:169], v[126:129]
	v_mfma_f32_16x16x32_bf16 v[122:125], v[142:145], v[166:169], v[122:125]
	v_mfma_f32_16x16x32_bf16 v[110:113], v[142:145], v[174:177], v[110:113]
	v_mfma_f32_16x16x32_bf16 v[118:121], v[134:137], v[174:177], v[118:121]
	v_mfma_f32_16x16x32_bf16 v[94:97], v[134:137], v[182:185], v[94:97]
	v_mfma_f32_16x16x32_bf16 v[90:93], v[142:145], v[182:185], v[90:93]
	v_mfma_f32_16x16x32_bf16 v[74:77], v[142:145], v[222:225], v[74:77]
	v_mfma_f32_16x16x32_bf16 v[82:85], v[134:137], v[222:225], v[82:85]
	s_setprio 0
	s_setprio 1
	v_mfma_f32_16x16x32_bf16 v[114:117], v[146:149], v[162:165], v[114:117]
	v_mfma_f32_16x16x32_bf16 v[106:109], v[154:157], v[162:165], v[106:109]
	v_mfma_f32_16x16x32_bf16 v[98:101], v[154:157], v[170:173], v[98:101]
	v_mfma_f32_16x16x32_bf16 v[102:105], v[146:149], v[170:173], v[102:105]
	v_mfma_f32_16x16x32_bf16 v[86:89], v[146:149], v[178:181], v[86:89]
	v_mfma_f32_16x16x32_bf16 v[78:81], v[154:157], v[178:181], v[78:81]
	v_mfma_f32_16x16x32_bf16 v[66:69], v[154:157], v[206:209], v[66:69]
	v_mfma_f32_16x16x32_bf16 v[70:73], v[146:149], v[206:209], v[70:73]
	v_mfma_f32_16x16x32_bf16 v[114:117], v[150:153], v[166:169], v[114:117]
	v_mfma_f32_16x16x32_bf16 v[106:109], v[158:161], v[166:169], v[106:109]
	v_mfma_f32_16x16x32_bf16 v[98:101], v[158:161], v[174:177], v[98:101]
	v_mfma_f32_16x16x32_bf16 v[102:105], v[150:153], v[174:177], v[102:105]
	v_mfma_f32_16x16x32_bf16 v[86:89], v[150:153], v[182:185], v[86:89]
	v_mfma_f32_16x16x32_bf16 v[78:81], v[158:161], v[182:185], v[78:81]
	v_mfma_f32_16x16x32_bf16 v[66:69], v[158:161], v[222:225], v[66:69]
	v_mfma_f32_16x16x32_bf16 v[70:73], v[150:153], v[222:225], v[70:73]
	s_setprio 0
	s_barrier
; #define PG8_STAGE(bufoff, gbase, voff) do { _Pragma("unroll") for (int _i = 0; _i < 2; ++_i) \
;         __builtin_amdgcn_global_load_lds((const unsigned*)((const char*)(gbase) + (voff)[_i]), (PG8_LAS unsigned*)(lds + (bufoff) + ldsw + _i * 8192), 16, 0, 0); } while (0)
; #define PG8_LDA(dst, b, h) do { _Pragma("unroll") for (int m = 0; m < 4; ++m) _Pragma("unroll") for (int k = 0; k < 2; ++k) dst[m][k] = *(const PG8_LAS bf16x8*)(lds + PG8_SA(b, h) + aoff + m * 2048 + k * 1024); } while (0)
; #define PG8_LDB(dst, b, h) do { _Pragma("unroll") for (int n = 0; n < 2; ++n) _Pragma("unroll") for (int k = 0; k < 2; ++k) dst[n][k] = *(const PG8_LAS bf16x8*)(lds + PG8_SB(b, h) + boff + n * 2048 + k * 1024); } while (0)
; #define PG8_WAIT_V(n) asm volatile("s_waitcnt vmcnt(" #n ")" ::: "memory")
; #define PG8_WAIT_L(n) asm volatile("s_waitcnt lgkmcnt(" #n ")" ::: "memory")
; #define PG8_BAR __builtin_amdgcn_s_barrier()
; #define PG8_SCHED __builtin_amdgcn_sched_barrier(0)
; template <class Epi, class Sched, bool ALIGN_EPI = false, bool SP2 = false>
; __device__ __forceinline__ void gemm_phase(PG8_LAS unsigned char* lds, const Gemm g, const Sched& S, const Epi& E) {
;     ...
;             PG8_LDB(B0, 0, 0); PG8_LDB(B1, 0, 1); PG8_SCHED; PG8_LDA(At, 0, 0); PG8_STAGE(PG8_SA(1, 1), a1 + hstep, voffA);
;             PG8_WAIT_V(8); PG8_WAIT_L(0); PG8_BAR; PG8_MMA(0, 0, At, B0); PG8_MMA(0, 1, At, B1); PG8_BAR; PG8_SCHED;
;             PG8_LDA(At, 0, 1); PG8_STAGE(PG8_SB(0, 0), b2, voffB); PG8_STAGE(PG8_SB(0, 1), b2 + hstep, voffB); PG8_STAGE(PG8_SA(0, 0), a2, voffA);
;             PG8_WAIT_V(8); PG8_WAIT_L(0); PG8_BAR; PG8_MMA(1, 0, At, B0); PG8_MMA(1, 1, At, B1); PG8_BAR; PG8_SCHED;
;             PG8_LDB(B0, 1, 0); PG8_LDB(B1, 1, 1); PG8_SCHED; PG8_LDA(At, 1, 0); PG8_STAGE(PG8_SA(0, 1), a2 + hstep, voffA);
;             PG8_WAIT_V(8); PG8_WAIT_L(0); PG8_BAR; PG8_MMA(0, 0, At, B0); PG8_MMA(0, 1, At, B1); PG8_BAR; PG8_SCHED;
;             PG8_LDA(At, 1, 1); PG8_STAGE(PG8_SB(1, 0), b3, voffB); PG8_STAGE(PG8_SB(1, 1), b3 + hstep, voffB); PG8_STAGE(PG8_SA(1, 0), a3, voffA);
;             PG8_WAIT_V(8); PG8_WAIT_L(0); PG8_BAR; PG8_MMA(1, 0, At, B0); PG8_MMA(1, 1, At, B1); PG8_BAR; PG8_SCHED;
	s_add_u32 s98, s30, 0x80
	s_addc_u32 s99, s31, 0
	s_add_u32 s100, s34, 0xfff80080
	s_addc_u32 s101, s35, -1
	s_add_i32 s34, s63, s38
	s_mov_b32 m0, s34
	ds_read_b128 v[162:165], v220 offset:49152
	ds_read_b128 v[166:169], v220 offset:50176
	ds_read_b128 v[170:173], v220 offset:51200
	ds_read_b128 v[174:177], v220 offset:52224
	ds_read_b128 v[178:181], v220 offset:53248
	ds_read_b128 v[182:185], v220 offset:54272
	ds_read_b128 v[206:209], v220 offset:55296
	ds_read_b128 v[222:225], v220 offset:56320
	global_load_lds_dwordx4 v192, s[98:99]
	s_add_i32 m0, s34, 0x2000
	s_add_u32 s30, s30, 0x80080
	s_addc_u32 s31, s31, 0
	s_add_i32 s34, s64, s38
	global_load_lds_dwordx4 v196, s[98:99]
	s_mov_b32 m0, s34
	s_nop 0
	global_load_lds_dwordx4 v192, s[30:31]
	s_add_i32 m0, s34, 0x2000
	s_nop 0
	global_load_lds_dwordx4 v196, s[30:31]
	s_mov_b32 m0, s45
	s_nop 0
	global_load_lds_dwordx4 v190, s[100:101]
	s_mov_b32 m0, s46
	s_nop 0
	global_load_lds_dwordx4 v194, s[100:101]
	s_waitcnt vmcnt(8)
	s_waitcnt lgkmcnt(0)
	s_barrier
	s_setprio 1
	s_waitcnt lgkmcnt(0)
	v_mfma_f32_16x16x32_bf16 v[62:65], v[130:133], v[162:165], v[62:65]
	v_mfma_f32_16x16x32_bf16 v[58:61], v[138:141], v[162:165], v[58:61]
	v_mfma_f32_16x16x32_bf16 v[42:45], v[138:141], v[170:173], v[42:45]
	v_mfma_f32_16x16x32_bf16 v[50:53], v[130:133], v[170:173], v[50:53]
	v_mfma_f32_16x16x32_bf16 v[34:37], v[130:133], v[178:181], v[34:37]
	v_mfma_f32_16x16x32_bf16 v[26:29], v[138:141], v[178:181], v[26:29]
	v_mfma_f32_16x16x32_bf16 v[10:13], v[138:141], v[206:209], v[10:13]
	v_mfma_f32_16x16x32_bf16 v[18:21], v[130:133], v[206:209], v[18:21]
	v_mfma_f32_16x16x32_bf16 v[62:65], v[134:137], v[166:169], v[62:65]
	v_mfma_f32_16x16x32_bf16 v[58:61], v[142:145], v[166:169], v[58:61]
	v_mfma_f32_16x16x32_bf16 v[42:45], v[142:145], v[174:177], v[42:45]
	v_mfma_f32_16x16x32_bf16 v[50:53], v[134:137], v[174:177], v[50:53]
	v_mfma_f32_16x16x32_bf16 v[34:37], v[134:137], v[182:185], v[34:37]
	v_mfma_f32_16x16x32_bf16 v[26:29], v[142:145], v[182:185], v[26:29]
	v_mfma_f32_16x16x32_bf16 v[10:13], v[142:145], v[222:225], v[10:13]
	v_mfma_f32_16x16x32_bf16 v[18:21], v[134:137], v[222:225], v[18:21]
	s_setprio 0
	s_setprio 1
	v_mfma_f32_16x16x32_bf16 v[54:57], v[146:149], v[162:165], v[54:57]
	v_mfma_f32_16x16x32_bf16 v[46:49], v[154:157], v[162:165], v[46:49]
	v_mfma_f32_16x16x32_bf16 v[30:33], v[154:157], v[170:173], v[30:33]
	v_mfma_f32_16x16x32_bf16 v[38:41], v[146:149], v[170:173], v[38:41]
	v_mfma_f32_16x16x32_bf16 v[22:25], v[146:149], v[178:181], v[22:25]
	v_mfma_f32_16x16x32_bf16 v[14:17], v[154:157], v[178:181], v[14:17]
	v_mfma_f32_16x16x32_bf16 v[2:5], v[154:157], v[206:209], v[2:5]
	v_mfma_f32_16x16x32_bf16 v[6:9], v[146:149], v[206:209], v[6:9]
	v_mfma_f32_16x16x32_bf16 v[54:57], v[150:153], v[166:169], v[54:57]
	v_mfma_f32_16x16x32_bf16 v[46:49], v[158:161], v[166:169], v[46:49]
	v_mfma_f32_16x16x32_bf16 v[30:33], v[158:161], v[174:177], v[30:33]
	v_mfma_f32_16x16x32_bf16 v[38:41], v[150:153], v[174:177], v[38:41]
	v_mfma_f32_16x16x32_bf16 v[22:25], v[150:153], v[182:185], v[22:25]
	v_mfma_f32_16x16x32_bf16 v[14:17], v[158:161], v[182:185], v[14:17]
	v_mfma_f32_16x16x32_bf16 v[2:5], v[158:161], v[222:225], v[2:5]
	v_mfma_f32_16x16x32_bf16 v[6:9], v[150:153], v[222:225], v[6:9]
	s_setprio 0
	s_barrier
	s_add_i32 s62, s62, 2
	s_add_u32 s28, s28, 0x100
	s_addc_u32 s29, s29, 0
	s_add_u32 s60, s60, 0x100
	s_addc_u32 s61, s61, 0
	s_cmp_gt_u32 s62, 29
.LBB0_747:
	ds_read_b128 v[130:133], v218
	ds_read_b128 v[134:137], v218 offset:1024
	ds_read_b128 v[138:141], v218 offset:2048
	ds_read_b128 v[142:145], v218 offset:3072
	ds_read_b128 v[146:149], v219
	ds_read_b128 v[150:153], v219 offset:1024
	ds_read_b128 v[154:157], v219 offset:2048
	ds_read_b128 v[158:161], v219 offset:3072
	s_add_u32 s30, s28, 0xfff80080
	s_addc_u32 s31, s29, -1
	s_cmp_eq_u32 s62, 28
	s_cselect_b32 s35, s21, s31
	s_cselect_b32 s34, s58, s30
	s_cselect_b32 s31, s19, s61
	s_cselect_b32 s30, s59, s60
	s_add_i32 m0, s27, 0xc000
	ds_read_b128 v[162:165], v220
	ds_read_b128 v[166:169], v220 offset:1024
	ds_read_b128 v[170:173], v220 offset:2048
	ds_read_b128 v[174:177], v220 offset:3072
	ds_read_b128 v[178:181], v220 offset:4096
	ds_read_b128 v[182:185], v220 offset:5120
	ds_read_b128 v[206:209], v220 offset:6144
	ds_read_b128 v[222:225], v220 offset:7168
	global_load_lds_dwordx4 v198, s[28:29]
	s_add_i32 m0, s27, 0xe000
	s_nop 0
	global_load_lds_dwordx4 v200, s[28:29]
	s_waitcnt vmcnt(8)
	s_waitcnt lgkmcnt(0)
	s_barrier
; #define PG8_STAGE(bufoff, gbase, voff) do { _Pragma("unroll") for (int _i = 0; _i < 2; ++_i) \
;         __builtin_amdgcn_global_load_lds((const unsigned*)((const char*)(gbase) + (voff)[_i]), (PG8_LAS unsigned*)(lds + (bufoff) + ldsw + _i * 8192), 16, 0, 0); } while (0)
; #define PG8_LDA(dst, b, h) do { _Pragma("unroll") for (int m = 0; m < 4; ++m) _Pragma("unroll") for (int k = 0; k < 2; ++k) dst[m][k] = *(const PG8_LAS bf16x8*)(lds + PG8_SA(b, h) + aoff + m * 2048 + k * 1024); } while (0)
; #define PG8_LDB(dst, b, h) do { _Pragma("unroll") for (int n = 0; n < 2; ++n) _Pragma("unroll") for (int k = 0; k < 2; ++k) dst[n][k] = *(const PG8_LAS bf16x8*)(lds + PG8_SB(b, h) + boff + n * 2048 + k * 1024); } while (0)
; #define PG8_WAIT_V(n) asm volatile("s_waitcnt vmcnt(" #n ")" ::: "memory")
; #define PG8_WAIT_L(n) asm volatile("s_waitcnt lgkmcnt(" #n ")" ::: "memory")
; #define PG8_BAR __builtin_amdgcn_s_barrier()
; #define PG8_SCHED __builtin_amdgcn_sched_barrier(0)
; template <class Epi, class Sched, bool ALIGN_EPI = false, bool SP2 = false>
; __device__ __forceinline__ void gemm_phase(PG8_LAS unsigned char* lds, const Gemm g, const Sched& S, const Epi& E) {
;     ...
;             PG8_LDB(B0, 0, 0); PG8_LDB(B1, 0, 1); PG8_SCHED; PG8_LDA(At, 0, 0); PG8_STAGE(PG8_SA(1, 1), a1 + hstep, voffA);
;             PG8_WAIT_V(8); PG8_WAIT_L(0); PG8_BAR; PG8_MMA(0, 0, At, B0); PG8_MMA(0, 1, At, B1); PG8_BAR; PG8_SCHED;
;             PG8_LDA(At, 0, 1); PG8_STAGE(PG8_SB(0, 0), b2, voffB); PG8_STAGE(PG8_SB(0, 1), b2 + hstep, voffB); PG8_STAGE(PG8_SA(0, 0), a2, voffA);
;             PG8_WAIT_V(8); PG8_WAIT_L(0); PG8_BAR; PG8_MMA(1, 0, At, B0); PG8_MMA(1, 1, At, B1); PG8_BAR; PG8_SCHED;
;             PG8_LDB(B0, 1, 0); PG8_LDB(B1, 1, 1); PG8_SCHED; PG8_LDA(At, 1, 0); PG8_STAGE(PG8_SA(0, 1), a2 + hstep, voffA);
;             PG8_WAIT_V(8); PG8_WAIT_L(0); PG8_BAR; PG8_MMA(0, 0, At, B0); PG8_MMA(0, 1, At, B1); PG8_BAR; PG8_SCHED;
	s_setprio 1
	s_waitcnt lgkmcnt(0)
	v_mfma_f32_16x16x32_bf16 v[126:129], v[130:133], v[162:165], v[126:129]
	v_mfma_f32_16x16x32_bf16 v[122:125], v[138:141], v[162:165], v[122:125]
	v_mfma_f32_16x16x32_bf16 v[110:113], v[138:141], v[170:173], v[110:113]
	v_mfma_f32_16x16x32_bf16 v[118:121], v[130:133], v[170:173], v[118:121]
	v_mfma_f32_16x16x32_bf16 v[94:97], v[130:133], v[178:181], v[94:97]
	v_mfma_f32_16x16x32_bf16 v[90:93], v[138:141], v[178:181], v[90:93]
	v_mfma_f32_16x16x32_bf16 v[74:77], v[138:141], v[206:209], v[74:77]
	v_mfma_f32_16x16x32_bf16 v[82:85], v[130:133], v[206:209], v[82:85]
	v_mfma_f32_16x16x32_bf16 v[126:129], v[134:137], v[166:169], v[126:129]
	v_mfma_f32_16x16x32_bf16 v[122:125], v[142:145], v[166:169], v[122:125]
	v_mfma_f32_16x16x32_bf16 v[110:113], v[142:145], v[174:177], v[110:113]
	v_mfma_f32_16x16x32_bf16 v[118:121], v[134:137], v[174:177], v[118:121]
	v_mfma_f32_16x16x32_bf16 v[94:97], v[134:137], v[182:185], v[94:97]
	v_mfma_f32_16x16x32_bf16 v[90:93], v[142:145], v[182:185], v[90:93]
	v_mfma_f32_16x16x32_bf16 v[74:77], v[142:145], v[222:225], v[74:77]
	v_mfma_f32_16x16x32_bf16 v[82:85], v[134:137], v[222:225], v[82:85]
	s_setprio 0
	s_setprio 1
	v_mfma_f32_16x16x32_bf16 v[114:117], v[146:149], v[162:165], v[114:117]
	v_mfma_f32_16x16x32_bf16 v[106:109], v[154:157], v[162:165], v[106:109]
	v_mfma_f32_16x16x32_bf16 v[98:101], v[154:157], v[170:173], v[98:101]
	v_mfma_f32_16x16x32_bf16 v[102:105], v[146:149], v[170:173], v[102:105]
	v_mfma_f32_16x16x32_bf16 v[86:89], v[146:149], v[178:181], v[86:89]
	v_mfma_f32_16x16x32_bf16 v[78:81], v[154:157], v[178:181], v[78:81]
	v_mfma_f32_16x16x32_bf16 v[66:69], v[154:157], v[206:209], v[66:69]
	v_mfma_f32_16x16x32_bf16 v[70:73], v[146:149], v[206:209], v[70:73]
	v_mfma_f32_16x16x32_bf16 v[114:117], v[150:153], v[166:169], v[114:117]
	v_mfma_f32_16x16x32_bf16 v[106:109], v[158:161], v[166:169], v[106:109]
	v_mfma_f32_16x16x32_bf16 v[98:101], v[158:161], v[174:177], v[98:101]
	v_mfma_f32_16x16x32_bf16 v[102:105], v[150:153], v[174:177], v[102:105]
	v_mfma_f32_16x16x32_bf16 v[86:89], v[150:153], v[182:185], v[86:89]
	v_mfma_f32_16x16x32_bf16 v[78:81], v[158:161], v[182:185], v[78:81]
	v_mfma_f32_16x16x32_bf16 v[66:69], v[158:161], v[222:225], v[66:69]
	v_mfma_f32_16x16x32_bf16 v[70:73], v[150:153], v[222:225], v[70:73]
	s_setprio 0
	s_barrier
	s_add_i32 s63, s48, s38
	s_mov_b32 m0, s63
	ds_read_b128 v[162:165], v220 offset:16384
	ds_read_b128 v[166:169], v220 offset:17408
	ds_read_b128 v[170:173], v220 offset:18432
	ds_read_b128 v[174:177], v220 offset:19456
	ds_read_b128 v[178:181], v220 offset:20480
	ds_read_b128 v[182:185], v220 offset:21504
	ds_read_b128 v[206:209], v220 offset:22528
	ds_read_b128 v[222:225], v220 offset:23552
	global_load_lds_dwordx4 v192, s[30:31]
	s_add_i32 m0, s63, 0x2000
	s_add_u32 s64, s30, 0x80000
	s_addc_u32 s65, s31, 0
	s_add_i32 s63, s49, s38
	global_load_lds_dwordx4 v196, s[30:31]
	s_mov_b32 m0, s63
	s_nop 0
	global_load_lds_dwordx4 v192, s[64:65]
	s_add_i32 m0, s63, 0x2000
	s_nop 0
	global_load_lds_dwordx4 v196, s[64:65]
	s_mov_b32 m0, s27
	s_nop 0
	global_load_lds_dwordx4 v190, s[34:35]
	s_mov_b32 m0, s39
	s_nop 0
	global_load_lds_dwordx4 v194, s[34:35]
	s_waitcnt vmcnt(8)
	s_waitcnt lgkmcnt(0)
	s_barrier
	s_setprio 1
	s_waitcnt lgkmcnt(0)
	v_mfma_f32_16x16x32_bf16 v[62:65], v[130:133], v[162:165], v[62:65]
	v_mfma_f32_16x16x32_bf16 v[58:61], v[138:141], v[162:165], v[58:61]
	v_mfma_f32_16x16x32_bf16 v[42:45], v[138:141], v[170:173], v[42:45]
	v_mfma_f32_16x16x32_bf16 v[50:53], v[130:133], v[170:173], v[50:53]
	v_mfma_f32_16x16x32_bf16 v[34:37], v[130:133], v[178:181], v[34:37]
	v_mfma_f32_16x16x32_bf16 v[26:29], v[138:141], v[178:181], v[26:29]
	v_mfma_f32_16x16x32_bf16 v[10:13], v[138:141], v[206:209], v[10:13]
	v_mfma_f32_16x16x32_bf16 v[18:21], v[130:133], v[206:209], v[18:21]
	v_mfma_f32_16x16x32_bf16 v[62:65], v[134:137], v[166:169], v[62:65]
	v_mfma_f32_16x16x32_bf16 v[58:61], v[142:145], v[166:169], v[58:61]
	v_mfma_f32_16x16x32_bf16 v[42:45], v[142:145], v[174:177], v[42:45]
	v_mfma_f32_16x16x32_bf16 v[50:53], v[134:137], v[174:177], v[50:53]
	v_mfma_f32_16x16x32_bf16 v[34:37], v[134:137], v[182:185], v[34:37]
	v_mfma_f32_16x16x32_bf16 v[26:29], v[142:145], v[182:185], v[26:29]
	v_mfma_f32_16x16x32_bf16 v[10:13], v[142:145], v[222:225], v[10:13]
	v_mfma_f32_16x16x32_bf16 v[18:21], v[134:137], v[222:225], v[18:21]
	s_setprio 0
	s_setprio 1
	v_mfma_f32_16x16x32_bf16 v[54:57], v[146:149], v[162:165], v[54:57]
	v_mfma_f32_16x16x32_bf16 v[46:49], v[154:157], v[162:165], v[46:49]
	v_mfma_f32_16x16x32_bf16 v[30:33], v[154:157], v[170:173], v[30:33]
	v_mfma_f32_16x16x32_bf16 v[38:41], v[146:149], v[170:173], v[38:41]
	v_mfma_f32_16x16x32_bf16 v[22:25], v[146:149], v[178:181], v[22:25]
	v_mfma_f32_16x16x32_bf16 v[14:17], v[154:157], v[178:181], v[14:17]
	v_mfma_f32_16x16x32_bf16 v[2:5], v[154:157], v[206:209], v[2:5]
	v_mfma_f32_16x16x32_bf16 v[6:9], v[146:149], v[206:209], v[6:9]
	v_mfma_f32_16x16x32_bf16 v[54:57], v[150:153], v[166:169], v[54:57]
	v_mfma_f32_16x16x32_bf16 v[46:49], v[158:161], v[166:169], v[46:49]
	v_mfma_f32_16x16x32_bf16 v[30:33], v[158:161], v[174:177], v[30:33]
	v_mfma_f32_16x16x32_bf16 v[38:41], v[150:153], v[174:177], v[38:41]
	v_mfma_f32_16x16x32_bf16 v[22:25], v[150:153], v[182:185], v[22:25]
	v_mfma_f32_16x16x32_bf16 v[14:17], v[158:161], v[182:185], v[14:17]
	v_mfma_f32_16x16x32_bf16 v[2:5], v[158:161], v[222:225], v[2:5]
	v_mfma_f32_16x16x32_bf16 v[6:9], v[150:153], v[222:225], v[6:9]
	s_setprio 0
	s_barrier
; #define PG8_STAGE(bufoff, gbase, voff) do { _Pragma("unroll") for (int _i = 0; _i < 2; ++_i) \
;         __builtin_amdgcn_global_load_lds((const unsigned*)((const char*)(gbase) + (voff)[_i]), (PG8_LAS unsigned*)(lds + (bufoff) + ldsw + _i * 8192), 16, 0, 0); } while (0)
; #define PG8_LDA(dst, b, h) do { _Pragma("unroll") for (int m = 0; m < 4; ++m) _Pragma("unroll") for (int k = 0; k < 2; ++k) dst[m][k] = *(const PG8_LAS bf16x8*)(lds + PG8_SA(b, h) + aoff + m * 2048 + k * 1024); } while (0)
; #define PG8_LDB(dst, b, h) do { _Pragma("unroll") for (int n = 0; n < 2; ++n) _Pragma("unroll") for (int k = 0; k < 2; ++k) dst[n][k] = *(const PG8_LAS bf16x8*)(lds + PG8_SB(b, h) + boff + n * 2048 + k * 1024); } while (0)
; #define PG8_WAIT_V(n) asm volatile("s_waitcnt vmcnt(" #n ")" ::: "memory")
; #define PG8_WAIT_L(n) asm volatile("s_waitcnt lgkmcnt(" #n ")" ::: "memory")
; #define PG8_BAR __builtin_amdgcn_s_barrier()
; #define PG8_SCHED __builtin_amdgcn_sched_barrier(0)
; template <class Epi, class Sched, bool ALIGN_EPI = false, bool SP2 = false>
; __device__ __forceinline__ void gemm_phase(PG8_LAS unsigned char* lds, const Gemm g, const Sched& S, const Epi& E) {
;     ...
;             PG8_LDB(B0, 1, 0); PG8_LDB(B1, 1, 1); PG8_SCHED; PG8_LDA(At, 1, 0); PG8_STAGE(PG8_SA(0, 1), a2 + hstep, voffA);
;             PG8_WAIT_V(8); PG8_WAIT_L(0); PG8_BAR; PG8_MMA(0, 0, At, B0); PG8_MMA(0, 1, At, B1); PG8_BAR; PG8_SCHED;
;             PG8_LDA(At, 1, 1); PG8_STAGE(PG8_SB(1, 0), b3, voffB); PG8_STAGE(PG8_SB(1, 1), b3 + hstep, voffB); PG8_STAGE(PG8_SA(1, 0), a3, voffA);
;             PG8_WAIT_V(8); PG8_WAIT_L(0); PG8_BAR; PG8_MMA(1, 0, At, B0); PG8_MMA(1, 1, At, B1); PG8_BAR; PG8_SCHED;
	s_add_i32 s63, 0, 0x18000
	s_add_i32 s64, 0, 0x1c000
	ds_read_b128 v[130:133], v248
	ds_read_b128 v[134:137], v248 offset:1024
	ds_read_b128 v[138:141], v248 offset:2048
	ds_read_b128 v[142:145], v248 offset:3072
	ds_read_b128 v[146:149], v249
	ds_read_b128 v[150:153], v249 offset:1024
	ds_read_b128 v[154:157], v249 offset:2048
	ds_read_b128 v[158:161], v249 offset:3072
	s_add_u32 s34, s34, 0x80000
	s_addc_u32 s35, s35, 0
	s_mov_b32 m0, s40
	ds_read_b128 v[162:165], v220 offset:32768
	ds_read_b128 v[166:169], v220 offset:33792
	ds_read_b128 v[170:173], v220 offset:34816
	ds_read_b128 v[174:177], v220 offset:35840
	ds_read_b128 v[178:181], v220 offset:36864
	ds_read_b128 v[182:185], v220 offset:37888
	ds_read_b128 v[206:209], v220 offset:38912
	ds_read_b128 v[222:225], v220 offset:39936
	global_load_lds_dwordx4 v190, s[34:35]
	s_mov_b32 m0, s41
	s_nop 0
	global_load_lds_dwordx4 v194, s[34:35]
	s_waitcnt vmcnt(8)
	s_waitcnt lgkmcnt(0)
	s_barrier
	s_setprio 1
	s_waitcnt lgkmcnt(0)
	v_mfma_f32_16x16x32_bf16 v[126:129], v[130:133], v[162:165], v[126:129]
	v_mfma_f32_16x16x32_bf16 v[122:125], v[138:141], v[162:165], v[122:125]
	v_mfma_f32_16x16x32_bf16 v[110:113], v[138:141], v[170:173], v[110:113]
	v_mfma_f32_16x16x32_bf16 v[118:121], v[130:133], v[170:173], v[118:121]
	v_mfma_f32_16x16x32_bf16 v[94:97], v[130:133], v[178:181], v[94:97]
	v_mfma_f32_16x16x32_bf16 v[90:93], v[138:141], v[178:181], v[90:93]
	v_mfma_f32_16x16x32_bf16 v[74:77], v[138:141], v[206:209], v[74:77]
	v_mfma_f32_16x16x32_bf16 v[82:85], v[130:133], v[206:209], v[82:85]
	v_mfma_f32_16x16x32_bf16 v[126:129], v[134:137], v[166:169], v[126:129]
	v_mfma_f32_16x16x32_bf16 v[122:125], v[142:145], v[166:169], v[122:125]
	v_mfma_f32_16x16x32_bf16 v[110:113], v[142:145], v[174:177], v[110:113]
	v_mfma_f32_16x16x32_bf16 v[118:121], v[134:137], v[174:177], v[118:121]
	v_mfma_f32_16x16x32_bf16 v[94:97], v[134:137], v[182:185], v[94:97]
	v_mfma_f32_16x16x32_bf16 v[90:93], v[142:145], v[182:185], v[90:93]
	v_mfma_f32_16x16x32_bf16 v[74:77], v[142:145], v[222:225], v[74:77]
	v_mfma_f32_16x16x32_bf16 v[82:85], v[134:137], v[222:225], v[82:85]
	s_setprio 0
	s_setprio 1
	v_mfma_f32_16x16x32_bf16 v[114:117], v[146:149], v[162:165], v[114:117]
	v_mfma_f32_16x16x32_bf16 v[106:109], v[154:157], v[162:165], v[106:109]
	v_mfma_f32_16x16x32_bf16 v[98:101], v[154:157], v[170:173], v[98:101]
	v_mfma_f32_16x16x32_bf16 v[102:105], v[146:149], v[170:173], v[102:105]
	v_mfma_f32_16x16x32_bf16 v[86:89], v[146:149], v[178:181], v[86:89]
	v_mfma_f32_16x16x32_bf16 v[78:81], v[154:157], v[178:181], v[78:81]
	v_mfma_f32_16x16x32_bf16 v[66:69], v[154:157], v[206:209], v[66:69]
	v_mfma_f32_16x16x32_bf16 v[70:73], v[146:149], v[206:209], v[70:73]
	v_mfma_f32_16x16x32_bf16 v[114:117], v[150:153], v[166:169], v[114:117]
	v_mfma_f32_16x16x32_bf16 v[106:109], v[158:161], v[166:169], v[106:109]
	v_mfma_f32_16x16x32_bf16 v[98:101], v[158:161], v[174:177], v[98:101]
	v_mfma_f32_16x16x32_bf16 v[102:105], v[150:153], v[174:177], v[102:105]
	v_mfma_f32_16x16x32_bf16 v[86:89], v[150:153], v[182:185], v[86:89]
	v_mfma_f32_16x16x32_bf16 v[78:81], v[158:161], v[182:185], v[78:81]
	v_mfma_f32_16x16x32_bf16 v[66:69], v[158:161], v[222:225], v[66:69]
	v_mfma_f32_16x16x32_bf16 v[70:73], v[150:153], v[222:225], v[70:73]
	s_setprio 0
	s_barrier
	s_add_u32 s98, s30, 0x80
	s_addc_u32 s99, s31, 0
	s_add_u32 s100, s34, 0xfff80080
	s_addc_u32 s101, s35, -1
	s_add_i32 s34, s63, s38
	s_mov_b32 m0, s34
	ds_read_b128 v[162:165], v220 offset:49152
	ds_read_b128 v[166:169], v220 offset:50176
	ds_read_b128 v[170:173], v220 offset:51200
	ds_read_b128 v[174:177], v220 offset:52224
	ds_read_b128 v[178:181], v220 offset:53248
	ds_read_b128 v[182:185], v220 offset:54272
	ds_read_b128 v[206:209], v220 offset:55296
	ds_read_b128 v[222:225], v220 offset:56320
	global_load_lds_dwordx4 v192, s[98:99]
	s_add_i32 m0, s34, 0x2000
	s_add_u32 s30, s30, 0x80080
	s_addc_u32 s31, s31, 0
	s_add_i32 s34, s64, s38
	global_load_lds_dwordx4 v196, s[98:99]
	s_mov_b32 m0, s34
	s_nop 0
	global_load_lds_dwordx4 v192, s[30:31]
	s_add_i32 m0, s34, 0x2000
	s_nop 0
	global_load_lds_dwordx4 v196, s[30:31]
	s_mov_b32 m0, s45
	s_nop 0
	global_load_lds_dwordx4 v190, s[100:101]
	s_mov_b32 m0, s46
	s_nop 0
	global_load_lds_dwordx4 v194, s[100:101]
	s_waitcnt vmcnt(8)
	s_waitcnt lgkmcnt(0)
	s_barrier
	s_setprio 1
	s_waitcnt lgkmcnt(0)
	v_mfma_f32_16x16x32_bf16 v[62:65], v[130:133], v[162:165], v[62:65]
	v_mfma_f32_16x16x32_bf16 v[58:61], v[138:141], v[162:165], v[58:61]
	v_mfma_f32_16x16x32_bf16 v[42:45], v[138:141], v[170:173], v[42:45]
	v_mfma_f32_16x16x32_bf16 v[50:53], v[130:133], v[170:173], v[50:53]
	v_mfma_f32_16x16x32_bf16 v[34:37], v[130:133], v[178:181], v[34:37]
	v_mfma_f32_16x16x32_bf16 v[26:29], v[138:141], v[178:181], v[26:29]
	v_mfma_f32_16x16x32_bf16 v[10:13], v[138:141], v[206:209], v[10:13]
	v_mfma_f32_16x16x32_bf16 v[18:21], v[130:133], v[206:209], v[18:21]
	v_mfma_f32_16x16x32_bf16 v[62:65], v[134:137], v[166:169], v[62:65]
	v_mfma_f32_16x16x32_bf16 v[58:61], v[142:145], v[166:169], v[58:61]
	v_mfma_f32_16x16x32_bf16 v[42:45], v[142:145], v[174:177], v[42:45]
	v_mfma_f32_16x16x32_bf16 v[50:53], v[134:137], v[174:177], v[50:53]
	v_mfma_f32_16x16x32_bf16 v[34:37], v[134:137], v[182:185], v[34:37]
	v_mfma_f32_16x16x32_bf16 v[26:29], v[142:145], v[182:185], v[26:29]
	v_mfma_f32_16x16x32_bf16 v[10:13], v[142:145], v[222:225], v[10:13]
	v_mfma_f32_16x16x32_bf16 v[18:21], v[134:137], v[222:225], v[18:21]
	s_setprio 0
	s_setprio 1
	v_mfma_f32_16x16x32_bf16 v[54:57], v[146:149], v[162:165], v[54:57]
	v_mfma_f32_16x16x32_bf16 v[46:49], v[154:157], v[162:165], v[46:49]
	v_mfma_f32_16x16x32_bf16 v[30:33], v[154:157], v[170:173], v[30:33]
	v_mfma_f32_16x16x32_bf16 v[38:41], v[146:149], v[170:173], v[38:41]
	v_mfma_f32_16x16x32_bf16 v[22:25], v[146:149], v[178:181], v[22:25]
	v_mfma_f32_16x16x32_bf16 v[14:17], v[154:157], v[178:181], v[14:17]
	v_mfma_f32_16x16x32_bf16 v[2:5], v[154:157], v[206:209], v[2:5]
	v_mfma_f32_16x16x32_bf16 v[6:9], v[146:149], v[206:209], v[6:9]
	v_mfma_f32_16x16x32_bf16 v[54:57], v[150:153], v[166:169], v[54:57]
	v_mfma_f32_16x16x32_bf16 v[46:49], v[158:161], v[166:169], v[46:49]
	v_mfma_f32_16x16x32_bf16 v[30:33], v[158:161], v[174:177], v[30:33]
	v_mfma_f32_16x16x32_bf16 v[38:41], v[150:153], v[174:177], v[38:41]
	v_mfma_f32_16x16x32_bf16 v[22:25], v[150:153], v[182:185], v[22:25]
	v_mfma_f32_16x16x32_bf16 v[14:17], v[158:161], v[182:185], v[14:17]
	v_mfma_f32_16x16x32_bf16 v[2:5], v[158:161], v[222:225], v[2:5]
	v_mfma_f32_16x16x32_bf16 v[6:9], v[150:153], v[222:225], v[6:9]
	s_setprio 0
	s_barrier
	s_add_i32 s62, s62, 2
	s_add_u32 s28, s28, 0x100
	s_addc_u32 s29, s29, 0
	s_add_u32 s60, s60, 0x100
	s_addc_u32 s61, s61, 0
	s_cmp_gt_u32 s62, 29
	s_cbranch_scc0 .LBB0_747
	s_and_b64 vcc, exec, s[8:9]
	s_cbranch_vccz .LBB0_750
	s_barrier

; #define PG8_STAGE(bufoff, gbase, voff) do { _Pragma("unroll") for (int _i = 0; _i < 2; ++_i) \
;         __builtin_amdgcn_global_load_lds((const unsigned*)((const char*)(gbase) + (voff)[_i]), (PG8_LAS unsigned*)(lds + (bufoff) + ldsw + _i * 8192), 16, 0, 0); } while (0)
; #define PG8_LDA(dst, b, h) do { _Pragma("unroll") for (int m = 0; m < 4; ++m) _Pragma("unroll") for (int k = 0; k < 2; ++k) dst[m][k] = *(const PG8_LAS bf16x8*)(lds + PG8_SA(b, h) + aoff + m * 2048 + k * 1024); } while (0)
; #define PG8_LDB(dst, b, h) do { _Pragma("unroll") for (int n = 0; n < 2; ++n) _Pragma("unroll") for (int k = 0; k < 2; ++k) dst[n][k] = *(const PG8_LAS bf16x8*)(lds + PG8_SB(b, h) + boff + n * 2048 + k * 1024); } while (0)
; #define PG8_WAIT_V(n) asm volatile("s_waitcnt vmcnt(" #n ")" ::: "memory")
; #define PG8_WAIT_L(n) asm volatile("s_waitcnt lgkmcnt(" #n ")" ::: "memory")
; #define PG8_BAR __builtin_amdgcn_s_barrier()
; #define PG8_SCHED __builtin_amdgcn_sched_barrier(0)
; template <class Epi, class Sched, bool ALIGN_EPI = false, bool SP2 = false>
; __device__ __forceinline__ void gemm_phase(PG8_LAS unsigned char* lds, const Gemm g, const Sched& S, const Epi& E) {
;     ...
;         const bool has_next = S.next(ui + 1, nxt);
;         const char* nA = has_next ? (const char*)g.A + (size_t)nxt.pm * tstep : cA; const char* nB = has_next ? (const char*)g.Bt + (size_t)nxt.pn * tstep : cB;
;         for (int t = 0; t < nt; t += 2) {
;             const bool last = (t == nt - 2);
;             const char* a1 = cA + (size_t)(t + 1) * kstep;
;             const char* a2 = last ? nA : cA + (size_t)(t + 2) * kstep; const char* b2 = last ? nB : cB + (size_t)(t + 2) * kstep;
;             const char* a3 = a2 + kstep; const char* b3 = b2 + kstep;
;             if (last && has_next) S.a_ready(nxt);
;             if constexpr (SP2) {
;             PG8_LDB(B0, 0, 0); PG8_LDB(B1, 0, 1); PG8_SCHED; PG8_LDA(At, 0, 0); PG8_STAGE(PG8_SA(1, 1), a1 + hstep, voffA);
;             PG8_WAIT_V(8); PG8_WAIT_L(0); PG8_BAR; PG8_MMA(0, 0, At, B0); PG8_MMA(0, 1, At, B1); PG8_BAR; PG8_SCHED;
;             PG8_LDA(At, 0, 1); PG8_STAGE(PG8_SB(0, 0), b2, voffB); PG8_STAGE(PG8_SB(0, 1), b2 + hstep, voffB); PG8_STAGE(PG8_SA(0, 0), a2, voffA);
;             PG8_WAIT_V(8); PG8_WAIT_L(0); PG8_BAR; PG8_MMA(1, 0, At, B0); PG8_MMA(1, 1, At, B1); PG8_BAR; PG8_SCHED;
.LBB0_871:
	s_ashr_i32 s15, s14, 31
	s_lshl_b64 s[16:17], s[14:15], 20
	s_add_u32 s16, s70, s16
	s_addc_u32 s17, s71, s17
	s_and_b64 s[18:19], s[2:3], exec
	s_cselect_b32 s15, s17, s23
	s_cselect_b32 s44, s16, s22
	s_ashr_i32 s13, s12, 31
	s_lshl_b64 s[18:19], s[12:13], 20
	s_add_u32 s18, s11, s18
	s_addc_u32 s19, s28, s19
	s_and_b64 s[26:27], s[2:3], exec
	s_cselect_b32 s13, s19, s25
	s_cselect_b32 s45, s18, s24
	s_add_u32 s22, s22, 0x80080
	s_addc_u32 s23, s23, 0
	s_add_u32 s46, s24, 0x100
	s_addc_u32 s47, s25, 0
	s_mov_b32 s48, -2
	v_add_u32_e32 v248, 0x18000, v151
	v_add_u32_e32 v249, 0x1c000, v151
	ds_read_b128 v[146:149], v153
	ds_read_b128 v[156:159], v153 offset:1024
	ds_read_b128 v[160:163], v153 offset:2048
	ds_read_b128 v[164:167], v153 offset:3072
	ds_read_b128 v[168:171], v154
	ds_read_b128 v[172:175], v154 offset:1024
	ds_read_b128 v[176:179], v154 offset:2048
	ds_read_b128 v[180:183], v154 offset:3072
	s_add_u32 s24, s22, 0xfff80080
	s_addc_u32 s25, s23, -1
	s_cmp_eq_u32 s48, 28
	s_cselect_b32 s27, s15, s25
	s_cselect_b32 s26, s44, s24
	s_cselect_b32 s25, s13, s47
	s_cselect_b32 s24, s45, s46
	s_add_i32 m0, s21, 0xc000
	ds_read_b128 v[190:193], v155
	ds_read_b128 v[194:197], v155 offset:1024
	ds_read_b128 v[198:201], v155 offset:2048
	ds_read_b128 v[202:205], v155 offset:3072
	ds_read_b128 v[206:209], v155 offset:4096
	ds_read_b128 v[216:219], v155 offset:5120
	ds_read_b128 v[220:223], v155 offset:6144
	ds_read_b128 v[224:227], v155 offset:7168
	global_load_lds_dwordx4 v138, s[22:23]
	s_add_i32 m0, s21, 0xe000
	s_nop 0
	global_load_lds_dwordx4 v140, s[22:23]
	s_waitcnt vmcnt(8)
	s_waitcnt lgkmcnt(0)
	s_barrier
	s_setprio 1
	s_waitcnt lgkmcnt(0)
	v_mfma_f32_16x16x32_bf16 v[126:129], v[146:149], v[190:193], 0
	v_mfma_f32_16x16x32_bf16 v[122:125], v[160:163], v[190:193], 0
	v_mfma_f32_16x16x32_bf16 v[106:109], v[160:163], v[198:201], 0
	v_mfma_f32_16x16x32_bf16 v[110:113], v[146:149], v[198:201], 0
	v_mfma_f32_16x16x32_bf16 v[94:97], v[146:149], v[206:209], 0
	v_mfma_f32_16x16x32_bf16 v[90:93], v[160:163], v[206:209], 0
	v_mfma_f32_16x16x32_bf16 v[74:77], v[160:163], v[220:223], 0
	v_mfma_f32_16x16x32_bf16 v[78:81], v[146:149], v[220:223], 0
	v_mfma_f32_16x16x32_bf16 v[126:129], v[156:159], v[194:197], v[126:129]
	v_mfma_f32_16x16x32_bf16 v[122:125], v[164:167], v[194:197], v[122:125]
	v_mfma_f32_16x16x32_bf16 v[106:109], v[164:167], v[202:205], v[106:109]
	v_mfma_f32_16x16x32_bf16 v[110:113], v[156:159], v[202:205], v[110:113]
	v_mfma_f32_16x16x32_bf16 v[94:97], v[156:159], v[216:219], v[94:97]
	v_mfma_f32_16x16x32_bf16 v[90:93], v[164:167], v[216:219], v[90:93]
	v_mfma_f32_16x16x32_bf16 v[74:77], v[164:167], v[224:227], v[74:77]
	v_mfma_f32_16x16x32_bf16 v[78:81], v[156:159], v[224:227], v[78:81]
	s_setprio 0
	s_setprio 1
	v_mfma_f32_16x16x32_bf16 v[118:121], v[168:171], v[190:193], 0
	v_mfma_f32_16x16x32_bf16 v[114:117], v[176:179], v[190:193], 0
	v_mfma_f32_16x16x32_bf16 v[98:101], v[176:179], v[198:201], 0
	v_mfma_f32_16x16x32_bf16 v[102:105], v[168:171], v[198:201], 0
	v_mfma_f32_16x16x32_bf16 v[86:89], v[168:171], v[206:209], 0
	v_mfma_f32_16x16x32_bf16 v[82:85], v[176:179], v[206:209], 0
	v_mfma_f32_16x16x32_bf16 v[66:69], v[176:179], v[220:223], 0
	v_mfma_f32_16x16x32_bf16 v[70:73], v[168:171], v[220:223], 0
	v_mfma_f32_16x16x32_bf16 v[118:121], v[172:175], v[194:197], v[118:121]
	v_mfma_f32_16x16x32_bf16 v[114:117], v[180:183], v[194:197], v[114:117]
	v_mfma_f32_16x16x32_bf16 v[98:101], v[180:183], v[202:205], v[98:101]
	v_mfma_f32_16x16x32_bf16 v[102:105], v[172:175], v[202:205], v[102:105]
	v_mfma_f32_16x16x32_bf16 v[86:89], v[172:175], v[216:219], v[86:89]
	v_mfma_f32_16x16x32_bf16 v[82:85], v[180:183], v[216:219], v[82:85]
	v_mfma_f32_16x16x32_bf16 v[66:69], v[180:183], v[224:227], v[66:69]
	v_mfma_f32_16x16x32_bf16 v[70:73], v[172:175], v[224:227], v[70:73]
	s_setprio 0
	s_barrier
	s_add_i32 s49, s40, s29
	s_mov_b32 m0, s49
	ds_read_b128 v[190:193], v155 offset:16384
	ds_read_b128 v[194:197], v155 offset:17408
	ds_read_b128 v[198:201], v155 offset:18432
	ds_read_b128 v[202:205], v155 offset:19456
	ds_read_b128 v[206:209], v155 offset:20480
	ds_read_b128 v[216:219], v155 offset:21504
	ds_read_b128 v[220:223], v155 offset:22528
	ds_read_b128 v[224:227], v155 offset:23552
	global_load_lds_dwordx4 v134, s[24:25]
	s_add_i32 m0, s49, 0x2000
	s_add_u32 s50, s24, 0x80000
	s_addc_u32 s51, s25, 0
	s_add_i32 s49, s41, s29
	global_load_lds_dwordx4 v130, s[24:25]
	s_mov_b32 m0, s49
	s_nop 0
	global_load_lds_dwordx4 v134, s[50:51]
	s_add_i32 m0, s49, 0x2000
	s_nop 0
	global_load_lds_dwordx4 v130, s[50:51]
	s_mov_b32 m0, s21
	s_nop 0
	global_load_lds_dwordx4 v136, s[26:27]
	s_mov_b32 m0, s33
	s_nop 0
	global_load_lds_dwordx4 v132, s[26:27]
	s_waitcnt vmcnt(8)
	s_waitcnt lgkmcnt(0)
	s_barrier
; #define PG8_STAGE(bufoff, gbase, voff) do { _Pragma("unroll") for (int _i = 0; _i < 2; ++_i) \
;         __builtin_amdgcn_global_load_lds((const unsigned*)((const char*)(gbase) + (voff)[_i]), (PG8_LAS unsigned*)(lds + (bufoff) + ldsw + _i * 8192), 16, 0, 0); } while (0)
; #define PG8_LDA(dst, b, h) do { _Pragma("unroll") for (int m = 0; m < 4; ++m) _Pragma("unroll") for (int k = 0; k < 2; ++k) dst[m][k] = *(const PG8_LAS bf16x8*)(lds + PG8_SA(b, h) + aoff + m * 2048 + k * 1024); } while (0)
; #define PG8_LDB(dst, b, h) do { _Pragma("unroll") for (int n = 0; n < 2; ++n) _Pragma("unroll") for (int k = 0; k < 2; ++k) dst[n][k] = *(const PG8_LAS bf16x8*)(lds + PG8_SB(b, h) + boff + n * 2048 + k * 1024); } while (0)
; #define PG8_WAIT_V(n) asm volatile("s_waitcnt vmcnt(" #n ")" ::: "memory")
; #define PG8_WAIT_L(n) asm volatile("s_waitcnt lgkmcnt(" #n ")" ::: "memory")
; #define PG8_BAR __builtin_amdgcn_s_barrier()
; #define PG8_SCHED __builtin_amdgcn_sched_barrier(0)
; template <class Epi, class Sched, bool ALIGN_EPI = false, bool SP2 = false>
; __device__ __forceinline__ void gemm_phase(PG8_LAS unsigned char* lds, const Gemm g, const Sched& S, const Epi& E) {
;     ...
;             PG8_WAIT_V(8); PG8_WAIT_L(0); PG8_BAR; PG8_MMA(1, 0, At, B0); PG8_MMA(1, 1, At, B1); PG8_BAR; PG8_SCHED;
;             PG8_LDB(B0, 1, 0); PG8_LDB(B1, 1, 1); PG8_SCHED; PG8_LDA(At, 1, 0); PG8_STAGE(PG8_SA(0, 1), a2 + hstep, voffA);
;             PG8_WAIT_V(8); PG8_WAIT_L(0); PG8_BAR; PG8_MMA(0, 0, At, B0); PG8_MMA(0, 1, At, B1); PG8_BAR; PG8_SCHED;
	s_setprio 1
	s_waitcnt lgkmcnt(0)
	v_mfma_f32_16x16x32_bf16 v[62:65], v[146:149], v[190:193], 0
	v_mfma_f32_16x16x32_bf16 v[58:61], v[160:163], v[190:193], 0
	v_mfma_f32_16x16x32_bf16 v[42:45], v[160:163], v[198:201], 0
	v_mfma_f32_16x16x32_bf16 v[46:49], v[146:149], v[198:201], 0
	v_mfma_f32_16x16x32_bf16 v[30:33], v[146:149], v[206:209], 0
	v_mfma_f32_16x16x32_bf16 v[26:29], v[160:163], v[206:209], 0
	v_mfma_f32_16x16x32_bf16 v[10:13], v[160:163], v[220:223], 0
	v_mfma_f32_16x16x32_bf16 v[14:17], v[146:149], v[220:223], 0
	v_mfma_f32_16x16x32_bf16 v[62:65], v[156:159], v[194:197], v[62:65]
	v_mfma_f32_16x16x32_bf16 v[58:61], v[164:167], v[194:197], v[58:61]
	v_mfma_f32_16x16x32_bf16 v[42:45], v[164:167], v[202:205], v[42:45]
	v_mfma_f32_16x16x32_bf16 v[46:49], v[156:159], v[202:205], v[46:49]
	v_mfma_f32_16x16x32_bf16 v[30:33], v[156:159], v[216:219], v[30:33]
	v_mfma_f32_16x16x32_bf16 v[26:29], v[164:167], v[216:219], v[26:29]
	v_mfma_f32_16x16x32_bf16 v[10:13], v[164:167], v[224:227], v[10:13]
	v_mfma_f32_16x16x32_bf16 v[14:17], v[156:159], v[224:227], v[14:17]
	s_setprio 0
	s_setprio 1
	v_mfma_f32_16x16x32_bf16 v[54:57], v[168:171], v[190:193], 0
	v_mfma_f32_16x16x32_bf16 v[50:53], v[176:179], v[190:193], 0
	v_mfma_f32_16x16x32_bf16 v[34:37], v[176:179], v[198:201], 0
	v_mfma_f32_16x16x32_bf16 v[38:41], v[168:171], v[198:201], 0
	v_mfma_f32_16x16x32_bf16 v[22:25], v[168:171], v[206:209], 0
	v_mfma_f32_16x16x32_bf16 v[18:21], v[176:179], v[206:209], 0
	v_mfma_f32_16x16x32_bf16 v[2:5], v[176:179], v[220:223], 0
	v_mfma_f32_16x16x32_bf16 v[6:9], v[168:171], v[220:223], 0
	v_mfma_f32_16x16x32_bf16 v[54:57], v[172:175], v[194:197], v[54:57]
	v_mfma_f32_16x16x32_bf16 v[50:53], v[180:183], v[194:197], v[50:53]
	v_mfma_f32_16x16x32_bf16 v[34:37], v[180:183], v[202:205], v[34:37]
	v_mfma_f32_16x16x32_bf16 v[38:41], v[172:175], v[202:205], v[38:41]
	v_mfma_f32_16x16x32_bf16 v[22:25], v[172:175], v[216:219], v[22:25]
	v_mfma_f32_16x16x32_bf16 v[18:21], v[180:183], v[216:219], v[18:21]
	v_mfma_f32_16x16x32_bf16 v[2:5], v[180:183], v[224:227], v[2:5]
	v_mfma_f32_16x16x32_bf16 v[6:9], v[172:175], v[224:227], v[6:9]
	s_setprio 0
	s_barrier
	s_add_i32 s49, 0, 0x18000
	s_add_i32 s50, 0, 0x1c000
	ds_read_b128 v[146:149], v248
	ds_read_b128 v[156:159], v248 offset:1024
	ds_read_b128 v[160:163], v248 offset:2048
	ds_read_b128 v[164:167], v248 offset:3072
	ds_read_b128 v[168:171], v249
	ds_read_b128 v[172:175], v249 offset:1024
	ds_read_b128 v[176:179], v249 offset:2048
	ds_read_b128 v[180:183], v249 offset:3072
	s_add_u32 s26, s26, 0x80000
	s_addc_u32 s27, s27, 0
	s_mov_b32 m0, s34
	ds_read_b128 v[190:193], v155 offset:32768
	ds_read_b128 v[194:197], v155 offset:33792
	ds_read_b128 v[198:201], v155 offset:34816
	ds_read_b128 v[202:205], v155 offset:35840
	ds_read_b128 v[206:209], v155 offset:36864
	ds_read_b128 v[216:219], v155 offset:37888
	ds_read_b128 v[220:223], v155 offset:38912
	ds_read_b128 v[224:227], v155 offset:39936
	global_load_lds_dwordx4 v136, s[26:27]
	s_mov_b32 m0, s35
	s_nop 0
	global_load_lds_dwordx4 v132, s[26:27]
	s_waitcnt vmcnt(8)
	s_waitcnt lgkmcnt(0)
	s_barrier
	s_setprio 1
	s_waitcnt lgkmcnt(0)
	v_mfma_f32_16x16x32_bf16 v[126:129], v[146:149], v[190:193], v[126:129]
	v_mfma_f32_16x16x32_bf16 v[122:125], v[160:163], v[190:193], v[122:125]
	v_mfma_f32_16x16x32_bf16 v[106:109], v[160:163], v[198:201], v[106:109]
	v_mfma_f32_16x16x32_bf16 v[110:113], v[146:149], v[198:201], v[110:113]
	v_mfma_f32_16x16x32_bf16 v[94:97], v[146:149], v[206:209], v[94:97]
	v_mfma_f32_16x16x32_bf16 v[90:93], v[160:163], v[206:209], v[90:93]
	v_mfma_f32_16x16x32_bf16 v[74:77], v[160:163], v[220:223], v[74:77]
	v_mfma_f32_16x16x32_bf16 v[78:81], v[146:149], v[220:223], v[78:81]
	v_mfma_f32_16x16x32_bf16 v[126:129], v[156:159], v[194:197], v[126:129]
	v_mfma_f32_16x16x32_bf16 v[122:125], v[164:167], v[194:197], v[122:125]
	v_mfma_f32_16x16x32_bf16 v[106:109], v[164:167], v[202:205], v[106:109]
	v_mfma_f32_16x16x32_bf16 v[110:113], v[156:159], v[202:205], v[110:113]
	v_mfma_f32_16x16x32_bf16 v[94:97], v[156:159], v[216:219], v[94:97]
	v_mfma_f32_16x16x32_bf16 v[90:93], v[164:167], v[216:219], v[90:93]
	v_mfma_f32_16x16x32_bf16 v[74:77], v[164:167], v[224:227], v[74:77]
	v_mfma_f32_16x16x32_bf16 v[78:81], v[156:159], v[224:227], v[78:81]
	s_setprio 0
	s_setprio 1
	v_mfma_f32_16x16x32_bf16 v[118:121], v[168:171], v[190:193], v[118:121]
	v_mfma_f32_16x16x32_bf16 v[114:117], v[176:179], v[190:193], v[114:117]
	v_mfma_f32_16x16x32_bf16 v[98:101], v[176:179], v[198:201], v[98:101]
	v_mfma_f32_16x16x32_bf16 v[102:105], v[168:171], v[198:201], v[102:105]
	v_mfma_f32_16x16x32_bf16 v[86:89], v[168:171], v[206:209], v[86:89]
	v_mfma_f32_16x16x32_bf16 v[82:85], v[176:179], v[206:209], v[82:85]
	v_mfma_f32_16x16x32_bf16 v[66:69], v[176:179], v[220:223], v[66:69]
	v_mfma_f32_16x16x32_bf16 v[70:73], v[168:171], v[220:223], v[70:73]
	v_mfma_f32_16x16x32_bf16 v[118:121], v[172:175], v[194:197], v[118:121]
	v_mfma_f32_16x16x32_bf16 v[114:117], v[180:183], v[194:197], v[114:117]
	v_mfma_f32_16x16x32_bf16 v[98:101], v[180:183], v[202:205], v[98:101]
	v_mfma_f32_16x16x32_bf16 v[102:105], v[172:175], v[202:205], v[102:105]
	v_mfma_f32_16x16x32_bf16 v[86:89], v[172:175], v[216:219], v[86:89]
	v_mfma_f32_16x16x32_bf16 v[82:85], v[180:183], v[216:219], v[82:85]
	v_mfma_f32_16x16x32_bf16 v[66:69], v[180:183], v[224:227], v[66:69]
	v_mfma_f32_16x16x32_bf16 v[70:73], v[172:175], v[224:227], v[70:73]
	s_setprio 0
	s_barrier
; #define PG8_STAGE(bufoff, gbase, voff) do { _Pragma("unroll") for (int _i = 0; _i < 2; ++_i) \
;         __builtin_amdgcn_global_load_lds((const unsigned*)((const char*)(gbase) + (voff)[_i]), (PG8_LAS unsigned*)(lds + (bufoff) + ldsw + _i * 8192), 16, 0, 0); } while (0)
; #define PG8_LDA(dst, b, h) do { _Pragma("unroll") for (int m = 0; m < 4; ++m) _Pragma("unroll") for (int k = 0; k < 2; ++k) dst[m][k] = *(const PG8_LAS bf16x8*)(lds + PG8_SA(b, h) + aoff + m * 2048 + k * 1024); } while (0)
; #define PG8_LDB(dst, b, h) do { _Pragma("unroll") for (int n = 0; n < 2; ++n) _Pragma("unroll") for (int k = 0; k < 2; ++k) dst[n][k] = *(const PG8_LAS bf16x8*)(lds + PG8_SB(b, h) + boff + n * 2048 + k * 1024); } while (0)
; #define PG8_WAIT_V(n) asm volatile("s_waitcnt vmcnt(" #n ")" ::: "memory")
; #define PG8_WAIT_L(n) asm volatile("s_waitcnt lgkmcnt(" #n ")" ::: "memory")
; #define PG8_BAR __builtin_amdgcn_s_barrier()
; #define PG8_SCHED __builtin_amdgcn_sched_barrier(0)
; template <class Epi, class Sched, bool ALIGN_EPI = false, bool SP2 = false>
; __device__ __forceinline__ void gemm_phase(PG8_LAS unsigned char* lds, const Gemm g, const Sched& S, const Epi& E) {
;     ...
;             PG8_LDB(B0, 0, 0); PG8_LDB(B1, 0, 1); PG8_SCHED; PG8_LDA(At, 0, 0); PG8_STAGE(PG8_SA(1, 1), a1 + hstep, voffA);
;             PG8_WAIT_V(8); PG8_WAIT_L(0); PG8_BAR; PG8_MMA(0, 0, At, B0); PG8_MMA(0, 1, At, B1); PG8_BAR; PG8_SCHED;
;             PG8_LDA(At, 0, 1); PG8_STAGE(PG8_SB(0, 0), b2, voffB); PG8_STAGE(PG8_SB(0, 1), b2 + hstep, voffB); PG8_STAGE(PG8_SA(0, 0), a2, voffA);
;             PG8_WAIT_V(8); PG8_WAIT_L(0); PG8_BAR; PG8_MMA(1, 0, At, B0); PG8_MMA(1, 1, At, B1); PG8_BAR; PG8_SCHED;
;             PG8_LDB(B0, 1, 0); PG8_LDB(B1, 1, 1); PG8_SCHED; PG8_LDA(At, 1, 0); PG8_STAGE(PG8_SA(0, 1), a2 + hstep, voffA);
;             PG8_WAIT_V(8); PG8_WAIT_L(0); PG8_BAR; PG8_MMA(0, 0, At, B0); PG8_MMA(0, 1, At, B1); PG8_BAR; PG8_SCHED;
;             PG8_LDA(At, 1, 1); PG8_STAGE(PG8_SB(1, 0), b3, voffB); PG8_STAGE(PG8_SB(1, 1), b3 + hstep, voffB); PG8_STAGE(PG8_SA(1, 0), a3, voffA);
;             PG8_WAIT_V(8); PG8_WAIT_L(0); PG8_BAR; PG8_MMA(1, 0, At, B0); PG8_MMA(1, 1, At, B1); PG8_BAR; PG8_SCHED;
	s_add_u32 s98, s24, 0x80
	s_addc_u32 s99, s25, 0
	s_add_u32 s100, s26, 0xfff80080
	s_addc_u32 s101, s27, -1
	s_add_i32 s26, s49, s29
	s_mov_b32 m0, s26
	ds_read_b128 v[190:193], v155 offset:49152
	ds_read_b128 v[194:197], v155 offset:50176
	ds_read_b128 v[198:201], v155 offset:51200
	ds_read_b128 v[202:205], v155 offset:52224
	ds_read_b128 v[206:209], v155 offset:53248
	ds_read_b128 v[216:219], v155 offset:54272
	ds_read_b128 v[220:223], v155 offset:55296
	ds_read_b128 v[224:227], v155 offset:56320
	global_load_lds_dwordx4 v134, s[98:99]
	s_add_i32 m0, s26, 0x2000
	s_add_u32 s24, s24, 0x80080
	s_addc_u32 s25, s25, 0
	s_add_i32 s26, s50, s29
	global_load_lds_dwordx4 v130, s[98:99]
	s_mov_b32 m0, s26
	s_nop 0
	global_load_lds_dwordx4 v134, s[24:25]
	s_add_i32 m0, s26, 0x2000
	s_nop 0
	global_load_lds_dwordx4 v130, s[24:25]
	s_mov_b32 m0, s37
	s_nop 0
	global_load_lds_dwordx4 v136, s[100:101]
	s_mov_b32 m0, s38
	s_nop 0
	global_load_lds_dwordx4 v132, s[100:101]
	s_waitcnt vmcnt(8)
	s_waitcnt lgkmcnt(0)
	s_barrier
	s_setprio 1
	s_waitcnt lgkmcnt(0)
	v_mfma_f32_16x16x32_bf16 v[62:65], v[146:149], v[190:193], v[62:65]
	v_mfma_f32_16x16x32_bf16 v[58:61], v[160:163], v[190:193], v[58:61]
	v_mfma_f32_16x16x32_bf16 v[42:45], v[160:163], v[198:201], v[42:45]
	v_mfma_f32_16x16x32_bf16 v[46:49], v[146:149], v[198:201], v[46:49]
	v_mfma_f32_16x16x32_bf16 v[30:33], v[146:149], v[206:209], v[30:33]
	v_mfma_f32_16x16x32_bf16 v[26:29], v[160:163], v[206:209], v[26:29]
	v_mfma_f32_16x16x32_bf16 v[10:13], v[160:163], v[220:223], v[10:13]
	v_mfma_f32_16x16x32_bf16 v[14:17], v[146:149], v[220:223], v[14:17]
	v_mfma_f32_16x16x32_bf16 v[62:65], v[156:159], v[194:197], v[62:65]
	v_mfma_f32_16x16x32_bf16 v[58:61], v[164:167], v[194:197], v[58:61]
	v_mfma_f32_16x16x32_bf16 v[42:45], v[164:167], v[202:205], v[42:45]
	v_mfma_f32_16x16x32_bf16 v[46:49], v[156:159], v[202:205], v[46:49]
	v_mfma_f32_16x16x32_bf16 v[30:33], v[156:159], v[216:219], v[30:33]
	v_mfma_f32_16x16x32_bf16 v[26:29], v[164:167], v[216:219], v[26:29]
	v_mfma_f32_16x16x32_bf16 v[10:13], v[164:167], v[224:227], v[10:13]
	v_mfma_f32_16x16x32_bf16 v[14:17], v[156:159], v[224:227], v[14:17]
	s_setprio 0
	s_setprio 1
	v_mfma_f32_16x16x32_bf16 v[54:57], v[168:171], v[190:193], v[54:57]
	v_mfma_f32_16x16x32_bf16 v[50:53], v[176:179], v[190:193], v[50:53]
	v_mfma_f32_16x16x32_bf16 v[34:37], v[176:179], v[198:201], v[34:37]
	v_mfma_f32_16x16x32_bf16 v[38:41], v[168:171], v[198:201], v[38:41]
	v_mfma_f32_16x16x32_bf16 v[22:25], v[168:171], v[206:209], v[22:25]
	v_mfma_f32_16x16x32_bf16 v[18:21], v[176:179], v[206:209], v[18:21]
	v_mfma_f32_16x16x32_bf16 v[2:5], v[176:179], v[220:223], v[2:5]
	v_mfma_f32_16x16x32_bf16 v[6:9], v[168:171], v[220:223], v[6:9]
	v_mfma_f32_16x16x32_bf16 v[54:57], v[172:175], v[194:197], v[54:57]
	v_mfma_f32_16x16x32_bf16 v[50:53], v[180:183], v[194:197], v[50:53]
	v_mfma_f32_16x16x32_bf16 v[34:37], v[180:183], v[202:205], v[34:37]
	v_mfma_f32_16x16x32_bf16 v[38:41], v[172:175], v[202:205], v[38:41]
	v_mfma_f32_16x16x32_bf16 v[22:25], v[172:175], v[216:219], v[22:25]
	v_mfma_f32_16x16x32_bf16 v[18:21], v[180:183], v[216:219], v[18:21]
	v_mfma_f32_16x16x32_bf16 v[2:5], v[180:183], v[224:227], v[2:5]
	v_mfma_f32_16x16x32_bf16 v[6:9], v[172:175], v[224:227], v[6:9]
	s_setprio 0
	s_barrier
	s_add_i32 s48, s48, 2
	s_add_u32 s22, s22, 0x100
	s_addc_u32 s23, s23, 0
	s_add_u32 s46, s46, 0x100
	s_addc_u32 s47, s47, 0
	s_cmp_gt_u32 s48, 29
.LBB0_872:
	ds_read_b128 v[146:149], v153
	ds_read_b128 v[156:159], v153 offset:1024
	ds_read_b128 v[160:163], v153 offset:2048
	ds_read_b128 v[164:167], v153 offset:3072
	ds_read_b128 v[168:171], v154
	ds_read_b128 v[172:175], v154 offset:1024
	ds_read_b128 v[176:179], v154 offset:2048
	ds_read_b128 v[180:183], v154 offset:3072
	s_add_u32 s24, s22, 0xfff80080
	s_addc_u32 s25, s23, -1
	s_cmp_eq_u32 s48, 28
	s_cselect_b32 s27, s15, s25
	s_cselect_b32 s26, s44, s24
	s_cselect_b32 s25, s13, s47
	s_cselect_b32 s24, s45, s46
	s_add_i32 m0, s21, 0xc000
	ds_read_b128 v[190:193], v155
	ds_read_b128 v[194:197], v155 offset:1024
	ds_read_b128 v[198:201], v155 offset:2048
	ds_read_b128 v[202:205], v155 offset:3072
	ds_read_b128 v[206:209], v155 offset:4096
	ds_read_b128 v[216:219], v155 offset:5120
	ds_read_b128 v[220:223], v155 offset:6144
	ds_read_b128 v[224:227], v155 offset:7168
	global_load_lds_dwordx4 v138, s[22:23]
	s_add_i32 m0, s21, 0xe000
	s_nop 0
	global_load_lds_dwordx4 v140, s[22:23]
	s_waitcnt vmcnt(8)
	s_waitcnt lgkmcnt(0)
	s_barrier
; #define PG8_STAGE(bufoff, gbase, voff) do { _Pragma("unroll") for (int _i = 0; _i < 2; ++_i) \
;         __builtin_amdgcn_global_load_lds((const unsigned*)((const char*)(gbase) + (voff)[_i]), (PG8_LAS unsigned*)(lds + (bufoff) + ldsw + _i * 8192), 16, 0, 0); } while (0)
; #define PG8_LDA(dst, b, h) do { _Pragma("unroll") for (int m = 0; m < 4; ++m) _Pragma("unroll") for (int k = 0; k < 2; ++k) dst[m][k] = *(const PG8_LAS bf16x8*)(lds + PG8_SA(b, h) + aoff + m * 2048 + k * 1024); } while (0)
; #define PG8_LDB(dst, b, h) do { _Pragma("unroll") for (int n = 0; n < 2; ++n) _Pragma("unroll") for (int k = 0; k < 2; ++k) dst[n][k] = *(const PG8_LAS bf16x8*)(lds + PG8_SB(b, h) + boff + n * 2048 + k * 1024); } while (0)
; #define PG8_WAIT_V(n) asm volatile("s_waitcnt vmcnt(" #n ")" ::: "memory")
; #define PG8_WAIT_L(n) asm volatile("s_waitcnt lgkmcnt(" #n ")" ::: "memory")
; #define PG8_BAR __builtin_amdgcn_s_barrier()
; #define PG8_SCHED __builtin_amdgcn_sched_barrier(0)
; template <class Epi, class Sched, bool ALIGN_EPI = false, bool SP2 = false>
; __device__ __forceinline__ void gemm_phase(PG8_LAS unsigned char* lds, const Gemm g, const Sched& S, const Epi& E) {
;     ...
;             PG8_LDB(B0, 0, 0); PG8_LDB(B1, 0, 1); PG8_SCHED; PG8_LDA(At, 0, 0); PG8_STAGE(PG8_SA(1, 1), a1 + hstep, voffA);
;             PG8_WAIT_V(8); PG8_WAIT_L(0); PG8_BAR; PG8_MMA(0, 0, At, B0); PG8_MMA(0, 1, At, B1); PG8_BAR; PG8_SCHED;
;             PG8_LDA(At, 0, 1); PG8_STAGE(PG8_SB(0, 0), b2, voffB); PG8_STAGE(PG8_SB(0, 1), b2 + hstep, voffB); PG8_STAGE(PG8_SA(0, 0), a2, voffA);
;             PG8_WAIT_V(8); PG8_WAIT_L(0); PG8_BAR; PG8_MMA(1, 0, At, B0); PG8_MMA(1, 1, At, B1); PG8_BAR; PG8_SCHED;
;             PG8_LDB(B0, 1, 0); PG8_LDB(B1, 1, 1); PG8_SCHED; PG8_LDA(At, 1, 0); PG8_STAGE(PG8_SA(0, 1), a2 + hstep, voffA);
;             PG8_WAIT_V(8); PG8_WAIT_L(0); PG8_BAR; PG8_MMA(0, 0, At, B0); PG8_MMA(0, 1, At, B1); PG8_BAR; PG8_SCHED;
	s_setprio 1
	s_waitcnt lgkmcnt(0)
	v_mfma_f32_16x16x32_bf16 v[126:129], v[146:149], v[190:193], v[126:129]
	v_mfma_f32_16x16x32_bf16 v[122:125], v[160:163], v[190:193], v[122:125]
	v_mfma_f32_16x16x32_bf16 v[106:109], v[160:163], v[198:201], v[106:109]
	v_mfma_f32_16x16x32_bf16 v[110:113], v[146:149], v[198:201], v[110:113]
	v_mfma_f32_16x16x32_bf16 v[94:97], v[146:149], v[206:209], v[94:97]
	v_mfma_f32_16x16x32_bf16 v[90:93], v[160:163], v[206:209], v[90:93]
	v_mfma_f32_16x16x32_bf16 v[74:77], v[160:163], v[220:223], v[74:77]
	v_mfma_f32_16x16x32_bf16 v[78:81], v[146:149], v[220:223], v[78:81]
	v_mfma_f32_16x16x32_bf16 v[126:129], v[156:159], v[194:197], v[126:129]
	v_mfma_f32_16x16x32_bf16 v[122:125], v[164:167], v[194:197], v[122:125]
	v_mfma_f32_16x16x32_bf16 v[106:109], v[164:167], v[202:205], v[106:109]
	v_mfma_f32_16x16x32_bf16 v[110:113], v[156:159], v[202:205], v[110:113]
	v_mfma_f32_16x16x32_bf16 v[94:97], v[156:159], v[216:219], v[94:97]
	v_mfma_f32_16x16x32_bf16 v[90:93], v[164:167], v[216:219], v[90:93]
	v_mfma_f32_16x16x32_bf16 v[74:77], v[164:167], v[224:227], v[74:77]
	v_mfma_f32_16x16x32_bf16 v[78:81], v[156:159], v[224:227], v[78:81]
	s_setprio 0
	s_setprio 1
	v_mfma_f32_16x16x32_bf16 v[118:121], v[168:171], v[190:193], v[118:121]
	v_mfma_f32_16x16x32_bf16 v[114:117], v[176:179], v[190:193], v[114:117]
	v_mfma_f32_16x16x32_bf16 v[98:101], v[176:179], v[198:201], v[98:101]
	v_mfma_f32_16x16x32_bf16 v[102:105], v[168:171], v[198:201], v[102:105]
	v_mfma_f32_16x16x32_bf16 v[86:89], v[168:171], v[206:209], v[86:89]
	v_mfma_f32_16x16x32_bf16 v[82:85], v[176:179], v[206:209], v[82:85]
	v_mfma_f32_16x16x32_bf16 v[66:69], v[176:179], v[220:223], v[66:69]
	v_mfma_f32_16x16x32_bf16 v[70:73], v[168:171], v[220:223], v[70:73]
	v_mfma_f32_16x16x32_bf16 v[118:121], v[172:175], v[194:197], v[118:121]
	v_mfma_f32_16x16x32_bf16 v[114:117], v[180:183], v[194:197], v[114:117]
	v_mfma_f32_16x16x32_bf16 v[98:101], v[180:183], v[202:205], v[98:101]
	v_mfma_f32_16x16x32_bf16 v[102:105], v[172:175], v[202:205], v[102:105]
	v_mfma_f32_16x16x32_bf16 v[86:89], v[172:175], v[216:219], v[86:89]
	v_mfma_f32_16x16x32_bf16 v[82:85], v[180:183], v[216:219], v[82:85]
	v_mfma_f32_16x16x32_bf16 v[66:69], v[180:183], v[224:227], v[66:69]
	v_mfma_f32_16x16x32_bf16 v[70:73], v[172:175], v[224:227], v[70:73]
	s_setprio 0
	s_barrier
	s_add_i32 s49, s40, s29
	s_mov_b32 m0, s49
	ds_read_b128 v[190:193], v155 offset:16384
	ds_read_b128 v[194:197], v155 offset:17408
	ds_read_b128 v[198:201], v155 offset:18432
	ds_read_b128 v[202:205], v155 offset:19456
	ds_read_b128 v[206:209], v155 offset:20480
	ds_read_b128 v[216:219], v155 offset:21504
	ds_read_b128 v[220:223], v155 offset:22528
	ds_read_b128 v[224:227], v155 offset:23552
	global_load_lds_dwordx4 v134, s[24:25]
	s_add_i32 m0, s49, 0x2000
	s_add_u32 s50, s24, 0x80000
	s_addc_u32 s51, s25, 0
	s_add_i32 s49, s41, s29
	global_load_lds_dwordx4 v130, s[24:25]
	s_mov_b32 m0, s49
	s_nop 0
	global_load_lds_dwordx4 v134, s[50:51]
	s_add_i32 m0, s49, 0x2000
	s_nop 0
	global_load_lds_dwordx4 v130, s[50:51]
	s_mov_b32 m0, s21
	s_nop 0
	global_load_lds_dwordx4 v136, s[26:27]
	s_mov_b32 m0, s33
	s_nop 0
	global_load_lds_dwordx4 v132, s[26:27]
	s_waitcnt vmcnt(8)
	s_waitcnt lgkmcnt(0)
	s_barrier
	s_setprio 1
	s_waitcnt lgkmcnt(0)
	v_mfma_f32_16x16x32_bf16 v[62:65], v[146:149], v[190:193], v[62:65]
	v_mfma_f32_16x16x32_bf16 v[58:61], v[160:163], v[190:193], v[58:61]
	v_mfma_f32_16x16x32_bf16 v[42:45], v[160:163], v[198:201], v[42:45]
	v_mfma_f32_16x16x32_bf16 v[46:49], v[146:149], v[198:201], v[46:49]
	v_mfma_f32_16x16x32_bf16 v[30:33], v[146:149], v[206:209], v[30:33]
	v_mfma_f32_16x16x32_bf16 v[26:29], v[160:163], v[206:209], v[26:29]
	v_mfma_f32_16x16x32_bf16 v[10:13], v[160:163], v[220:223], v[10:13]
	v_mfma_f32_16x16x32_bf16 v[14:17], v[146:149], v[220:223], v[14:17]
	v_mfma_f32_16x16x32_bf16 v[62:65], v[156:159], v[194:197], v[62:65]
	v_mfma_f32_16x16x32_bf16 v[58:61], v[164:167], v[194:197], v[58:61]
	v_mfma_f32_16x16x32_bf16 v[42:45], v[164:167], v[202:205], v[42:45]
	v_mfma_f32_16x16x32_bf16 v[46:49], v[156:159], v[202:205], v[46:49]
	v_mfma_f32_16x16x32_bf16 v[30:33], v[156:159], v[216:219], v[30:33]
	v_mfma_f32_16x16x32_bf16 v[26:29], v[164:167], v[216:219], v[26:29]
	v_mfma_f32_16x16x32_bf16 v[10:13], v[164:167], v[224:227], v[10:13]
	v_mfma_f32_16x16x32_bf16 v[14:17], v[156:159], v[224:227], v[14:17]
	s_setprio 0
	s_setprio 1
	v_mfma_f32_16x16x32_bf16 v[54:57], v[168:171], v[190:193], v[54:57]
	v_mfma_f32_16x16x32_bf16 v[50:53], v[176:179], v[190:193], v[50:53]
	v_mfma_f32_16x16x32_bf16 v[34:37], v[176:179], v[198:201], v[34:37]
	v_mfma_f32_16x16x32_bf16 v[38:41], v[168:171], v[198:201], v[38:41]
	v_mfma_f32_16x16x32_bf16 v[22:25], v[168:171], v[206:209], v[22:25]
	v_mfma_f32_16x16x32_bf16 v[18:21], v[176:179], v[206:209], v[18:21]
	v_mfma_f32_16x16x32_bf16 v[2:5], v[176:179], v[220:223], v[2:5]
	v_mfma_f32_16x16x32_bf16 v[6:9], v[168:171], v[220:223], v[6:9]
	v_mfma_f32_16x16x32_bf16 v[54:57], v[172:175], v[194:197], v[54:57]
	v_mfma_f32_16x16x32_bf16 v[50:53], v[180:183], v[194:197], v[50:53]
	v_mfma_f32_16x16x32_bf16 v[34:37], v[180:183], v[202:205], v[34:37]
	v_mfma_f32_16x16x32_bf16 v[38:41], v[172:175], v[202:205], v[38:41]
	v_mfma_f32_16x16x32_bf16 v[22:25], v[172:175], v[216:219], v[22:25]
	v_mfma_f32_16x16x32_bf16 v[18:21], v[180:183], v[216:219], v[18:21]
	v_mfma_f32_16x16x32_bf16 v[2:5], v[180:183], v[224:227], v[2:5]
	v_mfma_f32_16x16x32_bf16 v[6:9], v[172:175], v[224:227], v[6:9]
	s_setprio 0
	s_barrier
; #define PG8_STAGE(bufoff, gbase, voff) do { _Pragma("unroll") for (int _i = 0; _i < 2; ++_i) \
;         __builtin_amdgcn_global_load_lds((const unsigned*)((const char*)(gbase) + (voff)[_i]), (PG8_LAS unsigned*)(lds + (bufoff) + ldsw + _i * 8192), 16, 0, 0); } while (0)
; #define PG8_LDA(dst, b, h) do { _Pragma("unroll") for (int m = 0; m < 4; ++m) _Pragma("unroll") for (int k = 0; k < 2; ++k) dst[m][k] = *(const PG8_LAS bf16x8*)(lds + PG8_SA(b, h) + aoff + m * 2048 + k * 1024); } while (0)
; #define PG8_LDB(dst, b, h) do { _Pragma("unroll") for (int n = 0; n < 2; ++n) _Pragma("unroll") for (int k = 0; k < 2; ++k) dst[n][k] = *(const PG8_LAS bf16x8*)(lds + PG8_SB(b, h) + boff + n * 2048 + k * 1024); } while (0)
; #define PG8_WAIT_V(n) asm volatile("s_waitcnt vmcnt(" #n ")" ::: "memory")
; #define PG8_WAIT_L(n) asm volatile("s_waitcnt lgkmcnt(" #n ")" ::: "memory")
; #define PG8_BAR __builtin_amdgcn_s_barrier()
; #define PG8_SCHED __builtin_amdgcn_sched_barrier(0)
; template <class Epi, class Sched, bool ALIGN_EPI = false, bool SP2 = false>
; __device__ __forceinline__ void gemm_phase(PG8_LAS unsigned char* lds, const Gemm g, const Sched& S, const Epi& E) {
;     ...
;             PG8_LDB(B0, 1, 0); PG8_LDB(B1, 1, 1); PG8_SCHED; PG8_LDA(At, 1, 0); PG8_STAGE(PG8_SA(0, 1), a2 + hstep, voffA);
;             PG8_WAIT_V(8); PG8_WAIT_L(0); PG8_BAR; PG8_MMA(0, 0, At, B0); PG8_MMA(0, 1, At, B1); PG8_BAR; PG8_SCHED;
;             PG8_LDA(At, 1, 1); PG8_STAGE(PG8_SB(1, 0), b3, voffB); PG8_STAGE(PG8_SB(1, 1), b3 + hstep, voffB); PG8_STAGE(PG8_SA(1, 0), a3, voffA);
;             PG8_WAIT_V(8); PG8_WAIT_L(0); PG8_BAR; PG8_MMA(1, 0, At, B0); PG8_MMA(1, 1, At, B1); PG8_BAR; PG8_SCHED;
	s_add_i32 s49, 0, 0x18000
	s_add_i32 s50, 0, 0x1c000
	ds_read_b128 v[146:149], v248
	ds_read_b128 v[156:159], v248 offset:1024
	ds_read_b128 v[160:163], v248 offset:2048
	ds_read_b128 v[164:167], v248 offset:3072
	ds_read_b128 v[168:171], v249
	ds_read_b128 v[172:175], v249 offset:1024
	ds_read_b128 v[176:179], v249 offset:2048
	ds_read_b128 v[180:183], v249 offset:3072
	s_add_u32 s26, s26, 0x80000
	s_addc_u32 s27, s27, 0
	s_mov_b32 m0, s34
	ds_read_b128 v[190:193], v155 offset:32768
	ds_read_b128 v[194:197], v155 offset:33792
	ds_read_b128 v[198:201], v155 offset:34816
	ds_read_b128 v[202:205], v155 offset:35840
	ds_read_b128 v[206:209], v155 offset:36864
	ds_read_b128 v[216:219], v155 offset:37888
	ds_read_b128 v[220:223], v155 offset:38912
	ds_read_b128 v[224:227], v155 offset:39936
	global_load_lds_dwordx4 v136, s[26:27]
	s_mov_b32 m0, s35
	s_nop 0
	global_load_lds_dwordx4 v132, s[26:27]
	s_waitcnt vmcnt(8)
	s_waitcnt lgkmcnt(0)
	s_barrier
	s_setprio 1
	s_waitcnt lgkmcnt(0)
	v_mfma_f32_16x16x32_bf16 v[126:129], v[146:149], v[190:193], v[126:129]
	v_mfma_f32_16x16x32_bf16 v[122:125], v[160:163], v[190:193], v[122:125]
	v_mfma_f32_16x16x32_bf16 v[106:109], v[160:163], v[198:201], v[106:109]
	v_mfma_f32_16x16x32_bf16 v[110:113], v[146:149], v[198:201], v[110:113]
	v_mfma_f32_16x16x32_bf16 v[94:97], v[146:149], v[206:209], v[94:97]
	v_mfma_f32_16x16x32_bf16 v[90:93], v[160:163], v[206:209], v[90:93]
	v_mfma_f32_16x16x32_bf16 v[74:77], v[160:163], v[220:223], v[74:77]
	v_mfma_f32_16x16x32_bf16 v[78:81], v[146:149], v[220:223], v[78:81]
	v_mfma_f32_16x16x32_bf16 v[126:129], v[156:159], v[194:197], v[126:129]
	v_mfma_f32_16x16x32_bf16 v[122:125], v[164:167], v[194:197], v[122:125]
	v_mfma_f32_16x16x32_bf16 v[106:109], v[164:167], v[202:205], v[106:109]
	v_mfma_f32_16x16x32_bf16 v[110:113], v[156:159], v[202:205], v[110:113]
	v_mfma_f32_16x16x32_bf16 v[94:97], v[156:159], v[216:219], v[94:97]
	v_mfma_f32_16x16x32_bf16 v[90:93], v[164:167], v[216:219], v[90:93]
	v_mfma_f32_16x16x32_bf16 v[74:77], v[164:167], v[224:227], v[74:77]
	v_mfma_f32_16x16x32_bf16 v[78:81], v[156:159], v[224:227], v[78:81]
	s_setprio 0
	s_setprio 1
	v_mfma_f32_16x16x32_bf16 v[118:121], v[168:171], v[190:193], v[118:121]
	v_mfma_f32_16x16x32_bf16 v[114:117], v[176:179], v[190:193], v[114:117]
	v_mfma_f32_16x16x32_bf16 v[98:101], v[176:179], v[198:201], v[98:101]
	v_mfma_f32_16x16x32_bf16 v[102:105], v[168:171], v[198:201], v[102:105]
	v_mfma_f32_16x16x32_bf16 v[86:89], v[168:171], v[206:209], v[86:89]
	v_mfma_f32_16x16x32_bf16 v[82:85], v[176:179], v[206:209], v[82:85]
	v_mfma_f32_16x16x32_bf16 v[66:69], v[176:179], v[220:223], v[66:69]
	v_mfma_f32_16x16x32_bf16 v[70:73], v[168:171], v[220:223], v[70:73]
	v_mfma_f32_16x16x32_bf16 v[118:121], v[172:175], v[194:197], v[118:121]
	v_mfma_f32_16x16x32_bf16 v[114:117], v[180:183], v[194:197], v[114:117]
	v_mfma_f32_16x16x32_bf16 v[98:101], v[180:183], v[202:205], v[98:101]
	v_mfma_f32_16x16x32_bf16 v[102:105], v[172:175], v[202:205], v[102:105]
	v_mfma_f32_16x16x32_bf16 v[86:89], v[172:175], v[216:219], v[86:89]
	v_mfma_f32_16x16x32_bf16 v[82:85], v[180:183], v[216:219], v[82:85]
	v_mfma_f32_16x16x32_bf16 v[66:69], v[180:183], v[224:227], v[66:69]
	v_mfma_f32_16x16x32_bf16 v[70:73], v[172:175], v[224:227], v[70:73]
	s_setprio 0
	s_barrier
	s_add_u32 s98, s24, 0x80
	s_addc_u32 s99, s25, 0
	s_add_u32 s100, s26, 0xfff80080
	s_addc_u32 s101, s27, -1
	s_add_i32 s26, s49, s29
	s_mov_b32 m0, s26
	ds_read_b128 v[190:193], v155 offset:49152
	ds_read_b128 v[194:197], v155 offset:50176
	ds_read_b128 v[198:201], v155 offset:51200
	ds_read_b128 v[202:205], v155 offset:52224
	ds_read_b128 v[206:209], v155 offset:53248
	ds_read_b128 v[216:219], v155 offset:54272
	ds_read_b128 v[220:223], v155 offset:55296
	ds_read_b128 v[224:227], v155 offset:56320
	global_load_lds_dwordx4 v134, s[98:99]
	s_add_i32 m0, s26, 0x2000
	s_add_u32 s24, s24, 0x80080
	s_addc_u32 s25, s25, 0
	s_add_i32 s26, s50, s29
	global_load_lds_dwordx4 v130, s[98:99]
	s_mov_b32 m0, s26
	s_nop 0
	global_load_lds_dwordx4 v134, s[24:25]
	s_add_i32 m0, s26, 0x2000
	s_nop 0
	global_load_lds_dwordx4 v130, s[24:25]
	s_mov_b32 m0, s37
	s_nop 0
	global_load_lds_dwordx4 v136, s[100:101]
	s_mov_b32 m0, s38
	s_nop 0
	global_load_lds_dwordx4 v132, s[100:101]
	s_waitcnt vmcnt(8)
	s_waitcnt lgkmcnt(0)
	s_barrier
	s_setprio 1
	s_waitcnt lgkmcnt(0)
	v_mfma_f32_16x16x32_bf16 v[62:65], v[146:149], v[190:193], v[62:65]
	v_mfma_f32_16x16x32_bf16 v[58:61], v[160:163], v[190:193], v[58:61]
	v_mfma_f32_16x16x32_bf16 v[42:45], v[160:163], v[198:201], v[42:45]
	v_mfma_f32_16x16x32_bf16 v[46:49], v[146:149], v[198:201], v[46:49]
	v_mfma_f32_16x16x32_bf16 v[30:33], v[146:149], v[206:209], v[30:33]
	v_mfma_f32_16x16x32_bf16 v[26:29], v[160:163], v[206:209], v[26:29]
	v_mfma_f32_16x16x32_bf16 v[10:13], v[160:163], v[220:223], v[10:13]
	v_mfma_f32_16x16x32_bf16 v[14:17], v[146:149], v[220:223], v[14:17]
	v_mfma_f32_16x16x32_bf16 v[62:65], v[156:159], v[194:197], v[62:65]
	v_mfma_f32_16x16x32_bf16 v[58:61], v[164:167], v[194:197], v[58:61]
	v_mfma_f32_16x16x32_bf16 v[42:45], v[164:167], v[202:205], v[42:45]
	v_mfma_f32_16x16x32_bf16 v[46:49], v[156:159], v[202:205], v[46:49]
	v_mfma_f32_16x16x32_bf16 v[30:33], v[156:159], v[216:219], v[30:33]
	v_mfma_f32_16x16x32_bf16 v[26:29], v[164:167], v[216:219], v[26:29]
	v_mfma_f32_16x16x32_bf16 v[10:13], v[164:167], v[224:227], v[10:13]
	v_mfma_f32_16x16x32_bf16 v[14:17], v[156:159], v[224:227], v[14:17]
	s_setprio 0
	s_setprio 1
	v_mfma_f32_16x16x32_bf16 v[54:57], v[168:171], v[190:193], v[54:57]
	v_mfma_f32_16x16x32_bf16 v[50:53], v[176:179], v[190:193], v[50:53]
	v_mfma_f32_16x16x32_bf16 v[34:37], v[176:179], v[198:201], v[34:37]
	v_mfma_f32_16x16x32_bf16 v[38:41], v[168:171], v[198:201], v[38:41]
	v_mfma_f32_16x16x32_bf16 v[22:25], v[168:171], v[206:209], v[22:25]
	v_mfma_f32_16x16x32_bf16 v[18:21], v[176:179], v[206:209], v[18:21]
	v_mfma_f32_16x16x32_bf16 v[2:5], v[176:179], v[220:223], v[2:5]
	v_mfma_f32_16x16x32_bf16 v[6:9], v[168:171], v[220:223], v[6:9]
	v_mfma_f32_16x16x32_bf16 v[54:57], v[172:175], v[194:197], v[54:57]
	v_mfma_f32_16x16x32_bf16 v[50:53], v[180:183], v[194:197], v[50:53]
	v_mfma_f32_16x16x32_bf16 v[34:37], v[180:183], v[202:205], v[34:37]
	v_mfma_f32_16x16x32_bf16 v[38:41], v[172:175], v[202:205], v[38:41]
	v_mfma_f32_16x16x32_bf16 v[22:25], v[172:175], v[216:219], v[22:25]
	v_mfma_f32_16x16x32_bf16 v[18:21], v[180:183], v[216:219], v[18:21]
	v_mfma_f32_16x16x32_bf16 v[2:5], v[180:183], v[224:227], v[2:5]
	v_mfma_f32_16x16x32_bf16 v[6:9], v[172:175], v[224:227], v[6:9]
	s_setprio 0
	s_barrier
	s_add_i32 s48, s48, 2
	s_add_u32 s22, s22, 0x100
	s_addc_u32 s23, s23, 0
	s_add_u32 s46, s46, 0x100
	s_addc_u32 s47, s47, 0
	s_cmp_gt_u32 s48, 29
	s_cbranch_scc0 .LBB0_872
	s_and_b64 vcc, exec, s[8:9]
	s_cbranch_vccz .LBB0_875
	s_barrier

; #define PG8_STAGE(bufoff, gbase, voff) do { _Pragma("unroll") for (int _i = 0; _i < 2; ++_i) \
;         __builtin_amdgcn_global_load_lds((const unsigned*)((const char*)(gbase) + (voff)[_i]), (PG8_LAS unsigned*)(lds + (bufoff) + ldsw + _i * 8192), 16, 0, 0); } while (0)
; #define PG8_LDA(dst, b, h) do { _Pragma("unroll") for (int m = 0; m < 4; ++m) _Pragma("unroll") for (int k = 0; k < 2; ++k) dst[m][k] = *(const PG8_LAS bf16x8*)(lds + PG8_SA(b, h) + aoff + m * 2048 + k * 1024); } while (0)
; #define PG8_LDB(dst, b, h) do { _Pragma("unroll") for (int n = 0; n < 2; ++n) _Pragma("unroll") for (int k = 0; k < 2; ++k) dst[n][k] = *(const PG8_LAS bf16x8*)(lds + PG8_SB(b, h) + boff + n * 2048 + k * 1024); } while (0)
; #define PG8_WAIT_V(n) asm volatile("s_waitcnt vmcnt(" #n ")" ::: "memory")
; #define PG8_WAIT_L(n) asm volatile("s_waitcnt lgkmcnt(" #n ")" ::: "memory")
; #define PG8_BAR __builtin_amdgcn_s_barrier()
; #define PG8_SCHED __builtin_amdgcn_sched_barrier(0)
; template <class Epi, class Sched, bool ALIGN_EPI = false, bool SP2 = false>
; __device__ __forceinline__ void gemm_phase(PG8_LAS unsigned char* lds, const Gemm g, const Sched& S, const Epi& E) {
;     ...
;             const char* a1 = cA + (size_t)(t + 1) * kstep;
;             const char* a2 = last ? nA : cA + (size_t)(t + 2) * kstep; const char* b2 = last ? nB : cB + (size_t)(t + 2) * kstep;
;             const char* a3 = a2 + kstep; const char* b3 = b2 + kstep;
;             if (last && has_next) S.a_ready(nxt);
;             if constexpr (SP2) {
;             PG8_LDB(B0, 0, 0); PG8_LDB(B1, 0, 1); PG8_SCHED; PG8_LDA(At, 0, 0); PG8_STAGE(PG8_SA(1, 1), a1 + hstep, voffA);
;             PG8_WAIT_V(8); PG8_WAIT_L(0); PG8_BAR; PG8_MMA(0, 0, At, B0); PG8_MMA(0, 1, At, B1); PG8_BAR; PG8_SCHED;
;             PG8_LDA(At, 0, 1); PG8_STAGE(PG8_SB(0, 0), b2, voffB); PG8_STAGE(PG8_SB(0, 1), b2 + hstep, voffB); PG8_STAGE(PG8_SA(0, 0), a2, voffA);
;             PG8_WAIT_V(8); PG8_WAIT_L(0); PG8_BAR; PG8_MMA(1, 0, At, B0); PG8_MMA(1, 1, At, B1); PG8_BAR; PG8_SCHED;
.LBB0_950:
	s_add_u32 s14, s14, 0x160080
	s_addc_u32 s15, s15, 0
	s_add_u32 s48, s16, 0x100
	s_addc_u32 s49, s17, 0
	s_mov_b32 s50, -2
	v_add_u32_e32 v248, 0x18000, v175
	v_add_u32_e32 v249, 0x1c000, v175
	ds_read_b128 v[130:133], v177
	ds_read_b128 v[134:137], v177 offset:1024
	ds_read_b128 v[138:141], v177 offset:2048
	ds_read_b128 v[142:145], v177 offset:3072
	ds_read_b128 v[146:149], v178
	ds_read_b128 v[150:153], v178 offset:1024
	ds_read_b128 v[170:173], v178 offset:2048
	ds_read_b128 v[180:183], v178 offset:3072
	s_add_u32 s16, s14, 0xffea0080
	s_addc_u32 s17, s15, -1
	s_cmpk_eq_i32 s50, 0x54
	s_cselect_b32 s19, s5, s17
	s_cselect_b32 s18, s4, s16
	s_cselect_b32 s17, s13, s49
	s_cselect_b32 s16, s12, s48
	s_add_i32 m0, s24, 0xc000
	ds_read_b128 v[190:193], v179
	ds_read_b128 v[194:197], v179 offset:1024
	ds_read_b128 v[198:201], v179 offset:2048
	ds_read_b128 v[202:205], v179 offset:3072
	ds_read_b128 v[206:209], v179 offset:4096
	ds_read_b128 v[216:219], v179 offset:5120
	ds_read_b128 v[220:223], v179 offset:6144
	ds_read_b128 v[224:227], v179 offset:7168
	global_load_lds_dwordx4 v162, s[14:15]
	s_add_i32 m0, s24, 0xe000
	s_nop 0
	global_load_lds_dwordx4 v164, s[14:15]
	s_waitcnt vmcnt(8)
	s_waitcnt lgkmcnt(0)
	s_barrier
	s_setprio 1
	s_waitcnt lgkmcnt(0)
	v_mfma_f32_16x16x32_bf16 v[126:129], v[130:133], v[190:193], 0
	v_mfma_f32_16x16x32_bf16 v[122:125], v[138:141], v[190:193], 0
	v_mfma_f32_16x16x32_bf16 v[106:109], v[138:141], v[198:201], 0
	v_mfma_f32_16x16x32_bf16 v[110:113], v[130:133], v[198:201], 0
	v_mfma_f32_16x16x32_bf16 v[98:101], v[130:133], v[206:209], 0
	v_mfma_f32_16x16x32_bf16 v[90:93], v[138:141], v[206:209], 0
	v_mfma_f32_16x16x32_bf16 v[74:77], v[138:141], v[220:223], 0
	v_mfma_f32_16x16x32_bf16 v[82:85], v[130:133], v[220:223], 0
	v_mfma_f32_16x16x32_bf16 v[126:129], v[134:137], v[194:197], v[126:129]
	v_mfma_f32_16x16x32_bf16 v[122:125], v[142:145], v[194:197], v[122:125]
	v_mfma_f32_16x16x32_bf16 v[106:109], v[142:145], v[202:205], v[106:109]
	v_mfma_f32_16x16x32_bf16 v[110:113], v[134:137], v[202:205], v[110:113]
	v_mfma_f32_16x16x32_bf16 v[98:101], v[134:137], v[216:219], v[98:101]
	v_mfma_f32_16x16x32_bf16 v[90:93], v[142:145], v[216:219], v[90:93]
	v_mfma_f32_16x16x32_bf16 v[74:77], v[142:145], v[224:227], v[74:77]
	v_mfma_f32_16x16x32_bf16 v[82:85], v[134:137], v[224:227], v[82:85]
	s_setprio 0
	s_setprio 1
	v_mfma_f32_16x16x32_bf16 v[118:121], v[146:149], v[190:193], 0
	v_mfma_f32_16x16x32_bf16 v[114:117], v[170:173], v[190:193], 0
	v_mfma_f32_16x16x32_bf16 v[94:97], v[170:173], v[198:201], 0
	v_mfma_f32_16x16x32_bf16 v[102:105], v[146:149], v[198:201], 0
	v_mfma_f32_16x16x32_bf16 v[86:89], v[146:149], v[206:209], 0
	v_mfma_f32_16x16x32_bf16 v[78:81], v[170:173], v[206:209], 0
	v_mfma_f32_16x16x32_bf16 v[66:69], v[170:173], v[220:223], 0
	v_mfma_f32_16x16x32_bf16 v[70:73], v[146:149], v[220:223], 0
	v_mfma_f32_16x16x32_bf16 v[118:121], v[150:153], v[194:197], v[118:121]
	v_mfma_f32_16x16x32_bf16 v[114:117], v[180:183], v[194:197], v[114:117]
	v_mfma_f32_16x16x32_bf16 v[94:97], v[180:183], v[202:205], v[94:97]
	v_mfma_f32_16x16x32_bf16 v[102:105], v[150:153], v[202:205], v[102:105]
	v_mfma_f32_16x16x32_bf16 v[86:89], v[150:153], v[216:219], v[86:89]
	v_mfma_f32_16x16x32_bf16 v[78:81], v[180:183], v[216:219], v[78:81]
	v_mfma_f32_16x16x32_bf16 v[66:69], v[180:183], v[224:227], v[66:69]
	v_mfma_f32_16x16x32_bf16 v[70:73], v[150:153], v[224:227], v[70:73]
	s_setprio 0
	s_barrier
	s_add_i32 s51, s36, s23
	s_mov_b32 m0, s51
	ds_read_b128 v[190:193], v179 offset:16384
	ds_read_b128 v[194:197], v179 offset:17408
	ds_read_b128 v[198:201], v179 offset:18432
	ds_read_b128 v[202:205], v179 offset:19456
	ds_read_b128 v[206:209], v179 offset:20480
	ds_read_b128 v[216:219], v179 offset:21504
	ds_read_b128 v[220:223], v179 offset:22528
	ds_read_b128 v[224:227], v179 offset:23552
	global_load_lds_dwordx4 v156, s[16:17]
	s_add_i32 m0, s51, 0x2000
	s_add_u32 s52, s16, 0x160000
	s_addc_u32 s53, s17, 0
	s_add_i32 s51, s37, s23
	global_load_lds_dwordx4 v160, s[16:17]
	s_mov_b32 m0, s51
	s_nop 0
	global_load_lds_dwordx4 v156, s[52:53]
	s_add_i32 m0, s51, 0x2000
	s_nop 0
	global_load_lds_dwordx4 v160, s[52:53]
	s_mov_b32 m0, s24
	s_nop 0
	global_load_lds_dwordx4 v154, s[18:19]
	s_mov_b32 m0, s25
	s_nop 0
	global_load_lds_dwordx4 v158, s[18:19]
	s_waitcnt vmcnt(8)
	s_waitcnt lgkmcnt(0)
	s_barrier
	s_setprio 1
	s_waitcnt lgkmcnt(0)
	v_mfma_f32_16x16x32_bf16 v[62:65], v[130:133], v[190:193], 0
	v_mfma_f32_16x16x32_bf16 v[58:61], v[138:141], v[190:193], 0
	v_mfma_f32_16x16x32_bf16 v[42:45], v[138:141], v[198:201], 0
	v_mfma_f32_16x16x32_bf16 v[50:53], v[130:133], v[198:201], 0
	v_mfma_f32_16x16x32_bf16 v[34:37], v[130:133], v[206:209], 0
	v_mfma_f32_16x16x32_bf16 v[26:29], v[138:141], v[206:209], 0
	v_mfma_f32_16x16x32_bf16 v[10:13], v[138:141], v[220:223], 0
	v_mfma_f32_16x16x32_bf16 v[18:21], v[130:133], v[220:223], 0
	v_mfma_f32_16x16x32_bf16 v[62:65], v[134:137], v[194:197], v[62:65]
	v_mfma_f32_16x16x32_bf16 v[58:61], v[142:145], v[194:197], v[58:61]
	v_mfma_f32_16x16x32_bf16 v[42:45], v[142:145], v[202:205], v[42:45]
	v_mfma_f32_16x16x32_bf16 v[50:53], v[134:137], v[202:205], v[50:53]
	v_mfma_f32_16x16x32_bf16 v[34:37], v[134:137], v[216:219], v[34:37]
	v_mfma_f32_16x16x32_bf16 v[26:29], v[142:145], v[216:219], v[26:29]
	v_mfma_f32_16x16x32_bf16 v[10:13], v[142:145], v[224:227], v[10:13]
	v_mfma_f32_16x16x32_bf16 v[18:21], v[134:137], v[224:227], v[18:21]
	s_setprio 0
	s_setprio 1
	v_mfma_f32_16x16x32_bf16 v[54:57], v[146:149], v[190:193], 0
	v_mfma_f32_16x16x32_bf16 v[46:49], v[170:173], v[190:193], 0
	v_mfma_f32_16x16x32_bf16 v[30:33], v[170:173], v[198:201], 0
	v_mfma_f32_16x16x32_bf16 v[38:41], v[146:149], v[198:201], 0
	v_mfma_f32_16x16x32_bf16 v[22:25], v[146:149], v[206:209], 0
	v_mfma_f32_16x16x32_bf16 v[14:17], v[170:173], v[206:209], 0
	v_mfma_f32_16x16x32_bf16 v[2:5], v[170:173], v[220:223], 0
	v_mfma_f32_16x16x32_bf16 v[6:9], v[146:149], v[220:223], 0
	v_mfma_f32_16x16x32_bf16 v[54:57], v[150:153], v[194:197], v[54:57]
	v_mfma_f32_16x16x32_bf16 v[46:49], v[180:183], v[194:197], v[46:49]
	v_mfma_f32_16x16x32_bf16 v[30:33], v[180:183], v[202:205], v[30:33]
	v_mfma_f32_16x16x32_bf16 v[38:41], v[150:153], v[202:205], v[38:41]
	v_mfma_f32_16x16x32_bf16 v[22:25], v[150:153], v[216:219], v[22:25]
	v_mfma_f32_16x16x32_bf16 v[14:17], v[180:183], v[216:219], v[14:17]
	v_mfma_f32_16x16x32_bf16 v[2:5], v[180:183], v[224:227], v[2:5]
	v_mfma_f32_16x16x32_bf16 v[6:9], v[150:153], v[224:227], v[6:9]
	s_setprio 0
	s_barrier
; #define PG8_STAGE(bufoff, gbase, voff) do { _Pragma("unroll") for (int _i = 0; _i < 2; ++_i) \
;         __builtin_amdgcn_global_load_lds((const unsigned*)((const char*)(gbase) + (voff)[_i]), (PG8_LAS unsigned*)(lds + (bufoff) + ldsw + _i * 8192), 16, 0, 0); } while (0)
; #define PG8_LDA(dst, b, h) do { _Pragma("unroll") for (int m = 0; m < 4; ++m) _Pragma("unroll") for (int k = 0; k < 2; ++k) dst[m][k] = *(const PG8_LAS bf16x8*)(lds + PG8_SA(b, h) + aoff + m * 2048 + k * 1024); } while (0)
; #define PG8_LDB(dst, b, h) do { _Pragma("unroll") for (int n = 0; n < 2; ++n) _Pragma("unroll") for (int k = 0; k < 2; ++k) dst[n][k] = *(const PG8_LAS bf16x8*)(lds + PG8_SB(b, h) + boff + n * 2048 + k * 1024); } while (0)
; #define PG8_WAIT_V(n) asm volatile("s_waitcnt vmcnt(" #n ")" ::: "memory")
; #define PG8_WAIT_L(n) asm volatile("s_waitcnt lgkmcnt(" #n ")" ::: "memory")
; #define PG8_BAR __builtin_amdgcn_s_barrier()
; #define PG8_SCHED __builtin_amdgcn_sched_barrier(0)
; template <class Epi, class Sched, bool ALIGN_EPI = false, bool SP2 = false>
; __device__ __forceinline__ void gemm_phase(PG8_LAS unsigned char* lds, const Gemm g, const Sched& S, const Epi& E) {
;     ...
;             PG8_LDB(B0, 1, 0); PG8_LDB(B1, 1, 1); PG8_SCHED; PG8_LDA(At, 1, 0); PG8_STAGE(PG8_SA(0, 1), a2 + hstep, voffA);
;             PG8_WAIT_V(8); PG8_WAIT_L(0); PG8_BAR; PG8_MMA(0, 0, At, B0); PG8_MMA(0, 1, At, B1); PG8_BAR; PG8_SCHED;
;             PG8_LDA(At, 1, 1); PG8_STAGE(PG8_SB(1, 0), b3, voffB); PG8_STAGE(PG8_SB(1, 1), b3 + hstep, voffB); PG8_STAGE(PG8_SA(1, 0), a3, voffA);
;             PG8_WAIT_V(8); PG8_WAIT_L(0); PG8_BAR; PG8_MMA(1, 0, At, B0); PG8_MMA(1, 1, At, B1); PG8_BAR; PG8_SCHED;
	s_add_i32 s51, 0, 0x18000
	s_add_i32 s52, 0, 0x1c000
	ds_read_b128 v[130:133], v248
	ds_read_b128 v[134:137], v248 offset:1024
	ds_read_b128 v[138:141], v248 offset:2048
	ds_read_b128 v[142:145], v248 offset:3072
	ds_read_b128 v[146:149], v249
	ds_read_b128 v[150:153], v249 offset:1024
	ds_read_b128 v[170:173], v249 offset:2048
	ds_read_b128 v[180:183], v249 offset:3072
	s_add_u32 s18, s18, 0x160000
	s_addc_u32 s19, s19, 0
	s_mov_b32 m0, s26
	ds_read_b128 v[190:193], v179 offset:32768
	ds_read_b128 v[194:197], v179 offset:33792
	ds_read_b128 v[198:201], v179 offset:34816
	ds_read_b128 v[202:205], v179 offset:35840
	ds_read_b128 v[206:209], v179 offset:36864
	ds_read_b128 v[216:219], v179 offset:37888
	ds_read_b128 v[220:223], v179 offset:38912
	ds_read_b128 v[224:227], v179 offset:39936
	global_load_lds_dwordx4 v154, s[18:19]
	s_mov_b32 m0, s27
	s_nop 0
	global_load_lds_dwordx4 v158, s[18:19]
	s_waitcnt vmcnt(8)
	s_waitcnt lgkmcnt(0)
	s_barrier
	s_setprio 1
	s_waitcnt lgkmcnt(0)
	v_mfma_f32_16x16x32_bf16 v[126:129], v[130:133], v[190:193], v[126:129]
	v_mfma_f32_16x16x32_bf16 v[122:125], v[138:141], v[190:193], v[122:125]
	v_mfma_f32_16x16x32_bf16 v[106:109], v[138:141], v[198:201], v[106:109]
	v_mfma_f32_16x16x32_bf16 v[110:113], v[130:133], v[198:201], v[110:113]
	v_mfma_f32_16x16x32_bf16 v[98:101], v[130:133], v[206:209], v[98:101]
	v_mfma_f32_16x16x32_bf16 v[90:93], v[138:141], v[206:209], v[90:93]
	v_mfma_f32_16x16x32_bf16 v[74:77], v[138:141], v[220:223], v[74:77]
	v_mfma_f32_16x16x32_bf16 v[82:85], v[130:133], v[220:223], v[82:85]
	v_mfma_f32_16x16x32_bf16 v[126:129], v[134:137], v[194:197], v[126:129]
	v_mfma_f32_16x16x32_bf16 v[122:125], v[142:145], v[194:197], v[122:125]
	v_mfma_f32_16x16x32_bf16 v[106:109], v[142:145], v[202:205], v[106:109]
	v_mfma_f32_16x16x32_bf16 v[110:113], v[134:137], v[202:205], v[110:113]
	v_mfma_f32_16x16x32_bf16 v[98:101], v[134:137], v[216:219], v[98:101]
	v_mfma_f32_16x16x32_bf16 v[90:93], v[142:145], v[216:219], v[90:93]
	v_mfma_f32_16x16x32_bf16 v[74:77], v[142:145], v[224:227], v[74:77]
	v_mfma_f32_16x16x32_bf16 v[82:85], v[134:137], v[224:227], v[82:85]
	s_setprio 0
	s_setprio 1
	v_mfma_f32_16x16x32_bf16 v[118:121], v[146:149], v[190:193], v[118:121]
	v_mfma_f32_16x16x32_bf16 v[114:117], v[170:173], v[190:193], v[114:117]
	v_mfma_f32_16x16x32_bf16 v[94:97], v[170:173], v[198:201], v[94:97]
	v_mfma_f32_16x16x32_bf16 v[102:105], v[146:149], v[198:201], v[102:105]
	v_mfma_f32_16x16x32_bf16 v[86:89], v[146:149], v[206:209], v[86:89]
	v_mfma_f32_16x16x32_bf16 v[78:81], v[170:173], v[206:209], v[78:81]
	v_mfma_f32_16x16x32_bf16 v[66:69], v[170:173], v[220:223], v[66:69]
	v_mfma_f32_16x16x32_bf16 v[70:73], v[146:149], v[220:223], v[70:73]
	v_mfma_f32_16x16x32_bf16 v[118:121], v[150:153], v[194:197], v[118:121]
	v_mfma_f32_16x16x32_bf16 v[114:117], v[180:183], v[194:197], v[114:117]
	v_mfma_f32_16x16x32_bf16 v[94:97], v[180:183], v[202:205], v[94:97]
	v_mfma_f32_16x16x32_bf16 v[102:105], v[150:153], v[202:205], v[102:105]
	v_mfma_f32_16x16x32_bf16 v[86:89], v[150:153], v[216:219], v[86:89]
	v_mfma_f32_16x16x32_bf16 v[78:81], v[180:183], v[216:219], v[78:81]
	v_mfma_f32_16x16x32_bf16 v[66:69], v[180:183], v[224:227], v[66:69]
	v_mfma_f32_16x16x32_bf16 v[70:73], v[150:153], v[224:227], v[70:73]
	s_setprio 0
	s_barrier
	s_add_u32 s98, s16, 0x80
	s_addc_u32 s99, s17, 0
	s_add_u32 s100, s18, 0xffea0080
	s_addc_u32 s101, s19, -1
	s_add_i32 s18, s51, s23
	s_mov_b32 m0, s18
	ds_read_b128 v[190:193], v179 offset:49152
	ds_read_b128 v[194:197], v179 offset:50176
	ds_read_b128 v[198:201], v179 offset:51200
	ds_read_b128 v[202:205], v179 offset:52224
	ds_read_b128 v[206:209], v179 offset:53248
	ds_read_b128 v[216:219], v179 offset:54272
	ds_read_b128 v[220:223], v179 offset:55296
	ds_read_b128 v[224:227], v179 offset:56320
	global_load_lds_dwordx4 v156, s[98:99]
	s_add_i32 m0, s18, 0x2000
	s_add_u32 s16, s16, 0x160080
	s_addc_u32 s17, s17, 0
	s_add_i32 s18, s52, s23
	global_load_lds_dwordx4 v160, s[98:99]
	s_mov_b32 m0, s18
	s_nop 0
	global_load_lds_dwordx4 v156, s[16:17]
	s_add_i32 m0, s18, 0x2000
	s_nop 0
	global_load_lds_dwordx4 v160, s[16:17]
	s_mov_b32 m0, s33
	s_nop 0
	global_load_lds_dwordx4 v154, s[100:101]
	s_mov_b32 m0, s34
	s_nop 0
	global_load_lds_dwordx4 v158, s[100:101]
	s_waitcnt vmcnt(8)
	s_waitcnt lgkmcnt(0)
	s_barrier
	s_setprio 1
	s_waitcnt lgkmcnt(0)
	v_mfma_f32_16x16x32_bf16 v[62:65], v[130:133], v[190:193], v[62:65]
	v_mfma_f32_16x16x32_bf16 v[58:61], v[138:141], v[190:193], v[58:61]
	v_mfma_f32_16x16x32_bf16 v[42:45], v[138:141], v[198:201], v[42:45]
	v_mfma_f32_16x16x32_bf16 v[50:53], v[130:133], v[198:201], v[50:53]
	v_mfma_f32_16x16x32_bf16 v[34:37], v[130:133], v[206:209], v[34:37]
	v_mfma_f32_16x16x32_bf16 v[26:29], v[138:141], v[206:209], v[26:29]
	v_mfma_f32_16x16x32_bf16 v[10:13], v[138:141], v[220:223], v[10:13]
	v_mfma_f32_16x16x32_bf16 v[18:21], v[130:133], v[220:223], v[18:21]
	v_mfma_f32_16x16x32_bf16 v[62:65], v[134:137], v[194:197], v[62:65]
	v_mfma_f32_16x16x32_bf16 v[58:61], v[142:145], v[194:197], v[58:61]
	v_mfma_f32_16x16x32_bf16 v[42:45], v[142:145], v[202:205], v[42:45]
	v_mfma_f32_16x16x32_bf16 v[50:53], v[134:137], v[202:205], v[50:53]
	v_mfma_f32_16x16x32_bf16 v[34:37], v[134:137], v[216:219], v[34:37]
	v_mfma_f32_16x16x32_bf16 v[26:29], v[142:145], v[216:219], v[26:29]
	v_mfma_f32_16x16x32_bf16 v[10:13], v[142:145], v[224:227], v[10:13]
	v_mfma_f32_16x16x32_bf16 v[18:21], v[134:137], v[224:227], v[18:21]
	s_setprio 0
	s_setprio 1
	v_mfma_f32_16x16x32_bf16 v[54:57], v[146:149], v[190:193], v[54:57]
	v_mfma_f32_16x16x32_bf16 v[46:49], v[170:173], v[190:193], v[46:49]
	v_mfma_f32_16x16x32_bf16 v[30:33], v[170:173], v[198:201], v[30:33]
	v_mfma_f32_16x16x32_bf16 v[38:41], v[146:149], v[198:201], v[38:41]
	v_mfma_f32_16x16x32_bf16 v[22:25], v[146:149], v[206:209], v[22:25]
	v_mfma_f32_16x16x32_bf16 v[14:17], v[170:173], v[206:209], v[14:17]
	v_mfma_f32_16x16x32_bf16 v[2:5], v[170:173], v[220:223], v[2:5]
	v_mfma_f32_16x16x32_bf16 v[6:9], v[146:149], v[220:223], v[6:9]
	v_mfma_f32_16x16x32_bf16 v[54:57], v[150:153], v[194:197], v[54:57]
	v_mfma_f32_16x16x32_bf16 v[46:49], v[180:183], v[194:197], v[46:49]
	v_mfma_f32_16x16x32_bf16 v[30:33], v[180:183], v[202:205], v[30:33]
	v_mfma_f32_16x16x32_bf16 v[38:41], v[150:153], v[202:205], v[38:41]
	v_mfma_f32_16x16x32_bf16 v[22:25], v[150:153], v[216:219], v[22:25]
	v_mfma_f32_16x16x32_bf16 v[14:17], v[180:183], v[216:219], v[14:17]
	v_mfma_f32_16x16x32_bf16 v[2:5], v[180:183], v[224:227], v[2:5]
	v_mfma_f32_16x16x32_bf16 v[6:9], v[150:153], v[224:227], v[6:9]
	s_setprio 0
	s_barrier
	s_add_i32 s50, s50, 2
	s_add_u32 s14, s14, 0x100
	s_addc_u32 s15, s15, 0
	s_add_u32 s48, s48, 0x100
	s_addc_u32 s49, s49, 0
	s_cmpk_gt_u32 s50, 0x55
; #define PG8_STAGE(bufoff, gbase, voff) do { _Pragma("unroll") for (int _i = 0; _i < 2; ++_i) \
;         __builtin_amdgcn_global_load_lds((const unsigned*)((const char*)(gbase) + (voff)[_i]), (PG8_LAS unsigned*)(lds + (bufoff) + ldsw + _i * 8192), 16, 0, 0); } while (0)
; #define PG8_LDA(dst, b, h) do { _Pragma("unroll") for (int m = 0; m < 4; ++m) _Pragma("unroll") for (int k = 0; k < 2; ++k) dst[m][k] = *(const PG8_LAS bf16x8*)(lds + PG8_SA(b, h) + aoff + m * 2048 + k * 1024); } while (0)
; #define PG8_LDB(dst, b, h) do { _Pragma("unroll") for (int n = 0; n < 2; ++n) _Pragma("unroll") for (int k = 0; k < 2; ++k) dst[n][k] = *(const PG8_LAS bf16x8*)(lds + PG8_SB(b, h) + boff + n * 2048 + k * 1024); } while (0)
; #define PG8_WAIT_V(n) asm volatile("s_waitcnt vmcnt(" #n ")" ::: "memory")
; #define PG8_WAIT_L(n) asm volatile("s_waitcnt lgkmcnt(" #n ")" ::: "memory")
; #define PG8_BAR __builtin_amdgcn_s_barrier()
; #define PG8_SCHED __builtin_amdgcn_sched_barrier(0)
; template <class Epi, class Sched, bool ALIGN_EPI = false, bool SP2 = false>
; __device__ __forceinline__ void gemm_phase(PG8_LAS unsigned char* lds, const Gemm g, const Sched& S, const Epi& E) {
;     ...
;             PG8_LDB(B0, 0, 0); PG8_LDB(B1, 0, 1); PG8_SCHED; PG8_LDA(At, 0, 0); PG8_STAGE(PG8_SA(1, 1), a1 + hstep, voffA);
;             PG8_WAIT_V(8); PG8_WAIT_L(0); PG8_BAR; PG8_MMA(0, 0, At, B0); PG8_MMA(0, 1, At, B1); PG8_BAR; PG8_SCHED;
;             PG8_LDA(At, 0, 1); PG8_STAGE(PG8_SB(0, 0), b2, voffB); PG8_STAGE(PG8_SB(0, 1), b2 + hstep, voffB); PG8_STAGE(PG8_SA(0, 0), a2, voffA);
;             PG8_WAIT_V(8); PG8_WAIT_L(0); PG8_BAR; PG8_MMA(1, 0, At, B0); PG8_MMA(1, 1, At, B1); PG8_BAR; PG8_SCHED;
.LBB0_951:
	ds_read_b128 v[130:133], v177
	ds_read_b128 v[134:137], v177 offset:1024
	ds_read_b128 v[138:141], v177 offset:2048
	ds_read_b128 v[142:145], v177 offset:3072
	ds_read_b128 v[146:149], v178
	ds_read_b128 v[150:153], v178 offset:1024
	ds_read_b128 v[170:173], v178 offset:2048
	ds_read_b128 v[180:183], v178 offset:3072
	s_add_u32 s16, s14, 0xffea0080
	s_addc_u32 s17, s15, -1
	s_cmpk_eq_i32 s50, 0x54
	s_cselect_b32 s19, s5, s17
	s_cselect_b32 s18, s4, s16
	s_cselect_b32 s17, s13, s49
	s_cselect_b32 s16, s12, s48
	s_add_i32 m0, s24, 0xc000
	ds_read_b128 v[190:193], v179
	ds_read_b128 v[194:197], v179 offset:1024
	ds_read_b128 v[198:201], v179 offset:2048
	ds_read_b128 v[202:205], v179 offset:3072
	ds_read_b128 v[206:209], v179 offset:4096
	ds_read_b128 v[216:219], v179 offset:5120
	ds_read_b128 v[220:223], v179 offset:6144
	ds_read_b128 v[224:227], v179 offset:7168
	global_load_lds_dwordx4 v162, s[14:15]
	s_add_i32 m0, s24, 0xe000
	s_nop 0
	global_load_lds_dwordx4 v164, s[14:15]
	s_waitcnt vmcnt(8)
	s_waitcnt lgkmcnt(0)
	s_barrier
	s_setprio 1
	s_waitcnt lgkmcnt(0)
	v_mfma_f32_16x16x32_bf16 v[126:129], v[130:133], v[190:193], v[126:129]
	v_mfma_f32_16x16x32_bf16 v[122:125], v[138:141], v[190:193], v[122:125]
	v_mfma_f32_16x16x32_bf16 v[106:109], v[138:141], v[198:201], v[106:109]
	v_mfma_f32_16x16x32_bf16 v[110:113], v[130:133], v[198:201], v[110:113]
	v_mfma_f32_16x16x32_bf16 v[98:101], v[130:133], v[206:209], v[98:101]
	v_mfma_f32_16x16x32_bf16 v[90:93], v[138:141], v[206:209], v[90:93]
	v_mfma_f32_16x16x32_bf16 v[74:77], v[138:141], v[220:223], v[74:77]
	v_mfma_f32_16x16x32_bf16 v[82:85], v[130:133], v[220:223], v[82:85]
	v_mfma_f32_16x16x32_bf16 v[126:129], v[134:137], v[194:197], v[126:129]
	v_mfma_f32_16x16x32_bf16 v[122:125], v[142:145], v[194:197], v[122:125]
	v_mfma_f32_16x16x32_bf16 v[106:109], v[142:145], v[202:205], v[106:109]
	v_mfma_f32_16x16x32_bf16 v[110:113], v[134:137], v[202:205], v[110:113]
	v_mfma_f32_16x16x32_bf16 v[98:101], v[134:137], v[216:219], v[98:101]
	v_mfma_f32_16x16x32_bf16 v[90:93], v[142:145], v[216:219], v[90:93]
	v_mfma_f32_16x16x32_bf16 v[74:77], v[142:145], v[224:227], v[74:77]
	v_mfma_f32_16x16x32_bf16 v[82:85], v[134:137], v[224:227], v[82:85]
	s_setprio 0
	s_setprio 1
	v_mfma_f32_16x16x32_bf16 v[118:121], v[146:149], v[190:193], v[118:121]
	v_mfma_f32_16x16x32_bf16 v[114:117], v[170:173], v[190:193], v[114:117]
	v_mfma_f32_16x16x32_bf16 v[94:97], v[170:173], v[198:201], v[94:97]
	v_mfma_f32_16x16x32_bf16 v[102:105], v[146:149], v[198:201], v[102:105]
	v_mfma_f32_16x16x32_bf16 v[86:89], v[146:149], v[206:209], v[86:89]
	v_mfma_f32_16x16x32_bf16 v[78:81], v[170:173], v[206:209], v[78:81]
	v_mfma_f32_16x16x32_bf16 v[66:69], v[170:173], v[220:223], v[66:69]
	v_mfma_f32_16x16x32_bf16 v[70:73], v[146:149], v[220:223], v[70:73]
	v_mfma_f32_16x16x32_bf16 v[118:121], v[150:153], v[194:197], v[118:121]
	v_mfma_f32_16x16x32_bf16 v[114:117], v[180:183], v[194:197], v[114:117]
	v_mfma_f32_16x16x32_bf16 v[94:97], v[180:183], v[202:205], v[94:97]
	v_mfma_f32_16x16x32_bf16 v[102:105], v[150:153], v[202:205], v[102:105]
	v_mfma_f32_16x16x32_bf16 v[86:89], v[150:153], v[216:219], v[86:89]
	v_mfma_f32_16x16x32_bf16 v[78:81], v[180:183], v[216:219], v[78:81]
	v_mfma_f32_16x16x32_bf16 v[66:69], v[180:183], v[224:227], v[66:69]
	v_mfma_f32_16x16x32_bf16 v[70:73], v[150:153], v[224:227], v[70:73]
	s_setprio 0
	s_barrier
	s_add_i32 s51, s36, s23
	s_mov_b32 m0, s51
	ds_read_b128 v[190:193], v179 offset:16384
	ds_read_b128 v[194:197], v179 offset:17408
	ds_read_b128 v[198:201], v179 offset:18432
	ds_read_b128 v[202:205], v179 offset:19456
	ds_read_b128 v[206:209], v179 offset:20480
	ds_read_b128 v[216:219], v179 offset:21504
	ds_read_b128 v[220:223], v179 offset:22528
	ds_read_b128 v[224:227], v179 offset:23552
	global_load_lds_dwordx4 v156, s[16:17]
	s_add_i32 m0, s51, 0x2000
	s_add_u32 s52, s16, 0x160000
	s_addc_u32 s53, s17, 0
	s_add_i32 s51, s37, s23
	global_load_lds_dwordx4 v160, s[16:17]
	s_mov_b32 m0, s51
	s_nop 0
	global_load_lds_dwordx4 v156, s[52:53]
	s_add_i32 m0, s51, 0x2000
	s_nop 0
	global_load_lds_dwordx4 v160, s[52:53]
	s_mov_b32 m0, s24
	s_nop 0
	global_load_lds_dwordx4 v154, s[18:19]
	s_mov_b32 m0, s25
	s_nop 0
	global_load_lds_dwordx4 v158, s[18:19]
	s_waitcnt vmcnt(8)
	s_waitcnt lgkmcnt(0)
	s_barrier
	s_setprio 1
	s_waitcnt lgkmcnt(0)
	v_mfma_f32_16x16x32_bf16 v[62:65], v[130:133], v[190:193], v[62:65]
	v_mfma_f32_16x16x32_bf16 v[58:61], v[138:141], v[190:193], v[58:61]
	v_mfma_f32_16x16x32_bf16 v[42:45], v[138:141], v[198:201], v[42:45]
	v_mfma_f32_16x16x32_bf16 v[50:53], v[130:133], v[198:201], v[50:53]
	v_mfma_f32_16x16x32_bf16 v[34:37], v[130:133], v[206:209], v[34:37]
	v_mfma_f32_16x16x32_bf16 v[26:29], v[138:141], v[206:209], v[26:29]
	v_mfma_f32_16x16x32_bf16 v[10:13], v[138:141], v[220:223], v[10:13]
	v_mfma_f32_16x16x32_bf16 v[18:21], v[130:133], v[220:223], v[18:21]
	v_mfma_f32_16x16x32_bf16 v[62:65], v[134:137], v[194:197], v[62:65]
	v_mfma_f32_16x16x32_bf16 v[58:61], v[142:145], v[194:197], v[58:61]
	v_mfma_f32_16x16x32_bf16 v[42:45], v[142:145], v[202:205], v[42:45]
	v_mfma_f32_16x16x32_bf16 v[50:53], v[134:137], v[202:205], v[50:53]
	v_mfma_f32_16x16x32_bf16 v[34:37], v[134:137], v[216:219], v[34:37]
	v_mfma_f32_16x16x32_bf16 v[26:29], v[142:145], v[216:219], v[26:29]
	v_mfma_f32_16x16x32_bf16 v[10:13], v[142:145], v[224:227], v[10:13]
	v_mfma_f32_16x16x32_bf16 v[18:21], v[134:137], v[224:227], v[18:21]
	s_setprio 0
	s_setprio 1
	v_mfma_f32_16x16x32_bf16 v[54:57], v[146:149], v[190:193], v[54:57]
	v_mfma_f32_16x16x32_bf16 v[46:49], v[170:173], v[190:193], v[46:49]
	v_mfma_f32_16x16x32_bf16 v[30:33], v[170:173], v[198:201], v[30:33]
	v_mfma_f32_16x16x32_bf16 v[38:41], v[146:149], v[198:201], v[38:41]
	v_mfma_f32_16x16x32_bf16 v[22:25], v[146:149], v[206:209], v[22:25]
	v_mfma_f32_16x16x32_bf16 v[14:17], v[170:173], v[206:209], v[14:17]
	v_mfma_f32_16x16x32_bf16 v[2:5], v[170:173], v[220:223], v[2:5]
	v_mfma_f32_16x16x32_bf16 v[6:9], v[146:149], v[220:223], v[6:9]
	v_mfma_f32_16x16x32_bf16 v[54:57], v[150:153], v[194:197], v[54:57]
	v_mfma_f32_16x16x32_bf16 v[46:49], v[180:183], v[194:197], v[46:49]
	v_mfma_f32_16x16x32_bf16 v[30:33], v[180:183], v[202:205], v[30:33]
	v_mfma_f32_16x16x32_bf16 v[38:41], v[150:153], v[202:205], v[38:41]
	v_mfma_f32_16x16x32_bf16 v[22:25], v[150:153], v[216:219], v[22:25]
	v_mfma_f32_16x16x32_bf16 v[14:17], v[180:183], v[216:219], v[14:17]
	v_mfma_f32_16x16x32_bf16 v[2:5], v[180:183], v[224:227], v[2:5]
	v_mfma_f32_16x16x32_bf16 v[6:9], v[150:153], v[224:227], v[6:9]
	s_setprio 0
	s_barrier
; #define PG8_STAGE(bufoff, gbase, voff) do { _Pragma("unroll") for (int _i = 0; _i < 2; ++_i) \
;         __builtin_amdgcn_global_load_lds((const unsigned*)((const char*)(gbase) + (voff)[_i]), (PG8_LAS unsigned*)(lds + (bufoff) + ldsw + _i * 8192), 16, 0, 0); } while (0)
; #define PG8_LDA(dst, b, h) do { _Pragma("unroll") for (int m = 0; m < 4; ++m) _Pragma("unroll") for (int k = 0; k < 2; ++k) dst[m][k] = *(const PG8_LAS bf16x8*)(lds + PG8_SA(b, h) + aoff + m * 2048 + k * 1024); } while (0)
; #define PG8_LDB(dst, b, h) do { _Pragma("unroll") for (int n = 0; n < 2; ++n) _Pragma("unroll") for (int k = 0; k < 2; ++k) dst[n][k] = *(const PG8_LAS bf16x8*)(lds + PG8_SB(b, h) + boff + n * 2048 + k * 1024); } while (0)
; #define PG8_WAIT_V(n) asm volatile("s_waitcnt vmcnt(" #n ")" ::: "memory")
; #define PG8_WAIT_L(n) asm volatile("s_waitcnt lgkmcnt(" #n ")" ::: "memory")
; #define PG8_BAR __builtin_amdgcn_s_barrier()
; #define PG8_SCHED __builtin_amdgcn_sched_barrier(0)
; template <class Epi, class Sched, bool ALIGN_EPI = false, bool SP2 = false>
; __device__ __forceinline__ void gemm_phase(PG8_LAS unsigned char* lds, const Gemm g, const Sched& S, const Epi& E) {
;     ...
;             PG8_LDB(B0, 1, 0); PG8_LDB(B1, 1, 1); PG8_SCHED; PG8_LDA(At, 1, 0); PG8_STAGE(PG8_SA(0, 1), a2 + hstep, voffA);
;             PG8_WAIT_V(8); PG8_WAIT_L(0); PG8_BAR; PG8_MMA(0, 0, At, B0); PG8_MMA(0, 1, At, B1); PG8_BAR; PG8_SCHED;
;             PG8_LDA(At, 1, 1); PG8_STAGE(PG8_SB(1, 0), b3, voffB); PG8_STAGE(PG8_SB(1, 1), b3 + hstep, voffB); PG8_STAGE(PG8_SA(1, 0), a3, voffA);
;             PG8_WAIT_V(8); PG8_WAIT_L(0); PG8_BAR; PG8_MMA(1, 0, At, B0); PG8_MMA(1, 1, At, B1); PG8_BAR; PG8_SCHED;
	s_add_i32 s51, 0, 0x18000
	s_add_i32 s52, 0, 0x1c000
	ds_read_b128 v[130:133], v248
	ds_read_b128 v[134:137], v248 offset:1024
	ds_read_b128 v[138:141], v248 offset:2048
	ds_read_b128 v[142:145], v248 offset:3072
	ds_read_b128 v[146:149], v249
	ds_read_b128 v[150:153], v249 offset:1024
	ds_read_b128 v[170:173], v249 offset:2048
	ds_read_b128 v[180:183], v249 offset:3072
	s_add_u32 s18, s18, 0x160000
	s_addc_u32 s19, s19, 0
	s_mov_b32 m0, s26
	ds_read_b128 v[190:193], v179 offset:32768
	ds_read_b128 v[194:197], v179 offset:33792
	ds_read_b128 v[198:201], v179 offset:34816
	ds_read_b128 v[202:205], v179 offset:35840
	ds_read_b128 v[206:209], v179 offset:36864
	ds_read_b128 v[216:219], v179 offset:37888
	ds_read_b128 v[220:223], v179 offset:38912
	ds_read_b128 v[224:227], v179 offset:39936
	global_load_lds_dwordx4 v154, s[18:19]
	s_mov_b32 m0, s27
	s_nop 0
	global_load_lds_dwordx4 v158, s[18:19]
	s_waitcnt vmcnt(8)
	s_waitcnt lgkmcnt(0)
	s_barrier
	s_setprio 1
	s_waitcnt lgkmcnt(0)
	v_mfma_f32_16x16x32_bf16 v[126:129], v[130:133], v[190:193], v[126:129]
	v_mfma_f32_16x16x32_bf16 v[122:125], v[138:141], v[190:193], v[122:125]
	v_mfma_f32_16x16x32_bf16 v[106:109], v[138:141], v[198:201], v[106:109]
	v_mfma_f32_16x16x32_bf16 v[110:113], v[130:133], v[198:201], v[110:113]
	v_mfma_f32_16x16x32_bf16 v[98:101], v[130:133], v[206:209], v[98:101]
	v_mfma_f32_16x16x32_bf16 v[90:93], v[138:141], v[206:209], v[90:93]
	v_mfma_f32_16x16x32_bf16 v[74:77], v[138:141], v[220:223], v[74:77]
	v_mfma_f32_16x16x32_bf16 v[82:85], v[130:133], v[220:223], v[82:85]
	v_mfma_f32_16x16x32_bf16 v[126:129], v[134:137], v[194:197], v[126:129]
	v_mfma_f32_16x16x32_bf16 v[122:125], v[142:145], v[194:197], v[122:125]
	v_mfma_f32_16x16x32_bf16 v[106:109], v[142:145], v[202:205], v[106:109]
	v_mfma_f32_16x16x32_bf16 v[110:113], v[134:137], v[202:205], v[110:113]
	v_mfma_f32_16x16x32_bf16 v[98:101], v[134:137], v[216:219], v[98:101]
	v_mfma_f32_16x16x32_bf16 v[90:93], v[142:145], v[216:219], v[90:93]
	v_mfma_f32_16x16x32_bf16 v[74:77], v[142:145], v[224:227], v[74:77]
	v_mfma_f32_16x16x32_bf16 v[82:85], v[134:137], v[224:227], v[82:85]
	s_setprio 0
	s_setprio 1
	v_mfma_f32_16x16x32_bf16 v[118:121], v[146:149], v[190:193], v[118:121]
	v_mfma_f32_16x16x32_bf16 v[114:117], v[170:173], v[190:193], v[114:117]
	v_mfma_f32_16x16x32_bf16 v[94:97], v[170:173], v[198:201], v[94:97]
	v_mfma_f32_16x16x32_bf16 v[102:105], v[146:149], v[198:201], v[102:105]
	v_mfma_f32_16x16x32_bf16 v[86:89], v[146:149], v[206:209], v[86:89]
	v_mfma_f32_16x16x32_bf16 v[78:81], v[170:173], v[206:209], v[78:81]
	v_mfma_f32_16x16x32_bf16 v[66:69], v[170:173], v[220:223], v[66:69]
	v_mfma_f32_16x16x32_bf16 v[70:73], v[146:149], v[220:223], v[70:73]
	v_mfma_f32_16x16x32_bf16 v[118:121], v[150:153], v[194:197], v[118:121]
	v_mfma_f32_16x16x32_bf16 v[114:117], v[180:183], v[194:197], v[114:117]
	v_mfma_f32_16x16x32_bf16 v[94:97], v[180:183], v[202:205], v[94:97]
	v_mfma_f32_16x16x32_bf16 v[102:105], v[150:153], v[202:205], v[102:105]
	v_mfma_f32_16x16x32_bf16 v[86:89], v[150:153], v[216:219], v[86:89]
	v_mfma_f32_16x16x32_bf16 v[78:81], v[180:183], v[216:219], v[78:81]
	v_mfma_f32_16x16x32_bf16 v[66:69], v[180:183], v[224:227], v[66:69]
	v_mfma_f32_16x16x32_bf16 v[70:73], v[150:153], v[224:227], v[70:73]
	s_setprio 0
	s_barrier
	s_add_u32 s98, s16, 0x80
	s_addc_u32 s99, s17, 0
	s_add_u32 s100, s18, 0xffea0080
	s_addc_u32 s101, s19, -1
	s_add_i32 s18, s51, s23
	s_mov_b32 m0, s18
	ds_read_b128 v[190:193], v179 offset:49152
	ds_read_b128 v[194:197], v179 offset:50176
	ds_read_b128 v[198:201], v179 offset:51200
	ds_read_b128 v[202:205], v179 offset:52224
	ds_read_b128 v[206:209], v179 offset:53248
	ds_read_b128 v[216:219], v179 offset:54272
	ds_read_b128 v[220:223], v179 offset:55296
	ds_read_b128 v[224:227], v179 offset:56320
	global_load_lds_dwordx4 v156, s[98:99]
	s_add_i32 m0, s18, 0x2000
	s_add_u32 s16, s16, 0x160080
	s_addc_u32 s17, s17, 0
	s_add_i32 s18, s52, s23
	global_load_lds_dwordx4 v160, s[98:99]
	s_mov_b32 m0, s18
	s_nop 0
	global_load_lds_dwordx4 v156, s[16:17]
	s_add_i32 m0, s18, 0x2000
	s_nop 0
	global_load_lds_dwordx4 v160, s[16:17]
	s_mov_b32 m0, s33
	s_nop 0
	global_load_lds_dwordx4 v154, s[100:101]
	s_mov_b32 m0, s34
	s_nop 0
	global_load_lds_dwordx4 v158, s[100:101]
	s_waitcnt vmcnt(8)
	s_waitcnt lgkmcnt(0)
	s_barrier
	s_setprio 1
	s_waitcnt lgkmcnt(0)
	v_mfma_f32_16x16x32_bf16 v[62:65], v[130:133], v[190:193], v[62:65]
	v_mfma_f32_16x16x32_bf16 v[58:61], v[138:141], v[190:193], v[58:61]
	v_mfma_f32_16x16x32_bf16 v[42:45], v[138:141], v[198:201], v[42:45]
	v_mfma_f32_16x16x32_bf16 v[50:53], v[130:133], v[198:201], v[50:53]
	v_mfma_f32_16x16x32_bf16 v[34:37], v[130:133], v[206:209], v[34:37]
	v_mfma_f32_16x16x32_bf16 v[26:29], v[138:141], v[206:209], v[26:29]
	v_mfma_f32_16x16x32_bf16 v[10:13], v[138:141], v[220:223], v[10:13]
	v_mfma_f32_16x16x32_bf16 v[18:21], v[130:133], v[220:223], v[18:21]
	v_mfma_f32_16x16x32_bf16 v[62:65], v[134:137], v[194:197], v[62:65]
	v_mfma_f32_16x16x32_bf16 v[58:61], v[142:145], v[194:197], v[58:61]
	v_mfma_f32_16x16x32_bf16 v[42:45], v[142:145], v[202:205], v[42:45]
	v_mfma_f32_16x16x32_bf16 v[50:53], v[134:137], v[202:205], v[50:53]
	v_mfma_f32_16x16x32_bf16 v[34:37], v[134:137], v[216:219], v[34:37]
	v_mfma_f32_16x16x32_bf16 v[26:29], v[142:145], v[216:219], v[26:29]
	v_mfma_f32_16x16x32_bf16 v[10:13], v[142:145], v[224:227], v[10:13]
	v_mfma_f32_16x16x32_bf16 v[18:21], v[134:137], v[224:227], v[18:21]
	s_setprio 0
	s_setprio 1
	v_mfma_f32_16x16x32_bf16 v[54:57], v[146:149], v[190:193], v[54:57]
	v_mfma_f32_16x16x32_bf16 v[46:49], v[170:173], v[190:193], v[46:49]
	v_mfma_f32_16x16x32_bf16 v[30:33], v[170:173], v[198:201], v[30:33]
	v_mfma_f32_16x16x32_bf16 v[38:41], v[146:149], v[198:201], v[38:41]
	v_mfma_f32_16x16x32_bf16 v[22:25], v[146:149], v[206:209], v[22:25]
	v_mfma_f32_16x16x32_bf16 v[14:17], v[170:173], v[206:209], v[14:17]
	v_mfma_f32_16x16x32_bf16 v[2:5], v[170:173], v[220:223], v[2:5]
	v_mfma_f32_16x16x32_bf16 v[6:9], v[146:149], v[220:223], v[6:9]
	v_mfma_f32_16x16x32_bf16 v[54:57], v[150:153], v[194:197], v[54:57]
	v_mfma_f32_16x16x32_bf16 v[46:49], v[180:183], v[194:197], v[46:49]
	v_mfma_f32_16x16x32_bf16 v[30:33], v[180:183], v[202:205], v[30:33]
	v_mfma_f32_16x16x32_bf16 v[38:41], v[150:153], v[202:205], v[38:41]
	v_mfma_f32_16x16x32_bf16 v[22:25], v[150:153], v[216:219], v[22:25]
	v_mfma_f32_16x16x32_bf16 v[14:17], v[180:183], v[216:219], v[14:17]
	v_mfma_f32_16x16x32_bf16 v[2:5], v[180:183], v[224:227], v[2:5]
	v_mfma_f32_16x16x32_bf16 v[6:9], v[150:153], v[224:227], v[6:9]
	s_setprio 0
	s_barrier
	s_add_i32 s50, s50, 2
	s_add_u32 s14, s14, 0x100
	s_addc_u32 s15, s15, 0
	s_add_u32 s48, s48, 0x100
	s_addc_u32 s49, s49, 0
	s_cmpk_gt_u32 s50, 0x55
	s_cbranch_scc0 .LBB0_951
	s_and_b64 vcc, exec, s[10:11]
	s_cbranch_vccz .LBB0_954
	s_barrier

; #define PG8_STAGE(bufoff, gbase, voff) do { _Pragma("unroll") for (int _i = 0; _i < 2; ++_i) \
;         __builtin_amdgcn_global_load_lds((const unsigned*)((const char*)(gbase) + (voff)[_i]), (PG8_LAS unsigned*)(lds + (bufoff) + ldsw + _i * 8192), 16, 0, 0); } while (0)
; #define PG8_LDA(dst, b, h) do { _Pragma("unroll") for (int m = 0; m < 4; ++m) _Pragma("unroll") for (int k = 0; k < 2; ++k) dst[m][k] = *(const PG8_LAS bf16x8*)(lds + PG8_SA(b, h) + aoff + m * 2048 + k * 1024); } while (0)
; #define PG8_LDB(dst, b, h) do { _Pragma("unroll") for (int n = 0; n < 2; ++n) _Pragma("unroll") for (int k = 0; k < 2; ++k) dst[n][k] = *(const PG8_LAS bf16x8*)(lds + PG8_SB(b, h) + boff + n * 2048 + k * 1024); } while (0)
; #define PG8_WAIT_V(n) asm volatile("s_waitcnt vmcnt(" #n ")" ::: "memory")
; #define PG8_WAIT_L(n) asm volatile("s_waitcnt lgkmcnt(" #n ")" ::: "memory")
; #define PG8_BAR __builtin_amdgcn_s_barrier()
; #define PG8_SCHED __builtin_amdgcn_sched_barrier(0)
; template <class Epi, class Sched, bool ALIGN_EPI = false, bool SP2 = false>
; __device__ __forceinline__ void gemm_phase(PG8_LAS unsigned char* lds, const Gemm g, const Sched& S, const Epi& E) {
;     ...
;         const bool has_next = S.next(ui + 1, nxt);
;         const char* nA = has_next ? (const char*)g.A + (size_t)nxt.pm * tstep : cA; const char* nB = has_next ? (const char*)g.Bt + (size_t)nxt.pn * tstep : cB;
;         for (int t = 0; t < nt; t += 2) {
;             const bool last = (t == nt - 2);
;             const char* a1 = cA + (size_t)(t + 1) * kstep;
;             const char* a2 = last ? nA : cA + (size_t)(t + 2) * kstep; const char* b2 = last ? nB : cB + (size_t)(t + 2) * kstep;
;             const char* a3 = a2 + kstep; const char* b3 = b2 + kstep;
;             if (last && has_next) S.a_ready(nxt);
;             if constexpr (SP2) {
;             PG8_LDB(B0, 0, 0); PG8_LDB(B1, 0, 1); PG8_SCHED; PG8_LDA(At, 0, 0); PG8_STAGE(PG8_SA(1, 1), a1 + hstep, voffA);
;             PG8_WAIT_V(8); PG8_WAIT_L(0); PG8_BAR; PG8_MMA(0, 0, At, B0); PG8_MMA(0, 1, At, B1); PG8_BAR; PG8_SCHED;
;             PG8_LDA(At, 0, 1); PG8_STAGE(PG8_SB(0, 0), b2, voffB); PG8_STAGE(PG8_SB(0, 1), b2 + hstep, voffB); PG8_STAGE(PG8_SA(0, 0), a2, voffA);
;             PG8_WAIT_V(8); PG8_WAIT_L(0); PG8_BAR; PG8_MMA(1, 0, At, B0); PG8_MMA(1, 1, At, B1); PG8_BAR; PG8_SCHED;
.LBB0_1075:
	s_ashr_i32 s23, s22, 31
	s_lshl_b64 s[24:25], s[22:23], 20
	s_add_u32 s24, s70, s24
	s_addc_u32 s25, s71, s25
	s_and_b64 s[26:27], s[2:3], exec
	s_cselect_b32 s23, s25, s31
	s_cselect_b32 s29, s24, s30
	s_ashr_i32 s21, s20, 31
	s_lshl_b64 s[26:27], s[20:21], 20
	s_add_u32 s26, s33, s26
	s_addc_u32 s27, s38, s27
	s_and_b64 s[36:37], s[2:3], exec
	s_cselect_b32 s21, s27, s35
	s_cselect_b32 s55, s26, s34
	s_add_u32 s30, s30, 0x80080
	s_addc_u32 s31, s31, 0
	s_add_u32 s56, s34, 0x100
	s_addc_u32 s57, s35, 0
	s_mov_b32 s58, -2
	v_add_u32_e32 v248, 0x18000, v155
	v_add_u32_e32 v249, 0x1c000, v155
	ds_read_b128 v[148:151], v157
	ds_read_b128 v[160:163], v157 offset:1024
	ds_read_b128 v[164:167], v157 offset:2048
	ds_read_b128 v[168:171], v157 offset:3072
	ds_read_b128 v[172:175], v158
	ds_read_b128 v[176:179], v158 offset:1024
	ds_read_b128 v[180:183], v158 offset:2048
	ds_read_b128 v[190:193], v158 offset:3072
	s_add_u32 s34, s30, 0xfff80080
	s_addc_u32 s35, s31, -1
	s_cmp_eq_u32 s58, 28
	s_cselect_b32 s37, s23, s35
	s_cselect_b32 s36, s29, s34
	s_cselect_b32 s35, s21, s57
	s_cselect_b32 s34, s55, s56
	s_add_i32 m0, s42, 0xc000
	ds_read_b128 v[194:197], v159
	ds_read_b128 v[198:201], v159 offset:1024
	ds_read_b128 v[202:205], v159 offset:2048
	ds_read_b128 v[206:209], v159 offset:3072
	ds_read_b128 v[216:219], v159 offset:4096
	ds_read_b128 v[220:223], v159 offset:5120
	ds_read_b128 v[224:227], v159 offset:6144
	ds_read_b128 v[228:231], v159 offset:7168
	global_load_lds_dwordx4 v140, s[30:31]
	s_add_i32 m0, s42, 0xe000
	s_nop 0
	global_load_lds_dwordx4 v142, s[30:31]
	s_waitcnt vmcnt(8)
	s_waitcnt lgkmcnt(0)
	s_barrier
	s_setprio 1
	s_waitcnt lgkmcnt(0)
	v_mfma_f32_16x16x32_bf16 v[126:129], v[148:151], v[194:197], 0
	v_mfma_f32_16x16x32_bf16 v[122:125], v[164:167], v[194:197], 0
	v_mfma_f32_16x16x32_bf16 v[110:113], v[164:167], v[202:205], 0
	v_mfma_f32_16x16x32_bf16 v[118:121], v[148:151], v[202:205], 0
	v_mfma_f32_16x16x32_bf16 v[102:105], v[148:151], v[216:219], 0
	v_mfma_f32_16x16x32_bf16 v[94:97], v[164:167], v[216:219], 0
	v_mfma_f32_16x16x32_bf16 v[78:81], v[164:167], v[224:227], 0
	v_mfma_f32_16x16x32_bf16 v[86:89], v[148:151], v[224:227], 0
	v_mfma_f32_16x16x32_bf16 v[126:129], v[160:163], v[198:201], v[126:129]
	v_mfma_f32_16x16x32_bf16 v[122:125], v[168:171], v[198:201], v[122:125]
	v_mfma_f32_16x16x32_bf16 v[110:113], v[168:171], v[206:209], v[110:113]
	v_mfma_f32_16x16x32_bf16 v[118:121], v[160:163], v[206:209], v[118:121]
	v_mfma_f32_16x16x32_bf16 v[102:105], v[160:163], v[220:223], v[102:105]
	v_mfma_f32_16x16x32_bf16 v[94:97], v[168:171], v[220:223], v[94:97]
	v_mfma_f32_16x16x32_bf16 v[78:81], v[168:171], v[228:231], v[78:81]
	v_mfma_f32_16x16x32_bf16 v[86:89], v[160:163], v[228:231], v[86:89]
	s_setprio 0
	s_setprio 1
	v_mfma_f32_16x16x32_bf16 v[114:117], v[172:175], v[194:197], 0
	v_mfma_f32_16x16x32_bf16 v[106:109], v[180:183], v[194:197], 0
	v_mfma_f32_16x16x32_bf16 v[90:93], v[180:183], v[202:205], 0
	v_mfma_f32_16x16x32_bf16 v[98:101], v[172:175], v[202:205], 0
	v_mfma_f32_16x16x32_bf16 v[82:85], v[172:175], v[216:219], 0
	v_mfma_f32_16x16x32_bf16 v[74:77], v[180:183], v[216:219], 0
	v_mfma_f32_16x16x32_bf16 v[66:69], v[180:183], v[224:227], 0
	v_mfma_f32_16x16x32_bf16 v[70:73], v[172:175], v[224:227], 0
	v_mfma_f32_16x16x32_bf16 v[114:117], v[176:179], v[198:201], v[114:117]
	v_mfma_f32_16x16x32_bf16 v[106:109], v[190:193], v[198:201], v[106:109]
	v_mfma_f32_16x16x32_bf16 v[90:93], v[190:193], v[206:209], v[90:93]
	v_mfma_f32_16x16x32_bf16 v[98:101], v[176:179], v[206:209], v[98:101]
	v_mfma_f32_16x16x32_bf16 v[82:85], v[176:179], v[220:223], v[82:85]
	v_mfma_f32_16x16x32_bf16 v[74:77], v[190:193], v[220:223], v[74:77]
	v_mfma_f32_16x16x32_bf16 v[66:69], v[190:193], v[228:231], v[66:69]
	v_mfma_f32_16x16x32_bf16 v[70:73], v[176:179], v[228:231], v[70:73]
	s_setprio 0
	s_barrier
	s_add_i32 s59, s51, s39
	s_mov_b32 m0, s59
	ds_read_b128 v[194:197], v159 offset:16384
	ds_read_b128 v[198:201], v159 offset:17408
	ds_read_b128 v[202:205], v159 offset:18432
	ds_read_b128 v[206:209], v159 offset:19456
	ds_read_b128 v[216:219], v159 offset:20480
	ds_read_b128 v[220:223], v159 offset:21504
	ds_read_b128 v[224:227], v159 offset:22528
	ds_read_b128 v[228:231], v159 offset:23552
	global_load_lds_dwordx4 v134, s[34:35]
	s_add_i32 m0, s59, 0x2000
	s_add_u32 s60, s34, 0x80000
	s_addc_u32 s61, s35, 0
	s_add_i32 s59, s52, s39
	global_load_lds_dwordx4 v130, s[34:35]
	s_mov_b32 m0, s59
	s_nop 0
	global_load_lds_dwordx4 v134, s[60:61]
	s_add_i32 m0, s59, 0x2000
	s_nop 0
	global_load_lds_dwordx4 v130, s[60:61]
	s_mov_b32 m0, s42
	s_nop 0
	global_load_lds_dwordx4 v136, s[36:37]
	s_mov_b32 m0, s43
	s_nop 0
	global_load_lds_dwordx4 v132, s[36:37]
	s_waitcnt vmcnt(8)
	s_waitcnt lgkmcnt(0)
	s_barrier
; #define PG8_STAGE(bufoff, gbase, voff) do { _Pragma("unroll") for (int _i = 0; _i < 2; ++_i) \
;         __builtin_amdgcn_global_load_lds((const unsigned*)((const char*)(gbase) + (voff)[_i]), (PG8_LAS unsigned*)(lds + (bufoff) + ldsw + _i * 8192), 16, 0, 0); } while (0)
; #define PG8_LDA(dst, b, h) do { _Pragma("unroll") for (int m = 0; m < 4; ++m) _Pragma("unroll") for (int k = 0; k < 2; ++k) dst[m][k] = *(const PG8_LAS bf16x8*)(lds + PG8_SA(b, h) + aoff + m * 2048 + k * 1024); } while (0)
; #define PG8_LDB(dst, b, h) do { _Pragma("unroll") for (int n = 0; n < 2; ++n) _Pragma("unroll") for (int k = 0; k < 2; ++k) dst[n][k] = *(const PG8_LAS bf16x8*)(lds + PG8_SB(b, h) + boff + n * 2048 + k * 1024); } while (0)
; #define PG8_WAIT_V(n) asm volatile("s_waitcnt vmcnt(" #n ")" ::: "memory")
; #define PG8_WAIT_L(n) asm volatile("s_waitcnt lgkmcnt(" #n ")" ::: "memory")
; #define PG8_BAR __builtin_amdgcn_s_barrier()
; #define PG8_SCHED __builtin_amdgcn_sched_barrier(0)
; template <class Epi, class Sched, bool ALIGN_EPI = false, bool SP2 = false>
; __device__ __forceinline__ void gemm_phase(PG8_LAS unsigned char* lds, const Gemm g, const Sched& S, const Epi& E) {
;     ...
;             PG8_WAIT_V(8); PG8_WAIT_L(0); PG8_BAR; PG8_MMA(1, 0, At, B0); PG8_MMA(1, 1, At, B1); PG8_BAR; PG8_SCHED;
;             PG8_LDB(B0, 1, 0); PG8_LDB(B1, 1, 1); PG8_SCHED; PG8_LDA(At, 1, 0); PG8_STAGE(PG8_SA(0, 1), a2 + hstep, voffA);
;             PG8_WAIT_V(8); PG8_WAIT_L(0); PG8_BAR; PG8_MMA(0, 0, At, B0); PG8_MMA(0, 1, At, B1); PG8_BAR; PG8_SCHED;
	s_setprio 1
	s_waitcnt lgkmcnt(0)
	v_mfma_f32_16x16x32_bf16 v[62:65], v[148:151], v[194:197], 0
	v_mfma_f32_16x16x32_bf16 v[58:61], v[164:167], v[194:197], 0
	v_mfma_f32_16x16x32_bf16 v[46:49], v[164:167], v[202:205], 0
	v_mfma_f32_16x16x32_bf16 v[54:57], v[148:151], v[202:205], 0
	v_mfma_f32_16x16x32_bf16 v[38:41], v[148:151], v[216:219], 0
	v_mfma_f32_16x16x32_bf16 v[30:33], v[164:167], v[216:219], 0
	v_mfma_f32_16x16x32_bf16 v[14:17], v[164:167], v[224:227], 0
	v_mfma_f32_16x16x32_bf16 v[22:25], v[148:151], v[224:227], 0
	v_mfma_f32_16x16x32_bf16 v[62:65], v[160:163], v[198:201], v[62:65]
	v_mfma_f32_16x16x32_bf16 v[58:61], v[168:171], v[198:201], v[58:61]
	v_mfma_f32_16x16x32_bf16 v[46:49], v[168:171], v[206:209], v[46:49]
	v_mfma_f32_16x16x32_bf16 v[54:57], v[160:163], v[206:209], v[54:57]
	v_mfma_f32_16x16x32_bf16 v[38:41], v[160:163], v[220:223], v[38:41]
	v_mfma_f32_16x16x32_bf16 v[30:33], v[168:171], v[220:223], v[30:33]
	v_mfma_f32_16x16x32_bf16 v[14:17], v[168:171], v[228:231], v[14:17]
	v_mfma_f32_16x16x32_bf16 v[22:25], v[160:163], v[228:231], v[22:25]
	s_setprio 0
	s_setprio 1
	v_mfma_f32_16x16x32_bf16 v[50:53], v[172:175], v[194:197], 0
	v_mfma_f32_16x16x32_bf16 v[42:45], v[180:183], v[194:197], 0
	v_mfma_f32_16x16x32_bf16 v[26:29], v[180:183], v[202:205], 0
	v_mfma_f32_16x16x32_bf16 v[34:37], v[172:175], v[202:205], 0
	v_mfma_f32_16x16x32_bf16 v[18:21], v[172:175], v[216:219], 0
	v_mfma_f32_16x16x32_bf16 v[10:13], v[180:183], v[216:219], 0
	v_mfma_f32_16x16x32_bf16 v[2:5], v[180:183], v[224:227], 0
	v_mfma_f32_16x16x32_bf16 v[6:9], v[172:175], v[224:227], 0
	v_mfma_f32_16x16x32_bf16 v[50:53], v[176:179], v[198:201], v[50:53]
	v_mfma_f32_16x16x32_bf16 v[42:45], v[190:193], v[198:201], v[42:45]
	v_mfma_f32_16x16x32_bf16 v[26:29], v[190:193], v[206:209], v[26:29]
	v_mfma_f32_16x16x32_bf16 v[34:37], v[176:179], v[206:209], v[34:37]
	v_mfma_f32_16x16x32_bf16 v[18:21], v[176:179], v[220:223], v[18:21]
	v_mfma_f32_16x16x32_bf16 v[10:13], v[190:193], v[220:223], v[10:13]
	v_mfma_f32_16x16x32_bf16 v[2:5], v[190:193], v[228:231], v[2:5]
	v_mfma_f32_16x16x32_bf16 v[6:9], v[176:179], v[228:231], v[6:9]
	s_setprio 0
	s_barrier
	s_add_i32 s59, 0, 0x18000
	s_add_i32 s60, 0, 0x1c000
	ds_read_b128 v[148:151], v248
	ds_read_b128 v[160:163], v248 offset:1024
	ds_read_b128 v[164:167], v248 offset:2048
	ds_read_b128 v[168:171], v248 offset:3072
	ds_read_b128 v[172:175], v249
	ds_read_b128 v[176:179], v249 offset:1024
	ds_read_b128 v[180:183], v249 offset:2048
	ds_read_b128 v[190:193], v249 offset:3072
	s_add_u32 s36, s36, 0x80000
	s_addc_u32 s37, s37, 0
	s_mov_b32 m0, s44
	ds_read_b128 v[194:197], v159 offset:32768
	ds_read_b128 v[198:201], v159 offset:33792
	ds_read_b128 v[202:205], v159 offset:34816
	ds_read_b128 v[206:209], v159 offset:35840
	ds_read_b128 v[216:219], v159 offset:36864
	ds_read_b128 v[220:223], v159 offset:37888
	ds_read_b128 v[224:227], v159 offset:38912
	ds_read_b128 v[228:231], v159 offset:39936
	global_load_lds_dwordx4 v136, s[36:37]
	s_mov_b32 m0, s45
	s_nop 0
	global_load_lds_dwordx4 v132, s[36:37]
	s_waitcnt vmcnt(8)
	s_waitcnt lgkmcnt(0)
	s_barrier
	s_setprio 1
	s_waitcnt lgkmcnt(0)
	v_mfma_f32_16x16x32_bf16 v[126:129], v[148:151], v[194:197], v[126:129]
	v_mfma_f32_16x16x32_bf16 v[122:125], v[164:167], v[194:197], v[122:125]
	v_mfma_f32_16x16x32_bf16 v[110:113], v[164:167], v[202:205], v[110:113]
	v_mfma_f32_16x16x32_bf16 v[118:121], v[148:151], v[202:205], v[118:121]
	v_mfma_f32_16x16x32_bf16 v[102:105], v[148:151], v[216:219], v[102:105]
	v_mfma_f32_16x16x32_bf16 v[94:97], v[164:167], v[216:219], v[94:97]
	v_mfma_f32_16x16x32_bf16 v[78:81], v[164:167], v[224:227], v[78:81]
	v_mfma_f32_16x16x32_bf16 v[86:89], v[148:151], v[224:227], v[86:89]
	v_mfma_f32_16x16x32_bf16 v[126:129], v[160:163], v[198:201], v[126:129]
	v_mfma_f32_16x16x32_bf16 v[122:125], v[168:171], v[198:201], v[122:125]
	v_mfma_f32_16x16x32_bf16 v[110:113], v[168:171], v[206:209], v[110:113]
	v_mfma_f32_16x16x32_bf16 v[118:121], v[160:163], v[206:209], v[118:121]
	v_mfma_f32_16x16x32_bf16 v[102:105], v[160:163], v[220:223], v[102:105]
	v_mfma_f32_16x16x32_bf16 v[94:97], v[168:171], v[220:223], v[94:97]
	v_mfma_f32_16x16x32_bf16 v[78:81], v[168:171], v[228:231], v[78:81]
	v_mfma_f32_16x16x32_bf16 v[86:89], v[160:163], v[228:231], v[86:89]
	s_setprio 0
	s_setprio 1
	v_mfma_f32_16x16x32_bf16 v[114:117], v[172:175], v[194:197], v[114:117]
	v_mfma_f32_16x16x32_bf16 v[106:109], v[180:183], v[194:197], v[106:109]
	v_mfma_f32_16x16x32_bf16 v[90:93], v[180:183], v[202:205], v[90:93]
	v_mfma_f32_16x16x32_bf16 v[98:101], v[172:175], v[202:205], v[98:101]
	v_mfma_f32_16x16x32_bf16 v[82:85], v[172:175], v[216:219], v[82:85]
	v_mfma_f32_16x16x32_bf16 v[74:77], v[180:183], v[216:219], v[74:77]
	v_mfma_f32_16x16x32_bf16 v[66:69], v[180:183], v[224:227], v[66:69]
	v_mfma_f32_16x16x32_bf16 v[70:73], v[172:175], v[224:227], v[70:73]
	v_mfma_f32_16x16x32_bf16 v[114:117], v[176:179], v[198:201], v[114:117]
	v_mfma_f32_16x16x32_bf16 v[106:109], v[190:193], v[198:201], v[106:109]
	v_mfma_f32_16x16x32_bf16 v[90:93], v[190:193], v[206:209], v[90:93]
	v_mfma_f32_16x16x32_bf16 v[98:101], v[176:179], v[206:209], v[98:101]
	v_mfma_f32_16x16x32_bf16 v[82:85], v[176:179], v[220:223], v[82:85]
	v_mfma_f32_16x16x32_bf16 v[74:77], v[190:193], v[220:223], v[74:77]
	v_mfma_f32_16x16x32_bf16 v[66:69], v[190:193], v[228:231], v[66:69]
	v_mfma_f32_16x16x32_bf16 v[70:73], v[176:179], v[228:231], v[70:73]
	s_setprio 0
	s_barrier
; #define PG8_STAGE(bufoff, gbase, voff) do { _Pragma("unroll") for (int _i = 0; _i < 2; ++_i) \
;         __builtin_amdgcn_global_load_lds((const unsigned*)((const char*)(gbase) + (voff)[_i]), (PG8_LAS unsigned*)(lds + (bufoff) + ldsw + _i * 8192), 16, 0, 0); } while (0)
; #define PG8_LDA(dst, b, h) do { _Pragma("unroll") for (int m = 0; m < 4; ++m) _Pragma("unroll") for (int k = 0; k < 2; ++k) dst[m][k] = *(const PG8_LAS bf16x8*)(lds + PG8_SA(b, h) + aoff + m * 2048 + k * 1024); } while (0)
; #define PG8_LDB(dst, b, h) do { _Pragma("unroll") for (int n = 0; n < 2; ++n) _Pragma("unroll") for (int k = 0; k < 2; ++k) dst[n][k] = *(const PG8_LAS bf16x8*)(lds + PG8_SB(b, h) + boff + n * 2048 + k * 1024); } while (0)
; #define PG8_WAIT_V(n) asm volatile("s_waitcnt vmcnt(" #n ")" ::: "memory")
; #define PG8_WAIT_L(n) asm volatile("s_waitcnt lgkmcnt(" #n ")" ::: "memory")
; #define PG8_BAR __builtin_amdgcn_s_barrier()
; #define PG8_SCHED __builtin_amdgcn_sched_barrier(0)
; template <class Epi, class Sched, bool ALIGN_EPI = false, bool SP2 = false>
; __device__ __forceinline__ void gemm_phase(PG8_LAS unsigned char* lds, const Gemm g, const Sched& S, const Epi& E) {
;     ...
;             PG8_LDB(B0, 0, 0); PG8_LDB(B1, 0, 1); PG8_SCHED; PG8_LDA(At, 0, 0); PG8_STAGE(PG8_SA(1, 1), a1 + hstep, voffA);
;             PG8_WAIT_V(8); PG8_WAIT_L(0); PG8_BAR; PG8_MMA(0, 0, At, B0); PG8_MMA(0, 1, At, B1); PG8_BAR; PG8_SCHED;
;             PG8_LDA(At, 0, 1); PG8_STAGE(PG8_SB(0, 0), b2, voffB); PG8_STAGE(PG8_SB(0, 1), b2 + hstep, voffB); PG8_STAGE(PG8_SA(0, 0), a2, voffA);
;             PG8_WAIT_V(8); PG8_WAIT_L(0); PG8_BAR; PG8_MMA(1, 0, At, B0); PG8_MMA(1, 1, At, B1); PG8_BAR; PG8_SCHED;
;             PG8_LDB(B0, 1, 0); PG8_LDB(B1, 1, 1); PG8_SCHED; PG8_LDA(At, 1, 0); PG8_STAGE(PG8_SA(0, 1), a2 + hstep, voffA);
;             PG8_WAIT_V(8); PG8_WAIT_L(0); PG8_BAR; PG8_MMA(0, 0, At, B0); PG8_MMA(0, 1, At, B1); PG8_BAR; PG8_SCHED;
;             PG8_LDA(At, 1, 1); PG8_STAGE(PG8_SB(1, 0), b3, voffB); PG8_STAGE(PG8_SB(1, 1), b3 + hstep, voffB); PG8_STAGE(PG8_SA(1, 0), a3, voffA);
;             PG8_WAIT_V(8); PG8_WAIT_L(0); PG8_BAR; PG8_MMA(1, 0, At, B0); PG8_MMA(1, 1, At, B1); PG8_BAR; PG8_SCHED;
	s_add_u32 s98, s34, 0x80
	s_addc_u32 s99, s35, 0
	s_add_u32 s100, s36, 0xfff80080
	s_addc_u32 s101, s37, -1
	s_add_i32 s36, s59, s39
	s_mov_b32 m0, s36
	ds_read_b128 v[194:197], v159 offset:49152
	ds_read_b128 v[198:201], v159 offset:50176
	ds_read_b128 v[202:205], v159 offset:51200
	ds_read_b128 v[206:209], v159 offset:52224
	ds_read_b128 v[216:219], v159 offset:53248
	ds_read_b128 v[220:223], v159 offset:54272
	ds_read_b128 v[224:227], v159 offset:55296
	ds_read_b128 v[228:231], v159 offset:56320
	global_load_lds_dwordx4 v134, s[98:99]
	s_add_i32 m0, s36, 0x2000
	s_add_u32 s34, s34, 0x80080
	s_addc_u32 s35, s35, 0
	s_add_i32 s36, s60, s39
	global_load_lds_dwordx4 v130, s[98:99]
	s_mov_b32 m0, s36
	s_nop 0
	global_load_lds_dwordx4 v134, s[34:35]
	s_add_i32 m0, s36, 0x2000
	s_nop 0
	global_load_lds_dwordx4 v130, s[34:35]
	s_mov_b32 m0, s48
	s_nop 0
	global_load_lds_dwordx4 v136, s[100:101]
	s_mov_b32 m0, s49
	s_nop 0
	global_load_lds_dwordx4 v132, s[100:101]
	s_waitcnt vmcnt(8)
	s_waitcnt lgkmcnt(0)
	s_barrier
	s_setprio 1
	s_waitcnt lgkmcnt(0)
	v_mfma_f32_16x16x32_bf16 v[62:65], v[148:151], v[194:197], v[62:65]
	v_mfma_f32_16x16x32_bf16 v[58:61], v[164:167], v[194:197], v[58:61]
	v_mfma_f32_16x16x32_bf16 v[46:49], v[164:167], v[202:205], v[46:49]
	v_mfma_f32_16x16x32_bf16 v[54:57], v[148:151], v[202:205], v[54:57]
	v_mfma_f32_16x16x32_bf16 v[38:41], v[148:151], v[216:219], v[38:41]
	v_mfma_f32_16x16x32_bf16 v[30:33], v[164:167], v[216:219], v[30:33]
	v_mfma_f32_16x16x32_bf16 v[14:17], v[164:167], v[224:227], v[14:17]
	v_mfma_f32_16x16x32_bf16 v[22:25], v[148:151], v[224:227], v[22:25]
	v_mfma_f32_16x16x32_bf16 v[62:65], v[160:163], v[198:201], v[62:65]
	v_mfma_f32_16x16x32_bf16 v[58:61], v[168:171], v[198:201], v[58:61]
	v_mfma_f32_16x16x32_bf16 v[46:49], v[168:171], v[206:209], v[46:49]
	v_mfma_f32_16x16x32_bf16 v[54:57], v[160:163], v[206:209], v[54:57]
	v_mfma_f32_16x16x32_bf16 v[38:41], v[160:163], v[220:223], v[38:41]
	v_mfma_f32_16x16x32_bf16 v[30:33], v[168:171], v[220:223], v[30:33]
	v_mfma_f32_16x16x32_bf16 v[14:17], v[168:171], v[228:231], v[14:17]
	v_mfma_f32_16x16x32_bf16 v[22:25], v[160:163], v[228:231], v[22:25]
	s_setprio 0
	s_setprio 1
	v_mfma_f32_16x16x32_bf16 v[50:53], v[172:175], v[194:197], v[50:53]
	v_mfma_f32_16x16x32_bf16 v[42:45], v[180:183], v[194:197], v[42:45]
	v_mfma_f32_16x16x32_bf16 v[26:29], v[180:183], v[202:205], v[26:29]
	v_mfma_f32_16x16x32_bf16 v[34:37], v[172:175], v[202:205], v[34:37]
	v_mfma_f32_16x16x32_bf16 v[18:21], v[172:175], v[216:219], v[18:21]
	v_mfma_f32_16x16x32_bf16 v[10:13], v[180:183], v[216:219], v[10:13]
	v_mfma_f32_16x16x32_bf16 v[2:5], v[180:183], v[224:227], v[2:5]
	v_mfma_f32_16x16x32_bf16 v[6:9], v[172:175], v[224:227], v[6:9]
	v_mfma_f32_16x16x32_bf16 v[50:53], v[176:179], v[198:201], v[50:53]
	v_mfma_f32_16x16x32_bf16 v[42:45], v[190:193], v[198:201], v[42:45]
	v_mfma_f32_16x16x32_bf16 v[26:29], v[190:193], v[206:209], v[26:29]
	v_mfma_f32_16x16x32_bf16 v[34:37], v[176:179], v[206:209], v[34:37]
	v_mfma_f32_16x16x32_bf16 v[18:21], v[176:179], v[220:223], v[18:21]
	v_mfma_f32_16x16x32_bf16 v[10:13], v[190:193], v[220:223], v[10:13]
	v_mfma_f32_16x16x32_bf16 v[2:5], v[190:193], v[228:231], v[2:5]
	v_mfma_f32_16x16x32_bf16 v[6:9], v[176:179], v[228:231], v[6:9]
	s_setprio 0
	s_barrier
	s_add_i32 s58, s58, 2
	s_add_u32 s30, s30, 0x100
	s_addc_u32 s31, s31, 0
	s_add_u32 s56, s56, 0x100
	s_addc_u32 s57, s57, 0
	s_cmp_gt_u32 s58, 29
.LBB0_1076:
	ds_read_b128 v[148:151], v157
	ds_read_b128 v[160:163], v157 offset:1024
	ds_read_b128 v[164:167], v157 offset:2048
	ds_read_b128 v[168:171], v157 offset:3072
	ds_read_b128 v[172:175], v158
	ds_read_b128 v[176:179], v158 offset:1024
	ds_read_b128 v[180:183], v158 offset:2048
	ds_read_b128 v[190:193], v158 offset:3072
	s_add_u32 s34, s30, 0xfff80080
	s_addc_u32 s35, s31, -1
	s_cmp_eq_u32 s58, 28
	s_cselect_b32 s37, s23, s35
	s_cselect_b32 s36, s29, s34
	s_cselect_b32 s35, s21, s57
	s_cselect_b32 s34, s55, s56
	s_add_i32 m0, s42, 0xc000
	ds_read_b128 v[194:197], v159
	ds_read_b128 v[198:201], v159 offset:1024
	ds_read_b128 v[202:205], v159 offset:2048
	ds_read_b128 v[206:209], v159 offset:3072
	ds_read_b128 v[216:219], v159 offset:4096
	ds_read_b128 v[220:223], v159 offset:5120
	ds_read_b128 v[224:227], v159 offset:6144
	ds_read_b128 v[228:231], v159 offset:7168
	global_load_lds_dwordx4 v140, s[30:31]
	s_add_i32 m0, s42, 0xe000
	s_nop 0
	global_load_lds_dwordx4 v142, s[30:31]
	s_waitcnt vmcnt(8)
	s_waitcnt lgkmcnt(0)
	s_barrier
; #define PG8_STAGE(bufoff, gbase, voff) do { _Pragma("unroll") for (int _i = 0; _i < 2; ++_i) \
;         __builtin_amdgcn_global_load_lds((const unsigned*)((const char*)(gbase) + (voff)[_i]), (PG8_LAS unsigned*)(lds + (bufoff) + ldsw + _i * 8192), 16, 0, 0); } while (0)
; #define PG8_LDA(dst, b, h) do { _Pragma("unroll") for (int m = 0; m < 4; ++m) _Pragma("unroll") for (int k = 0; k < 2; ++k) dst[m][k] = *(const PG8_LAS bf16x8*)(lds + PG8_SA(b, h) + aoff + m * 2048 + k * 1024); } while (0)
; #define PG8_LDB(dst, b, h) do { _Pragma("unroll") for (int n = 0; n < 2; ++n) _Pragma("unroll") for (int k = 0; k < 2; ++k) dst[n][k] = *(const PG8_LAS bf16x8*)(lds + PG8_SB(b, h) + boff + n * 2048 + k * 1024); } while (0)
; #define PG8_WAIT_V(n) asm volatile("s_waitcnt vmcnt(" #n ")" ::: "memory")
; #define PG8_WAIT_L(n) asm volatile("s_waitcnt lgkmcnt(" #n ")" ::: "memory")
; #define PG8_BAR __builtin_amdgcn_s_barrier()
; #define PG8_SCHED __builtin_amdgcn_sched_barrier(0)
; template <class Epi, class Sched, bool ALIGN_EPI = false, bool SP2 = false>
; __device__ __forceinline__ void gemm_phase(PG8_LAS unsigned char* lds, const Gemm g, const Sched& S, const Epi& E) {
;     ...
;             PG8_LDB(B0, 0, 0); PG8_LDB(B1, 0, 1); PG8_SCHED; PG8_LDA(At, 0, 0); PG8_STAGE(PG8_SA(1, 1), a1 + hstep, voffA);
;             PG8_WAIT_V(8); PG8_WAIT_L(0); PG8_BAR; PG8_MMA(0, 0, At, B0); PG8_MMA(0, 1, At, B1); PG8_BAR; PG8_SCHED;
;             PG8_LDA(At, 0, 1); PG8_STAGE(PG8_SB(0, 0), b2, voffB); PG8_STAGE(PG8_SB(0, 1), b2 + hstep, voffB); PG8_STAGE(PG8_SA(0, 0), a2, voffA);
;             PG8_WAIT_V(8); PG8_WAIT_L(0); PG8_BAR; PG8_MMA(1, 0, At, B0); PG8_MMA(1, 1, At, B1); PG8_BAR; PG8_SCHED;
;             PG8_LDB(B0, 1, 0); PG8_LDB(B1, 1, 1); PG8_SCHED; PG8_LDA(At, 1, 0); PG8_STAGE(PG8_SA(0, 1), a2 + hstep, voffA);
;             PG8_WAIT_V(8); PG8_WAIT_L(0); PG8_BAR; PG8_MMA(0, 0, At, B0); PG8_MMA(0, 1, At, B1); PG8_BAR; PG8_SCHED;
	s_setprio 1
	s_waitcnt lgkmcnt(0)
	v_mfma_f32_16x16x32_bf16 v[126:129], v[148:151], v[194:197], v[126:129]
	v_mfma_f32_16x16x32_bf16 v[122:125], v[164:167], v[194:197], v[122:125]
	v_mfma_f32_16x16x32_bf16 v[110:113], v[164:167], v[202:205], v[110:113]
	v_mfma_f32_16x16x32_bf16 v[118:121], v[148:151], v[202:205], v[118:121]
	v_mfma_f32_16x16x32_bf16 v[102:105], v[148:151], v[216:219], v[102:105]
	v_mfma_f32_16x16x32_bf16 v[94:97], v[164:167], v[216:219], v[94:97]
	v_mfma_f32_16x16x32_bf16 v[78:81], v[164:167], v[224:227], v[78:81]
	v_mfma_f32_16x16x32_bf16 v[86:89], v[148:151], v[224:227], v[86:89]
	v_mfma_f32_16x16x32_bf16 v[126:129], v[160:163], v[198:201], v[126:129]
	v_mfma_f32_16x16x32_bf16 v[122:125], v[168:171], v[198:201], v[122:125]
	v_mfma_f32_16x16x32_bf16 v[110:113], v[168:171], v[206:209], v[110:113]
	v_mfma_f32_16x16x32_bf16 v[118:121], v[160:163], v[206:209], v[118:121]
	v_mfma_f32_16x16x32_bf16 v[102:105], v[160:163], v[220:223], v[102:105]
	v_mfma_f32_16x16x32_bf16 v[94:97], v[168:171], v[220:223], v[94:97]
	v_mfma_f32_16x16x32_bf16 v[78:81], v[168:171], v[228:231], v[78:81]
	v_mfma_f32_16x16x32_bf16 v[86:89], v[160:163], v[228:231], v[86:89]
	s_setprio 0
	s_setprio 1
	v_mfma_f32_16x16x32_bf16 v[114:117], v[172:175], v[194:197], v[114:117]
	v_mfma_f32_16x16x32_bf16 v[106:109], v[180:183], v[194:197], v[106:109]
	v_mfma_f32_16x16x32_bf16 v[90:93], v[180:183], v[202:205], v[90:93]
	v_mfma_f32_16x16x32_bf16 v[98:101], v[172:175], v[202:205], v[98:101]
	v_mfma_f32_16x16x32_bf16 v[82:85], v[172:175], v[216:219], v[82:85]
	v_mfma_f32_16x16x32_bf16 v[74:77], v[180:183], v[216:219], v[74:77]
	v_mfma_f32_16x16x32_bf16 v[66:69], v[180:183], v[224:227], v[66:69]
	v_mfma_f32_16x16x32_bf16 v[70:73], v[172:175], v[224:227], v[70:73]
	v_mfma_f32_16x16x32_bf16 v[114:117], v[176:179], v[198:201], v[114:117]
	v_mfma_f32_16x16x32_bf16 v[106:109], v[190:193], v[198:201], v[106:109]
	v_mfma_f32_16x16x32_bf16 v[90:93], v[190:193], v[206:209], v[90:93]
	v_mfma_f32_16x16x32_bf16 v[98:101], v[176:179], v[206:209], v[98:101]
	v_mfma_f32_16x16x32_bf16 v[82:85], v[176:179], v[220:223], v[82:85]
	v_mfma_f32_16x16x32_bf16 v[74:77], v[190:193], v[220:223], v[74:77]
	v_mfma_f32_16x16x32_bf16 v[66:69], v[190:193], v[228:231], v[66:69]
	v_mfma_f32_16x16x32_bf16 v[70:73], v[176:179], v[228:231], v[70:73]
	s_setprio 0
	s_barrier
	s_add_i32 s59, s51, s39
	s_mov_b32 m0, s59
	ds_read_b128 v[194:197], v159 offset:16384
	ds_read_b128 v[198:201], v159 offset:17408
	ds_read_b128 v[202:205], v159 offset:18432
	ds_read_b128 v[206:209], v159 offset:19456
	ds_read_b128 v[216:219], v159 offset:20480
	ds_read_b128 v[220:223], v159 offset:21504
	ds_read_b128 v[224:227], v159 offset:22528
	ds_read_b128 v[228:231], v159 offset:23552
	global_load_lds_dwordx4 v134, s[34:35]
	s_add_i32 m0, s59, 0x2000
	s_add_u32 s60, s34, 0x80000
	s_addc_u32 s61, s35, 0
	s_add_i32 s59, s52, s39
	global_load_lds_dwordx4 v130, s[34:35]
	s_mov_b32 m0, s59
	s_nop 0
	global_load_lds_dwordx4 v134, s[60:61]
	s_add_i32 m0, s59, 0x2000
	s_nop 0
	global_load_lds_dwordx4 v130, s[60:61]
	s_mov_b32 m0, s42
	s_nop 0
	global_load_lds_dwordx4 v136, s[36:37]
	s_mov_b32 m0, s43
	s_nop 0
	global_load_lds_dwordx4 v132, s[36:37]
	s_waitcnt vmcnt(8)
	s_waitcnt lgkmcnt(0)
	s_barrier
	s_setprio 1
	s_waitcnt lgkmcnt(0)
	v_mfma_f32_16x16x32_bf16 v[62:65], v[148:151], v[194:197], v[62:65]
	v_mfma_f32_16x16x32_bf16 v[58:61], v[164:167], v[194:197], v[58:61]
	v_mfma_f32_16x16x32_bf16 v[46:49], v[164:167], v[202:205], v[46:49]
	v_mfma_f32_16x16x32_bf16 v[54:57], v[148:151], v[202:205], v[54:57]
	v_mfma_f32_16x16x32_bf16 v[38:41], v[148:151], v[216:219], v[38:41]
	v_mfma_f32_16x16x32_bf16 v[30:33], v[164:167], v[216:219], v[30:33]
	v_mfma_f32_16x16x32_bf16 v[14:17], v[164:167], v[224:227], v[14:17]
	v_mfma_f32_16x16x32_bf16 v[22:25], v[148:151], v[224:227], v[22:25]
	v_mfma_f32_16x16x32_bf16 v[62:65], v[160:163], v[198:201], v[62:65]
	v_mfma_f32_16x16x32_bf16 v[58:61], v[168:171], v[198:201], v[58:61]
	v_mfma_f32_16x16x32_bf16 v[46:49], v[168:171], v[206:209], v[46:49]
	v_mfma_f32_16x16x32_bf16 v[54:57], v[160:163], v[206:209], v[54:57]
	v_mfma_f32_16x16x32_bf16 v[38:41], v[160:163], v[220:223], v[38:41]
	v_mfma_f32_16x16x32_bf16 v[30:33], v[168:171], v[220:223], v[30:33]
	v_mfma_f32_16x16x32_bf16 v[14:17], v[168:171], v[228:231], v[14:17]
	v_mfma_f32_16x16x32_bf16 v[22:25], v[160:163], v[228:231], v[22:25]
	s_setprio 0
	s_setprio 1
	v_mfma_f32_16x16x32_bf16 v[50:53], v[172:175], v[194:197], v[50:53]
	v_mfma_f32_16x16x32_bf16 v[42:45], v[180:183], v[194:197], v[42:45]
	v_mfma_f32_16x16x32_bf16 v[26:29], v[180:183], v[202:205], v[26:29]
	v_mfma_f32_16x16x32_bf16 v[34:37], v[172:175], v[202:205], v[34:37]
	v_mfma_f32_16x16x32_bf16 v[18:21], v[172:175], v[216:219], v[18:21]
	v_mfma_f32_16x16x32_bf16 v[10:13], v[180:183], v[216:219], v[10:13]
	v_mfma_f32_16x16x32_bf16 v[2:5], v[180:183], v[224:227], v[2:5]
	v_mfma_f32_16x16x32_bf16 v[6:9], v[172:175], v[224:227], v[6:9]
	v_mfma_f32_16x16x32_bf16 v[50:53], v[176:179], v[198:201], v[50:53]
	v_mfma_f32_16x16x32_bf16 v[42:45], v[190:193], v[198:201], v[42:45]
	v_mfma_f32_16x16x32_bf16 v[26:29], v[190:193], v[206:209], v[26:29]
	v_mfma_f32_16x16x32_bf16 v[34:37], v[176:179], v[206:209], v[34:37]
	v_mfma_f32_16x16x32_bf16 v[18:21], v[176:179], v[220:223], v[18:21]
	v_mfma_f32_16x16x32_bf16 v[10:13], v[190:193], v[220:223], v[10:13]
	v_mfma_f32_16x16x32_bf16 v[2:5], v[190:193], v[228:231], v[2:5]
	v_mfma_f32_16x16x32_bf16 v[6:9], v[176:179], v[228:231], v[6:9]
	s_setprio 0
	s_barrier
; #define PG8_STAGE(bufoff, gbase, voff) do { _Pragma("unroll") for (int _i = 0; _i < 2; ++_i) \
;         __builtin_amdgcn_global_load_lds((const unsigned*)((const char*)(gbase) + (voff)[_i]), (PG8_LAS unsigned*)(lds + (bufoff) + ldsw + _i * 8192), 16, 0, 0); } while (0)
; #define PG8_LDA(dst, b, h) do { _Pragma("unroll") for (int m = 0; m < 4; ++m) _Pragma("unroll") for (int k = 0; k < 2; ++k) dst[m][k] = *(const PG8_LAS bf16x8*)(lds + PG8_SA(b, h) + aoff + m * 2048 + k * 1024); } while (0)
; #define PG8_LDB(dst, b, h) do { _Pragma("unroll") for (int n = 0; n < 2; ++n) _Pragma("unroll") for (int k = 0; k < 2; ++k) dst[n][k] = *(const PG8_LAS bf16x8*)(lds + PG8_SB(b, h) + boff + n * 2048 + k * 1024); } while (0)
; template <class Epi, class Sched, bool ALIGN_EPI = false, bool SP2 = false>
; __device__ __forceinline__ void gemm_phase(PG8_LAS unsigned char* lds, const Gemm g, const Sched& S, const Epi& E) {
;     ...
;         for (int t = 0; t < nt; t += 2) {
;             const bool last = (t == nt - 2);
;             const char* a1 = cA + (size_t)(t + 1) * kstep;
;             const char* a2 = last ? nA : cA + (size_t)(t + 2) * kstep; const char* b2 = last ? nB : cB + (size_t)(t + 2) * kstep;
;             const char* a3 = a2 + kstep; const char* b3 = b2 + kstep;
;             if (last && has_next) S.a_ready(nxt);
;             if constexpr (SP2) {
;             PG8_LDB(B0, 0, 0); PG8_LDB(B1, 0, 1); PG8_SCHED; PG8_LDA(At, 0, 0); PG8_STAGE(PG8_SA(1, 1), a1 + hstep, voffA);
;             PG8_WAIT_V(8); PG8_WAIT_L(0); PG8_BAR; PG8_MMA(0, 0, At, B0); PG8_MMA(0, 1, At, B1); PG8_BAR; PG8_SCHED;
;             PG8_LDA(At, 0, 1); PG8_STAGE(PG8_SB(0, 0), b2, voffB); PG8_STAGE(PG8_SB(0, 1), b2 + hstep, voffB); PG8_STAGE(PG8_SA(0, 0), a2, voffA);
;             PG8_WAIT_V(8); PG8_WAIT_L(0); PG8_BAR; PG8_MMA(1, 0, At, B0); PG8_MMA(1, 1, At, B1); PG8_BAR; PG8_SCHED;
;             PG8_LDB(B0, 1, 0); PG8_LDB(B1, 1, 1); PG8_SCHED; PG8_LDA(At, 1, 0); PG8_STAGE(PG8_SA(0, 1), a2 + hstep, voffA);
;             PG8_WAIT_V(8); PG8_WAIT_L(0); PG8_BAR; PG8_MMA(0, 0, At, B0); PG8_MMA(0, 1, At, B1); PG8_BAR; PG8_SCHED;
;             PG8_LDA(At, 1, 1); PG8_STAGE(PG8_SB(1, 0), b3, voffB); PG8_STAGE(PG8_SB(1, 1), b3 + hstep, voffB); PG8_STAGE(PG8_SA(1, 0), a3, voffA);
;             PG8_WAIT_V(8); PG8_WAIT_L(0); PG8_BAR; PG8_MMA(1, 0, At, B0); PG8_MMA(1, 1, At, B1); PG8_BAR; PG8_SCHED;
	s_add_i32 s59, 0, 0x18000
	s_add_i32 s60, 0, 0x1c000
	ds_read_b128 v[148:151], v248
	ds_read_b128 v[160:163], v248 offset:1024
	ds_read_b128 v[164:167], v248 offset:2048
	ds_read_b128 v[168:171], v248 offset:3072
	ds_read_b128 v[172:175], v249
	ds_read_b128 v[176:179], v249 offset:1024
	ds_read_b128 v[180:183], v249 offset:2048
	ds_read_b128 v[190:193], v249 offset:3072
	s_add_u32 s36, s36, 0x80000
	s_addc_u32 s37, s37, 0
	s_mov_b32 m0, s44
	ds_read_b128 v[194:197], v159 offset:32768
	ds_read_b128 v[198:201], v159 offset:33792
	ds_read_b128 v[202:205], v159 offset:34816
	ds_read_b128 v[206:209], v159 offset:35840
	ds_read_b128 v[216:219], v159 offset:36864
	ds_read_b128 v[220:223], v159 offset:37888
	ds_read_b128 v[224:227], v159 offset:38912
	ds_read_b128 v[228:231], v159 offset:39936
	global_load_lds_dwordx4 v136, s[36:37]
	s_mov_b32 m0, s45
	s_nop 0
	global_load_lds_dwordx4 v132, s[36:37]
	s_waitcnt vmcnt(8)
	s_waitcnt lgkmcnt(0)
	s_barrier
	s_setprio 1
	s_waitcnt lgkmcnt(0)
	v_mfma_f32_16x16x32_bf16 v[126:129], v[148:151], v[194:197], v[126:129]
	v_mfma_f32_16x16x32_bf16 v[122:125], v[164:167], v[194:197], v[122:125]
	v_mfma_f32_16x16x32_bf16 v[110:113], v[164:167], v[202:205], v[110:113]
	v_mfma_f32_16x16x32_bf16 v[118:121], v[148:151], v[202:205], v[118:121]
	v_mfma_f32_16x16x32_bf16 v[102:105], v[148:151], v[216:219], v[102:105]
	v_mfma_f32_16x16x32_bf16 v[94:97], v[164:167], v[216:219], v[94:97]
	v_mfma_f32_16x16x32_bf16 v[78:81], v[164:167], v[224:227], v[78:81]
	v_mfma_f32_16x16x32_bf16 v[86:89], v[148:151], v[224:227], v[86:89]
	v_mfma_f32_16x16x32_bf16 v[126:129], v[160:163], v[198:201], v[126:129]
	v_mfma_f32_16x16x32_bf16 v[122:125], v[168:171], v[198:201], v[122:125]
	v_mfma_f32_16x16x32_bf16 v[110:113], v[168:171], v[206:209], v[110:113]
	v_mfma_f32_16x16x32_bf16 v[118:121], v[160:163], v[206:209], v[118:121]
	v_mfma_f32_16x16x32_bf16 v[102:105], v[160:163], v[220:223], v[102:105]
	v_mfma_f32_16x16x32_bf16 v[94:97], v[168:171], v[220:223], v[94:97]
	v_mfma_f32_16x16x32_bf16 v[78:81], v[168:171], v[228:231], v[78:81]
	v_mfma_f32_16x16x32_bf16 v[86:89], v[160:163], v[228:231], v[86:89]
	s_setprio 0
	s_setprio 1
	v_mfma_f32_16x16x32_bf16 v[114:117], v[172:175], v[194:197], v[114:117]
	v_mfma_f32_16x16x32_bf16 v[106:109], v[180:183], v[194:197], v[106:109]
	v_mfma_f32_16x16x32_bf16 v[90:93], v[180:183], v[202:205], v[90:93]
	v_mfma_f32_16x16x32_bf16 v[98:101], v[172:175], v[202:205], v[98:101]
	v_mfma_f32_16x16x32_bf16 v[82:85], v[172:175], v[216:219], v[82:85]
	v_mfma_f32_16x16x32_bf16 v[74:77], v[180:183], v[216:219], v[74:77]
	v_mfma_f32_16x16x32_bf16 v[66:69], v[180:183], v[224:227], v[66:69]
	v_mfma_f32_16x16x32_bf16 v[70:73], v[172:175], v[224:227], v[70:73]
	v_mfma_f32_16x16x32_bf16 v[114:117], v[176:179], v[198:201], v[114:117]
	v_mfma_f32_16x16x32_bf16 v[106:109], v[190:193], v[198:201], v[106:109]
	v_mfma_f32_16x16x32_bf16 v[90:93], v[190:193], v[206:209], v[90:93]
	v_mfma_f32_16x16x32_bf16 v[98:101], v[176:179], v[206:209], v[98:101]
	v_mfma_f32_16x16x32_bf16 v[82:85], v[176:179], v[220:223], v[82:85]
	v_mfma_f32_16x16x32_bf16 v[74:77], v[190:193], v[220:223], v[74:77]
	v_mfma_f32_16x16x32_bf16 v[66:69], v[190:193], v[228:231], v[66:69]
	v_mfma_f32_16x16x32_bf16 v[70:73], v[176:179], v[228:231], v[70:73]
	s_setprio 0
	s_barrier
	s_add_u32 s98, s34, 0x80
	s_addc_u32 s99, s35, 0
	s_add_u32 s100, s36, 0xfff80080
	s_addc_u32 s101, s37, -1
	s_add_i32 s36, s59, s39
	s_mov_b32 m0, s36
	ds_read_b128 v[194:197], v159 offset:49152
	ds_read_b128 v[198:201], v159 offset:50176
	ds_read_b128 v[202:205], v159 offset:51200
	ds_read_b128 v[206:209], v159 offset:52224
	ds_read_b128 v[216:219], v159 offset:53248
	ds_read_b128 v[220:223], v159 offset:54272
	ds_read_b128 v[224:227], v159 offset:55296
	ds_read_b128 v[228:231], v159 offset:56320
	global_load_lds_dwordx4 v134, s[98:99]
	s_add_i32 m0, s36, 0x2000
	s_add_u32 s34, s34, 0x80080
	s_addc_u32 s35, s35, 0
	s_add_i32 s36, s60, s39
	global_load_lds_dwordx4 v130, s[98:99]
	s_mov_b32 m0, s36
	s_nop 0
	global_load_lds_dwordx4 v134, s[34:35]
	s_add_i32 m0, s36, 0x2000
	s_nop 0
	global_load_lds_dwordx4 v130, s[34:35]
	s_mov_b32 m0, s48
	s_nop 0
	global_load_lds_dwordx4 v136, s[100:101]
	s_mov_b32 m0, s49
	s_nop 0
	global_load_lds_dwordx4 v132, s[100:101]
	s_waitcnt vmcnt(8)
	s_waitcnt lgkmcnt(0)
	s_barrier
	s_setprio 1
	s_waitcnt lgkmcnt(0)
	v_mfma_f32_16x16x32_bf16 v[62:65], v[148:151], v[194:197], v[62:65]
	v_mfma_f32_16x16x32_bf16 v[58:61], v[164:167], v[194:197], v[58:61]
	v_mfma_f32_16x16x32_bf16 v[46:49], v[164:167], v[202:205], v[46:49]
	v_mfma_f32_16x16x32_bf16 v[54:57], v[148:151], v[202:205], v[54:57]
	v_mfma_f32_16x16x32_bf16 v[38:41], v[148:151], v[216:219], v[38:41]
	v_mfma_f32_16x16x32_bf16 v[30:33], v[164:167], v[216:219], v[30:33]
	v_mfma_f32_16x16x32_bf16 v[14:17], v[164:167], v[224:227], v[14:17]
	v_mfma_f32_16x16x32_bf16 v[22:25], v[148:151], v[224:227], v[22:25]
	v_mfma_f32_16x16x32_bf16 v[62:65], v[160:163], v[198:201], v[62:65]
	v_mfma_f32_16x16x32_bf16 v[58:61], v[168:171], v[198:201], v[58:61]
	v_mfma_f32_16x16x32_bf16 v[46:49], v[168:171], v[206:209], v[46:49]
	v_mfma_f32_16x16x32_bf16 v[54:57], v[160:163], v[206:209], v[54:57]
	v_mfma_f32_16x16x32_bf16 v[38:41], v[160:163], v[220:223], v[38:41]
	v_mfma_f32_16x16x32_bf16 v[30:33], v[168:171], v[220:223], v[30:33]
	v_mfma_f32_16x16x32_bf16 v[14:17], v[168:171], v[228:231], v[14:17]
	v_mfma_f32_16x16x32_bf16 v[22:25], v[160:163], v[228:231], v[22:25]
	s_setprio 0
	s_setprio 1
	v_mfma_f32_16x16x32_bf16 v[50:53], v[172:175], v[194:197], v[50:53]
	v_mfma_f32_16x16x32_bf16 v[42:45], v[180:183], v[194:197], v[42:45]
	v_mfma_f32_16x16x32_bf16 v[26:29], v[180:183], v[202:205], v[26:29]
	v_mfma_f32_16x16x32_bf16 v[34:37], v[172:175], v[202:205], v[34:37]
	v_mfma_f32_16x16x32_bf16 v[18:21], v[172:175], v[216:219], v[18:21]
	v_mfma_f32_16x16x32_bf16 v[10:13], v[180:183], v[216:219], v[10:13]
	v_mfma_f32_16x16x32_bf16 v[2:5], v[180:183], v[224:227], v[2:5]
	v_mfma_f32_16x16x32_bf16 v[6:9], v[172:175], v[224:227], v[6:9]
	v_mfma_f32_16x16x32_bf16 v[50:53], v[176:179], v[198:201], v[50:53]
	v_mfma_f32_16x16x32_bf16 v[42:45], v[190:193], v[198:201], v[42:45]
	v_mfma_f32_16x16x32_bf16 v[26:29], v[190:193], v[206:209], v[26:29]
	v_mfma_f32_16x16x32_bf16 v[34:37], v[176:179], v[206:209], v[34:37]
	v_mfma_f32_16x16x32_bf16 v[18:21], v[176:179], v[220:223], v[18:21]
	v_mfma_f32_16x16x32_bf16 v[10:13], v[190:193], v[220:223], v[10:13]
	v_mfma_f32_16x16x32_bf16 v[2:5], v[190:193], v[228:231], v[2:5]
	v_mfma_f32_16x16x32_bf16 v[6:9], v[176:179], v[228:231], v[6:9]
	s_setprio 0
	s_barrier
	s_add_i32 s58, s58, 2
	s_add_u32 s30, s30, 0x100
	s_addc_u32 s31, s31, 0
	s_add_u32 s56, s56, 0x100
	s_addc_u32 s57, s57, 0
	s_cmp_gt_u32 s58, 29
	s_cbranch_scc0 .LBB0_1076
	s_and_b64 vcc, exec, s[8:9]
	s_cbranch_vccnz .LBB0_1081
	v_lshl_add_u32 v148, s28, 8, v154
	s_cmp_gt_i32 s54, 16
	s_mov_b64 s[28:29], -1
	s_cbranch_scc1 .LBB0_1082

; #define PG8_STAGE(bufoff, gbase, voff) do { _Pragma("unroll") for (int _i = 0; _i < 2; ++_i) \
;         __builtin_amdgcn_global_load_lds((const unsigned*)((const char*)(gbase) + (voff)[_i]), (PG8_LAS unsigned*)(lds + (bufoff) + ldsw + _i * 8192), 16, 0, 0); } while (0)
; #define PG8_LDA(dst, b, h) do { _Pragma("unroll") for (int m = 0; m < 4; ++m) _Pragma("unroll") for (int k = 0; k < 2; ++k) dst[m][k] = *(const PG8_LAS bf16x8*)(lds + PG8_SA(b, h) + aoff + m * 2048 + k * 1024); } while (0)
; #define PG8_LDB(dst, b, h) do { _Pragma("unroll") for (int n = 0; n < 2; ++n) _Pragma("unroll") for (int k = 0; k < 2; ++k) dst[n][k] = *(const PG8_LAS bf16x8*)(lds + PG8_SB(b, h) + boff + n * 2048 + k * 1024); } while (0)
; #define PG8_WAIT_V(n) asm volatile("s_waitcnt vmcnt(" #n ")" ::: "memory")
; #define PG8_WAIT_L(n) asm volatile("s_waitcnt lgkmcnt(" #n ")" ::: "memory")
; #define PG8_BAR __builtin_amdgcn_s_barrier()
; #define PG8_SCHED __builtin_amdgcn_sched_barrier(0)
; template <class Epi, class Sched, bool ALIGN_EPI = false, bool SP2 = false>
; __device__ __forceinline__ void gemm_phase(PG8_LAS unsigned char* lds, const Gemm g, const Sched& S, const Epi& E) {
;     ...
;         const bool has_next = S.next(ui + 1, nxt);
;         const char* nA = has_next ? (const char*)g.A + (size_t)nxt.pm * tstep : cA; const char* nB = has_next ? (const char*)g.Bt + (size_t)nxt.pn * tstep : cB;
;         for (int t = 0; t < nt; t += 2) {
;             const bool last = (t == nt - 2);
;             const char* a1 = cA + (size_t)(t + 1) * kstep;
;             const char* a2 = last ? nA : cA + (size_t)(t + 2) * kstep; const char* b2 = last ? nB : cB + (size_t)(t + 2) * kstep;
;             const char* a3 = a2 + kstep; const char* b3 = b2 + kstep;
;             if (last && has_next) S.a_ready(nxt);
;             if constexpr (SP2) {
;             PG8_LDB(B0, 0, 0); PG8_LDB(B1, 0, 1); PG8_SCHED; PG8_LDA(At, 0, 0); PG8_STAGE(PG8_SA(1, 1), a1 + hstep, voffA);
;             PG8_WAIT_V(8); PG8_WAIT_L(0); PG8_BAR; PG8_MMA(0, 0, At, B0); PG8_MMA(0, 1, At, B1); PG8_BAR; PG8_SCHED;
;             PG8_LDA(At, 0, 1); PG8_STAGE(PG8_SB(0, 0), b2, voffB); PG8_STAGE(PG8_SB(0, 1), b2 + hstep, voffB); PG8_STAGE(PG8_SA(0, 0), a2, voffA);
;             PG8_WAIT_V(8); PG8_WAIT_L(0); PG8_BAR; PG8_MMA(1, 0, At, B0); PG8_MMA(1, 1, At, B1); PG8_BAR; PG8_SCHED;
.LBB0_1455:
	s_ashr_i32 s13, s12, 31
	s_lshl_b64 s[14:15], s[12:13], 20
	v_readlane_b32 s16, v247, 17
	v_readlane_b32 s17, v247, 18
	s_add_u32 s14, s16, s14
	s_addc_u32 s15, s17, s15
	s_and_b64 s[16:17], s[2:3], exec
	s_cselect_b32 s13, s15, s21
	s_cselect_b32 s50, s14, s20
	s_ashr_i32 s11, s10, 31
	s_lshl_b64 s[16:17], s[10:11], 20
	s_add_u32 s16, s27, s16
	s_addc_u32 s17, s28, s17
	s_and_b64 s[24:25], s[2:3], exec
	s_cselect_b32 s11, s17, s23
	s_cselect_b32 s51, s16, s22
	s_add_u32 s20, s20, 0x80080
	s_addc_u32 s21, s21, 0
	s_add_u32 s52, s22, 0x100
	s_addc_u32 s53, s23, 0
	s_mov_b32 s54, -2
	v_add_u32_e32 v248, 0x18000, v174
	v_add_u32_e32 v249, 0x1c000, v174
	ds_read_b128 v[130:133], v176
	ds_read_b128 v[134:137], v176 offset:1024
	ds_read_b128 v[138:141], v176 offset:2048
	ds_read_b128 v[142:145], v176 offset:3072
	ds_read_b128 v[146:149], v177
	ds_read_b128 v[150:153], v177 offset:1024
	ds_read_b128 v[170:173], v177 offset:2048
	ds_read_b128 v[180:183], v177 offset:3072
	s_add_u32 s22, s20, 0xfff80080
	s_addc_u32 s23, s21, -1
	s_cmp_eq_u32 s54, 28
	s_cselect_b32 s25, s13, s23
	s_cselect_b32 s24, s50, s22
	s_cselect_b32 s23, s11, s53
	s_cselect_b32 s22, s51, s52
	s_add_i32 m0, s19, 0xc000
	ds_read_b128 v[188:191], v178
	ds_read_b128 v[192:195], v178 offset:1024
	ds_read_b128 v[196:199], v178 offset:2048
	ds_read_b128 v[200:203], v178 offset:3072
	ds_read_b128 v[204:207], v178 offset:4096
	ds_read_b128 v[214:217], v178 offset:5120
	ds_read_b128 v[218:221], v178 offset:6144
	ds_read_b128 v[222:225], v178 offset:7168
	global_load_lds_dwordx4 v162, s[20:21]
	s_add_i32 m0, s19, 0xe000
	s_nop 0
	global_load_lds_dwordx4 v164, s[20:21]
	s_waitcnt vmcnt(8)
	s_waitcnt lgkmcnt(0)
	s_barrier
	s_setprio 1
	s_waitcnt lgkmcnt(0)
	v_mfma_f32_16x16x32_bf16 v[126:129], v[130:133], v[188:191], 0
	v_mfma_f32_16x16x32_bf16 v[122:125], v[138:141], v[188:191], 0
	v_mfma_f32_16x16x32_bf16 v[106:109], v[138:141], v[196:199], 0
	v_mfma_f32_16x16x32_bf16 v[110:113], v[130:133], v[196:199], 0
	v_mfma_f32_16x16x32_bf16 v[98:101], v[130:133], v[204:207], 0
	v_mfma_f32_16x16x32_bf16 v[90:93], v[138:141], v[204:207], 0
	v_mfma_f32_16x16x32_bf16 v[74:77], v[138:141], v[218:221], 0
	v_mfma_f32_16x16x32_bf16 v[82:85], v[130:133], v[218:221], 0
	v_mfma_f32_16x16x32_bf16 v[126:129], v[134:137], v[192:195], v[126:129]
	v_mfma_f32_16x16x32_bf16 v[122:125], v[142:145], v[192:195], v[122:125]
	v_mfma_f32_16x16x32_bf16 v[106:109], v[142:145], v[200:203], v[106:109]
	v_mfma_f32_16x16x32_bf16 v[110:113], v[134:137], v[200:203], v[110:113]
	v_mfma_f32_16x16x32_bf16 v[98:101], v[134:137], v[214:217], v[98:101]
	v_mfma_f32_16x16x32_bf16 v[90:93], v[142:145], v[214:217], v[90:93]
	v_mfma_f32_16x16x32_bf16 v[74:77], v[142:145], v[222:225], v[74:77]
	v_mfma_f32_16x16x32_bf16 v[82:85], v[134:137], v[222:225], v[82:85]
	s_setprio 0
	s_setprio 1
	v_mfma_f32_16x16x32_bf16 v[118:121], v[146:149], v[188:191], 0
	v_mfma_f32_16x16x32_bf16 v[114:117], v[170:173], v[188:191], 0
	v_mfma_f32_16x16x32_bf16 v[94:97], v[170:173], v[196:199], 0
	v_mfma_f32_16x16x32_bf16 v[102:105], v[146:149], v[196:199], 0
	v_mfma_f32_16x16x32_bf16 v[86:89], v[146:149], v[204:207], 0
	v_mfma_f32_16x16x32_bf16 v[78:81], v[170:173], v[204:207], 0
	v_mfma_f32_16x16x32_bf16 v[66:69], v[170:173], v[218:221], 0
	v_mfma_f32_16x16x32_bf16 v[70:73], v[146:149], v[218:221], 0
	v_mfma_f32_16x16x32_bf16 v[118:121], v[150:153], v[192:195], v[118:121]
	v_mfma_f32_16x16x32_bf16 v[114:117], v[180:183], v[192:195], v[114:117]
	v_mfma_f32_16x16x32_bf16 v[94:97], v[180:183], v[200:203], v[94:97]
	v_mfma_f32_16x16x32_bf16 v[102:105], v[150:153], v[200:203], v[102:105]
	v_mfma_f32_16x16x32_bf16 v[86:89], v[150:153], v[214:217], v[86:89]
	v_mfma_f32_16x16x32_bf16 v[78:81], v[180:183], v[214:217], v[78:81]
	v_mfma_f32_16x16x32_bf16 v[66:69], v[180:183], v[222:225], v[66:69]
	v_mfma_f32_16x16x32_bf16 v[70:73], v[150:153], v[222:225], v[70:73]
	s_setprio 0
	s_barrier
	s_add_i32 s55, s42, s29
	s_mov_b32 m0, s55
	ds_read_b128 v[188:191], v178 offset:16384
	ds_read_b128 v[192:195], v178 offset:17408
	ds_read_b128 v[196:199], v178 offset:18432
	ds_read_b128 v[200:203], v178 offset:19456
	ds_read_b128 v[204:207], v178 offset:20480
	ds_read_b128 v[214:217], v178 offset:21504
	ds_read_b128 v[218:221], v178 offset:22528
	ds_read_b128 v[222:225], v178 offset:23552
	global_load_lds_dwordx4 v156, s[22:23]
	s_add_i32 m0, s55, 0x2000
	s_add_u32 s56, s22, 0x80000
	s_addc_u32 s57, s23, 0
	s_add_i32 s55, s43, s29
	global_load_lds_dwordx4 v160, s[22:23]
	s_mov_b32 m0, s55
	s_nop 0
	global_load_lds_dwordx4 v156, s[56:57]
	s_add_i32 m0, s55, 0x2000
	s_nop 0
	global_load_lds_dwordx4 v160, s[56:57]
	s_mov_b32 m0, s19
	s_nop 0
	global_load_lds_dwordx4 v154, s[24:25]
	s_mov_b32 m0, s30
	s_nop 0
	global_load_lds_dwordx4 v158, s[24:25]
	s_waitcnt vmcnt(8)
	s_waitcnt lgkmcnt(0)
	s_barrier
; #define PG8_STAGE(bufoff, gbase, voff) do { _Pragma("unroll") for (int _i = 0; _i < 2; ++_i) \
;         __builtin_amdgcn_global_load_lds((const unsigned*)((const char*)(gbase) + (voff)[_i]), (PG8_LAS unsigned*)(lds + (bufoff) + ldsw + _i * 8192), 16, 0, 0); } while (0)
; #define PG8_LDA(dst, b, h) do { _Pragma("unroll") for (int m = 0; m < 4; ++m) _Pragma("unroll") for (int k = 0; k < 2; ++k) dst[m][k] = *(const PG8_LAS bf16x8*)(lds + PG8_SA(b, h) + aoff + m * 2048 + k * 1024); } while (0)
; #define PG8_LDB(dst, b, h) do { _Pragma("unroll") for (int n = 0; n < 2; ++n) _Pragma("unroll") for (int k = 0; k < 2; ++k) dst[n][k] = *(const PG8_LAS bf16x8*)(lds + PG8_SB(b, h) + boff + n * 2048 + k * 1024); } while (0)
; #define PG8_WAIT_V(n) asm volatile("s_waitcnt vmcnt(" #n ")" ::: "memory")
; #define PG8_WAIT_L(n) asm volatile("s_waitcnt lgkmcnt(" #n ")" ::: "memory")
; #define PG8_BAR __builtin_amdgcn_s_barrier()
; #define PG8_SCHED __builtin_amdgcn_sched_barrier(0)
; template <class Epi, class Sched, bool ALIGN_EPI = false, bool SP2 = false>
; __device__ __forceinline__ void gemm_phase(PG8_LAS unsigned char* lds, const Gemm g, const Sched& S, const Epi& E) {
;     ...
;             PG8_LDB(B0, 0, 0); PG8_LDB(B1, 0, 1); PG8_SCHED; PG8_LDA(At, 0, 0); PG8_STAGE(PG8_SA(1, 1), a1 + hstep, voffA);
;             PG8_WAIT_V(8); PG8_WAIT_L(0); PG8_BAR; PG8_MMA(0, 0, At, B0); PG8_MMA(0, 1, At, B1); PG8_BAR; PG8_SCHED;
;             PG8_LDA(At, 0, 1); PG8_STAGE(PG8_SB(0, 0), b2, voffB); PG8_STAGE(PG8_SB(0, 1), b2 + hstep, voffB); PG8_STAGE(PG8_SA(0, 0), a2, voffA);
;             PG8_WAIT_V(8); PG8_WAIT_L(0); PG8_BAR; PG8_MMA(1, 0, At, B0); PG8_MMA(1, 1, At, B1); PG8_BAR; PG8_SCHED;
;             PG8_LDB(B0, 1, 0); PG8_LDB(B1, 1, 1); PG8_SCHED; PG8_LDA(At, 1, 0); PG8_STAGE(PG8_SA(0, 1), a2 + hstep, voffA);
;             PG8_WAIT_V(8); PG8_WAIT_L(0); PG8_BAR; PG8_MMA(0, 0, At, B0); PG8_MMA(0, 1, At, B1); PG8_BAR; PG8_SCHED;
	s_setprio 1
	s_waitcnt lgkmcnt(0)
	v_mfma_f32_16x16x32_bf16 v[62:65], v[130:133], v[188:191], 0
	v_mfma_f32_16x16x32_bf16 v[58:61], v[138:141], v[188:191], 0
	v_mfma_f32_16x16x32_bf16 v[42:45], v[138:141], v[196:199], 0
	v_mfma_f32_16x16x32_bf16 v[50:53], v[130:133], v[196:199], 0
	v_mfma_f32_16x16x32_bf16 v[34:37], v[130:133], v[204:207], 0
	v_mfma_f32_16x16x32_bf16 v[26:29], v[138:141], v[204:207], 0
	v_mfma_f32_16x16x32_bf16 v[10:13], v[138:141], v[218:221], 0
	v_mfma_f32_16x16x32_bf16 v[18:21], v[130:133], v[218:221], 0
	v_mfma_f32_16x16x32_bf16 v[62:65], v[134:137], v[192:195], v[62:65]
	v_mfma_f32_16x16x32_bf16 v[58:61], v[142:145], v[192:195], v[58:61]
	v_mfma_f32_16x16x32_bf16 v[42:45], v[142:145], v[200:203], v[42:45]
	v_mfma_f32_16x16x32_bf16 v[50:53], v[134:137], v[200:203], v[50:53]
	v_mfma_f32_16x16x32_bf16 v[34:37], v[134:137], v[214:217], v[34:37]
	v_mfma_f32_16x16x32_bf16 v[26:29], v[142:145], v[214:217], v[26:29]
	v_mfma_f32_16x16x32_bf16 v[10:13], v[142:145], v[222:225], v[10:13]
	v_mfma_f32_16x16x32_bf16 v[18:21], v[134:137], v[222:225], v[18:21]
	s_setprio 0
	s_setprio 1
	v_mfma_f32_16x16x32_bf16 v[54:57], v[146:149], v[188:191], 0
	v_mfma_f32_16x16x32_bf16 v[46:49], v[170:173], v[188:191], 0
	v_mfma_f32_16x16x32_bf16 v[30:33], v[170:173], v[196:199], 0
	v_mfma_f32_16x16x32_bf16 v[38:41], v[146:149], v[196:199], 0
	v_mfma_f32_16x16x32_bf16 v[22:25], v[146:149], v[204:207], 0
	v_mfma_f32_16x16x32_bf16 v[14:17], v[170:173], v[204:207], 0
	v_mfma_f32_16x16x32_bf16 v[2:5], v[170:173], v[218:221], 0
	v_mfma_f32_16x16x32_bf16 v[6:9], v[146:149], v[218:221], 0
	v_mfma_f32_16x16x32_bf16 v[54:57], v[150:153], v[192:195], v[54:57]
	v_mfma_f32_16x16x32_bf16 v[46:49], v[180:183], v[192:195], v[46:49]
	v_mfma_f32_16x16x32_bf16 v[30:33], v[180:183], v[200:203], v[30:33]
	v_mfma_f32_16x16x32_bf16 v[38:41], v[150:153], v[200:203], v[38:41]
	v_mfma_f32_16x16x32_bf16 v[22:25], v[150:153], v[214:217], v[22:25]
	v_mfma_f32_16x16x32_bf16 v[14:17], v[180:183], v[214:217], v[14:17]
	v_mfma_f32_16x16x32_bf16 v[2:5], v[180:183], v[222:225], v[2:5]
	v_mfma_f32_16x16x32_bf16 v[6:9], v[150:153], v[222:225], v[6:9]
	s_setprio 0
	s_barrier
	s_add_i32 s55, 0, 0x18000
	s_add_i32 s56, 0, 0x1c000
	ds_read_b128 v[130:133], v248
	ds_read_b128 v[134:137], v248 offset:1024
	ds_read_b128 v[138:141], v248 offset:2048
	ds_read_b128 v[142:145], v248 offset:3072
	ds_read_b128 v[146:149], v249
	ds_read_b128 v[150:153], v249 offset:1024
	ds_read_b128 v[170:173], v249 offset:2048
	ds_read_b128 v[180:183], v249 offset:3072
	s_add_u32 s24, s24, 0x80000
	s_addc_u32 s25, s25, 0
	s_mov_b32 m0, s31
	ds_read_b128 v[188:191], v178 offset:32768
	ds_read_b128 v[192:195], v178 offset:33792
	ds_read_b128 v[196:199], v178 offset:34816
	ds_read_b128 v[200:203], v178 offset:35840
	ds_read_b128 v[204:207], v178 offset:36864
	ds_read_b128 v[214:217], v178 offset:37888
	ds_read_b128 v[218:221], v178 offset:38912
	ds_read_b128 v[222:225], v178 offset:39936
	global_load_lds_dwordx4 v154, s[24:25]
	s_mov_b32 m0, s33
	s_nop 0
	global_load_lds_dwordx4 v158, s[24:25]
	s_waitcnt vmcnt(8)
	s_waitcnt lgkmcnt(0)
	s_barrier
	s_setprio 1
	s_waitcnt lgkmcnt(0)
	v_mfma_f32_16x16x32_bf16 v[126:129], v[130:133], v[188:191], v[126:129]
	v_mfma_f32_16x16x32_bf16 v[122:125], v[138:141], v[188:191], v[122:125]
	v_mfma_f32_16x16x32_bf16 v[106:109], v[138:141], v[196:199], v[106:109]
	v_mfma_f32_16x16x32_bf16 v[110:113], v[130:133], v[196:199], v[110:113]
	v_mfma_f32_16x16x32_bf16 v[98:101], v[130:133], v[204:207], v[98:101]
	v_mfma_f32_16x16x32_bf16 v[90:93], v[138:141], v[204:207], v[90:93]
	v_mfma_f32_16x16x32_bf16 v[74:77], v[138:141], v[218:221], v[74:77]
	v_mfma_f32_16x16x32_bf16 v[82:85], v[130:133], v[218:221], v[82:85]
	v_mfma_f32_16x16x32_bf16 v[126:129], v[134:137], v[192:195], v[126:129]
	v_mfma_f32_16x16x32_bf16 v[122:125], v[142:145], v[192:195], v[122:125]
	v_mfma_f32_16x16x32_bf16 v[106:109], v[142:145], v[200:203], v[106:109]
	v_mfma_f32_16x16x32_bf16 v[110:113], v[134:137], v[200:203], v[110:113]
	v_mfma_f32_16x16x32_bf16 v[98:101], v[134:137], v[214:217], v[98:101]
	v_mfma_f32_16x16x32_bf16 v[90:93], v[142:145], v[214:217], v[90:93]
	v_mfma_f32_16x16x32_bf16 v[74:77], v[142:145], v[222:225], v[74:77]
	v_mfma_f32_16x16x32_bf16 v[82:85], v[134:137], v[222:225], v[82:85]
	s_setprio 0
	s_setprio 1
	v_mfma_f32_16x16x32_bf16 v[118:121], v[146:149], v[188:191], v[118:121]
	v_mfma_f32_16x16x32_bf16 v[114:117], v[170:173], v[188:191], v[114:117]
	v_mfma_f32_16x16x32_bf16 v[94:97], v[170:173], v[196:199], v[94:97]
	v_mfma_f32_16x16x32_bf16 v[102:105], v[146:149], v[196:199], v[102:105]
	v_mfma_f32_16x16x32_bf16 v[86:89], v[146:149], v[204:207], v[86:89]
	v_mfma_f32_16x16x32_bf16 v[78:81], v[170:173], v[204:207], v[78:81]
	v_mfma_f32_16x16x32_bf16 v[66:69], v[170:173], v[218:221], v[66:69]
	v_mfma_f32_16x16x32_bf16 v[70:73], v[146:149], v[218:221], v[70:73]
	v_mfma_f32_16x16x32_bf16 v[118:121], v[150:153], v[192:195], v[118:121]
	v_mfma_f32_16x16x32_bf16 v[114:117], v[180:183], v[192:195], v[114:117]
	v_mfma_f32_16x16x32_bf16 v[94:97], v[180:183], v[200:203], v[94:97]
	v_mfma_f32_16x16x32_bf16 v[102:105], v[150:153], v[200:203], v[102:105]
	v_mfma_f32_16x16x32_bf16 v[86:89], v[150:153], v[214:217], v[86:89]
	v_mfma_f32_16x16x32_bf16 v[78:81], v[180:183], v[214:217], v[78:81]
	v_mfma_f32_16x16x32_bf16 v[66:69], v[180:183], v[222:225], v[66:69]
	v_mfma_f32_16x16x32_bf16 v[70:73], v[150:153], v[222:225], v[70:73]
	s_setprio 0
	s_barrier
; #define PG8_STAGE(bufoff, gbase, voff) do { _Pragma("unroll") for (int _i = 0; _i < 2; ++_i) \
;         __builtin_amdgcn_global_load_lds((const unsigned*)((const char*)(gbase) + (voff)[_i]), (PG8_LAS unsigned*)(lds + (bufoff) + ldsw + _i * 8192), 16, 0, 0); } while (0)
; #define PG8_LDA(dst, b, h) do { _Pragma("unroll") for (int m = 0; m < 4; ++m) _Pragma("unroll") for (int k = 0; k < 2; ++k) dst[m][k] = *(const PG8_LAS bf16x8*)(lds + PG8_SA(b, h) + aoff + m * 2048 + k * 1024); } while (0)
; #define PG8_LDB(dst, b, h) do { _Pragma("unroll") for (int n = 0; n < 2; ++n) _Pragma("unroll") for (int k = 0; k < 2; ++k) dst[n][k] = *(const PG8_LAS bf16x8*)(lds + PG8_SB(b, h) + boff + n * 2048 + k * 1024); } while (0)
; template <class Epi, class Sched, bool ALIGN_EPI = false, bool SP2 = false>
; __device__ __forceinline__ void gemm_phase(PG8_LAS unsigned char* lds, const Gemm g, const Sched& S, const Epi& E) {
;     ...
;         for (int t = 0; t < nt; t += 2) {
;             const bool last = (t == nt - 2);
;             const char* a1 = cA + (size_t)(t + 1) * kstep;
;             const char* a2 = last ? nA : cA + (size_t)(t + 2) * kstep; const char* b2 = last ? nB : cB + (size_t)(t + 2) * kstep;
;             const char* a3 = a2 + kstep; const char* b3 = b2 + kstep;
;             if (last && has_next) S.a_ready(nxt);
;             if constexpr (SP2) {
;             PG8_LDB(B0, 0, 0); PG8_LDB(B1, 0, 1); PG8_SCHED; PG8_LDA(At, 0, 0); PG8_STAGE(PG8_SA(1, 1), a1 + hstep, voffA);
;             PG8_WAIT_V(8); PG8_WAIT_L(0); PG8_BAR; PG8_MMA(0, 0, At, B0); PG8_MMA(0, 1, At, B1); PG8_BAR; PG8_SCHED;
;             PG8_LDA(At, 0, 1); PG8_STAGE(PG8_SB(0, 0), b2, voffB); PG8_STAGE(PG8_SB(0, 1), b2 + hstep, voffB); PG8_STAGE(PG8_SA(0, 0), a2, voffA);
;             PG8_WAIT_V(8); PG8_WAIT_L(0); PG8_BAR; PG8_MMA(1, 0, At, B0); PG8_MMA(1, 1, At, B1); PG8_BAR; PG8_SCHED;
;             PG8_LDB(B0, 1, 0); PG8_LDB(B1, 1, 1); PG8_SCHED; PG8_LDA(At, 1, 0); PG8_STAGE(PG8_SA(0, 1), a2 + hstep, voffA);
;             PG8_WAIT_V(8); PG8_WAIT_L(0); PG8_BAR; PG8_MMA(0, 0, At, B0); PG8_MMA(0, 1, At, B1); PG8_BAR; PG8_SCHED;
;             PG8_LDA(At, 1, 1); PG8_STAGE(PG8_SB(1, 0), b3, voffB); PG8_STAGE(PG8_SB(1, 1), b3 + hstep, voffB); PG8_STAGE(PG8_SA(1, 0), a3, voffA);
;             PG8_WAIT_V(8); PG8_WAIT_L(0); PG8_BAR; PG8_MMA(1, 0, At, B0); PG8_MMA(1, 1, At, B1); PG8_BAR; PG8_SCHED;
	s_add_u32 s98, s22, 0x80
	s_addc_u32 s99, s23, 0
	s_add_u32 s100, s24, 0xfff80080
	s_addc_u32 s101, s25, -1
	s_add_i32 s24, s55, s29
	s_mov_b32 m0, s24
	ds_read_b128 v[188:191], v178 offset:49152
	ds_read_b128 v[192:195], v178 offset:50176
	ds_read_b128 v[196:199], v178 offset:51200
	ds_read_b128 v[200:203], v178 offset:52224
	ds_read_b128 v[204:207], v178 offset:53248
	ds_read_b128 v[214:217], v178 offset:54272
	ds_read_b128 v[218:221], v178 offset:55296
	ds_read_b128 v[222:225], v178 offset:56320
	global_load_lds_dwordx4 v156, s[98:99]
	s_add_i32 m0, s24, 0x2000
	s_add_u32 s22, s22, 0x80080
	s_addc_u32 s23, s23, 0
	s_add_i32 s24, s56, s29
	global_load_lds_dwordx4 v160, s[98:99]
	s_mov_b32 m0, s24
	s_nop 0
	global_load_lds_dwordx4 v156, s[22:23]
	s_add_i32 m0, s24, 0x2000
	s_nop 0
	global_load_lds_dwordx4 v160, s[22:23]
	s_mov_b32 m0, s38
	s_nop 0
	global_load_lds_dwordx4 v154, s[100:101]
	s_mov_b32 m0, s39
	s_nop 0
	global_load_lds_dwordx4 v158, s[100:101]
	s_waitcnt vmcnt(8)
	s_waitcnt lgkmcnt(0)
	s_barrier
	s_setprio 1
	s_waitcnt lgkmcnt(0)
	v_mfma_f32_16x16x32_bf16 v[62:65], v[130:133], v[188:191], v[62:65]
	v_mfma_f32_16x16x32_bf16 v[58:61], v[138:141], v[188:191], v[58:61]
	v_mfma_f32_16x16x32_bf16 v[42:45], v[138:141], v[196:199], v[42:45]
	v_mfma_f32_16x16x32_bf16 v[50:53], v[130:133], v[196:199], v[50:53]
	v_mfma_f32_16x16x32_bf16 v[34:37], v[130:133], v[204:207], v[34:37]
	v_mfma_f32_16x16x32_bf16 v[26:29], v[138:141], v[204:207], v[26:29]
	v_mfma_f32_16x16x32_bf16 v[10:13], v[138:141], v[218:221], v[10:13]
	v_mfma_f32_16x16x32_bf16 v[18:21], v[130:133], v[218:221], v[18:21]
	v_mfma_f32_16x16x32_bf16 v[62:65], v[134:137], v[192:195], v[62:65]
	v_mfma_f32_16x16x32_bf16 v[58:61], v[142:145], v[192:195], v[58:61]
	v_mfma_f32_16x16x32_bf16 v[42:45], v[142:145], v[200:203], v[42:45]
	v_mfma_f32_16x16x32_bf16 v[50:53], v[134:137], v[200:203], v[50:53]
	v_mfma_f32_16x16x32_bf16 v[34:37], v[134:137], v[214:217], v[34:37]
	v_mfma_f32_16x16x32_bf16 v[26:29], v[142:145], v[214:217], v[26:29]
	v_mfma_f32_16x16x32_bf16 v[10:13], v[142:145], v[222:225], v[10:13]
	v_mfma_f32_16x16x32_bf16 v[18:21], v[134:137], v[222:225], v[18:21]
	s_setprio 0
	s_setprio 1
	v_mfma_f32_16x16x32_bf16 v[54:57], v[146:149], v[188:191], v[54:57]
	v_mfma_f32_16x16x32_bf16 v[46:49], v[170:173], v[188:191], v[46:49]
	v_mfma_f32_16x16x32_bf16 v[30:33], v[170:173], v[196:199], v[30:33]
	v_mfma_f32_16x16x32_bf16 v[38:41], v[146:149], v[196:199], v[38:41]
	v_mfma_f32_16x16x32_bf16 v[22:25], v[146:149], v[204:207], v[22:25]
	v_mfma_f32_16x16x32_bf16 v[14:17], v[170:173], v[204:207], v[14:17]
	v_mfma_f32_16x16x32_bf16 v[2:5], v[170:173], v[218:221], v[2:5]
	v_mfma_f32_16x16x32_bf16 v[6:9], v[146:149], v[218:221], v[6:9]
	v_mfma_f32_16x16x32_bf16 v[54:57], v[150:153], v[192:195], v[54:57]
	v_mfma_f32_16x16x32_bf16 v[46:49], v[180:183], v[192:195], v[46:49]
	v_mfma_f32_16x16x32_bf16 v[30:33], v[180:183], v[200:203], v[30:33]
	v_mfma_f32_16x16x32_bf16 v[38:41], v[150:153], v[200:203], v[38:41]
	v_mfma_f32_16x16x32_bf16 v[22:25], v[150:153], v[214:217], v[22:25]
	v_mfma_f32_16x16x32_bf16 v[14:17], v[180:183], v[214:217], v[14:17]
	v_mfma_f32_16x16x32_bf16 v[2:5], v[180:183], v[222:225], v[2:5]
	v_mfma_f32_16x16x32_bf16 v[6:9], v[150:153], v[222:225], v[6:9]
	s_setprio 0
	s_barrier
	s_add_i32 s54, s54, 2
	s_add_u32 s20, s20, 0x100
	s_addc_u32 s21, s21, 0
	s_add_u32 s52, s52, 0x100
	s_addc_u32 s53, s53, 0
	s_cmp_gt_u32 s54, 29
.LBB0_1456:
	ds_read_b128 v[130:133], v176
	ds_read_b128 v[134:137], v176 offset:1024
	ds_read_b128 v[138:141], v176 offset:2048
	ds_read_b128 v[142:145], v176 offset:3072
	ds_read_b128 v[146:149], v177
	ds_read_b128 v[150:153], v177 offset:1024
	ds_read_b128 v[170:173], v177 offset:2048
	ds_read_b128 v[180:183], v177 offset:3072
	s_add_u32 s22, s20, 0xfff80080
	s_addc_u32 s23, s21, -1
	s_cmp_eq_u32 s54, 28
	s_cselect_b32 s25, s13, s23
	s_cselect_b32 s24, s50, s22
	s_cselect_b32 s23, s11, s53
	s_cselect_b32 s22, s51, s52
	s_add_i32 m0, s19, 0xc000
	ds_read_b128 v[188:191], v178
	ds_read_b128 v[192:195], v178 offset:1024
	ds_read_b128 v[196:199], v178 offset:2048
	ds_read_b128 v[200:203], v178 offset:3072
	ds_read_b128 v[204:207], v178 offset:4096
	ds_read_b128 v[214:217], v178 offset:5120
	ds_read_b128 v[218:221], v178 offset:6144
	ds_read_b128 v[222:225], v178 offset:7168
	global_load_lds_dwordx4 v162, s[20:21]
	s_add_i32 m0, s19, 0xe000
	s_nop 0
	global_load_lds_dwordx4 v164, s[20:21]
	s_waitcnt vmcnt(8)
	s_waitcnt lgkmcnt(0)
	s_barrier
; #define PG8_STAGE(bufoff, gbase, voff) do { _Pragma("unroll") for (int _i = 0; _i < 2; ++_i) \
;         __builtin_amdgcn_global_load_lds((const unsigned*)((const char*)(gbase) + (voff)[_i]), (PG8_LAS unsigned*)(lds + (bufoff) + ldsw + _i * 8192), 16, 0, 0); } while (0)
; #define PG8_LDA(dst, b, h) do { _Pragma("unroll") for (int m = 0; m < 4; ++m) _Pragma("unroll") for (int k = 0; k < 2; ++k) dst[m][k] = *(const PG8_LAS bf16x8*)(lds + PG8_SA(b, h) + aoff + m * 2048 + k * 1024); } while (0)
; #define PG8_LDB(dst, b, h) do { _Pragma("unroll") for (int n = 0; n < 2; ++n) _Pragma("unroll") for (int k = 0; k < 2; ++k) dst[n][k] = *(const PG8_LAS bf16x8*)(lds + PG8_SB(b, h) + boff + n * 2048 + k * 1024); } while (0)
; #define PG8_WAIT_V(n) asm volatile("s_waitcnt vmcnt(" #n ")" ::: "memory")
; #define PG8_WAIT_L(n) asm volatile("s_waitcnt lgkmcnt(" #n ")" ::: "memory")
; #define PG8_BAR __builtin_amdgcn_s_barrier()
; #define PG8_SCHED __builtin_amdgcn_sched_barrier(0)
; template <class Epi, class Sched, bool ALIGN_EPI = false, bool SP2 = false>
; __device__ __forceinline__ void gemm_phase(PG8_LAS unsigned char* lds, const Gemm g, const Sched& S, const Epi& E) {
;     ...
;             PG8_LDB(B0, 0, 0); PG8_LDB(B1, 0, 1); PG8_SCHED; PG8_LDA(At, 0, 0); PG8_STAGE(PG8_SA(1, 1), a1 + hstep, voffA);
;             PG8_WAIT_V(8); PG8_WAIT_L(0); PG8_BAR; PG8_MMA(0, 0, At, B0); PG8_MMA(0, 1, At, B1); PG8_BAR; PG8_SCHED;
;             PG8_LDA(At, 0, 1); PG8_STAGE(PG8_SB(0, 0), b2, voffB); PG8_STAGE(PG8_SB(0, 1), b2 + hstep, voffB); PG8_STAGE(PG8_SA(0, 0), a2, voffA);
;             PG8_WAIT_V(8); PG8_WAIT_L(0); PG8_BAR; PG8_MMA(1, 0, At, B0); PG8_MMA(1, 1, At, B1); PG8_BAR; PG8_SCHED;
	s_setprio 1
	s_waitcnt lgkmcnt(0)
	v_mfma_f32_16x16x32_bf16 v[126:129], v[130:133], v[188:191], v[126:129]
	v_mfma_f32_16x16x32_bf16 v[122:125], v[138:141], v[188:191], v[122:125]
	v_mfma_f32_16x16x32_bf16 v[106:109], v[138:141], v[196:199], v[106:109]
	v_mfma_f32_16x16x32_bf16 v[110:113], v[130:133], v[196:199], v[110:113]
	v_mfma_f32_16x16x32_bf16 v[98:101], v[130:133], v[204:207], v[98:101]
	v_mfma_f32_16x16x32_bf16 v[90:93], v[138:141], v[204:207], v[90:93]
	v_mfma_f32_16x16x32_bf16 v[74:77], v[138:141], v[218:221], v[74:77]
	v_mfma_f32_16x16x32_bf16 v[82:85], v[130:133], v[218:221], v[82:85]
	v_mfma_f32_16x16x32_bf16 v[126:129], v[134:137], v[192:195], v[126:129]
	v_mfma_f32_16x16x32_bf16 v[122:125], v[142:145], v[192:195], v[122:125]
	v_mfma_f32_16x16x32_bf16 v[106:109], v[142:145], v[200:203], v[106:109]
	v_mfma_f32_16x16x32_bf16 v[110:113], v[134:137], v[200:203], v[110:113]
	v_mfma_f32_16x16x32_bf16 v[98:101], v[134:137], v[214:217], v[98:101]
	v_mfma_f32_16x16x32_bf16 v[90:93], v[142:145], v[214:217], v[90:93]
	v_mfma_f32_16x16x32_bf16 v[74:77], v[142:145], v[222:225], v[74:77]
	v_mfma_f32_16x16x32_bf16 v[82:85], v[134:137], v[222:225], v[82:85]
	s_setprio 0
	s_setprio 1
	v_mfma_f32_16x16x32_bf16 v[118:121], v[146:149], v[188:191], v[118:121]
	v_mfma_f32_16x16x32_bf16 v[114:117], v[170:173], v[188:191], v[114:117]
	v_mfma_f32_16x16x32_bf16 v[94:97], v[170:173], v[196:199], v[94:97]
	v_mfma_f32_16x16x32_bf16 v[102:105], v[146:149], v[196:199], v[102:105]
	v_mfma_f32_16x16x32_bf16 v[86:89], v[146:149], v[204:207], v[86:89]
	v_mfma_f32_16x16x32_bf16 v[78:81], v[170:173], v[204:207], v[78:81]
	v_mfma_f32_16x16x32_bf16 v[66:69], v[170:173], v[218:221], v[66:69]
	v_mfma_f32_16x16x32_bf16 v[70:73], v[146:149], v[218:221], v[70:73]
	v_mfma_f32_16x16x32_bf16 v[118:121], v[150:153], v[192:195], v[118:121]
	v_mfma_f32_16x16x32_bf16 v[114:117], v[180:183], v[192:195], v[114:117]
	v_mfma_f32_16x16x32_bf16 v[94:97], v[180:183], v[200:203], v[94:97]
	v_mfma_f32_16x16x32_bf16 v[102:105], v[150:153], v[200:203], v[102:105]
	v_mfma_f32_16x16x32_bf16 v[86:89], v[150:153], v[214:217], v[86:89]
	v_mfma_f32_16x16x32_bf16 v[78:81], v[180:183], v[214:217], v[78:81]
	v_mfma_f32_16x16x32_bf16 v[66:69], v[180:183], v[222:225], v[66:69]
	v_mfma_f32_16x16x32_bf16 v[70:73], v[150:153], v[222:225], v[70:73]
	s_setprio 0
	s_barrier
	s_add_i32 s55, s42, s29
	s_mov_b32 m0, s55
	ds_read_b128 v[188:191], v178 offset:16384
	ds_read_b128 v[192:195], v178 offset:17408
	ds_read_b128 v[196:199], v178 offset:18432
	ds_read_b128 v[200:203], v178 offset:19456
	ds_read_b128 v[204:207], v178 offset:20480
	ds_read_b128 v[214:217], v178 offset:21504
	ds_read_b128 v[218:221], v178 offset:22528
	ds_read_b128 v[222:225], v178 offset:23552
	global_load_lds_dwordx4 v156, s[22:23]
	s_add_i32 m0, s55, 0x2000
	s_add_u32 s56, s22, 0x80000
	s_addc_u32 s57, s23, 0
	s_add_i32 s55, s43, s29
	global_load_lds_dwordx4 v160, s[22:23]
	s_mov_b32 m0, s55
	s_nop 0
	global_load_lds_dwordx4 v156, s[56:57]
	s_add_i32 m0, s55, 0x2000
	s_nop 0
	global_load_lds_dwordx4 v160, s[56:57]
	s_mov_b32 m0, s19
	s_nop 0
	global_load_lds_dwordx4 v154, s[24:25]
	s_mov_b32 m0, s30
	s_nop 0
	global_load_lds_dwordx4 v158, s[24:25]
	s_waitcnt vmcnt(8)
	s_waitcnt lgkmcnt(0)
	s_barrier
	s_setprio 1
	s_waitcnt lgkmcnt(0)
	v_mfma_f32_16x16x32_bf16 v[62:65], v[130:133], v[188:191], v[62:65]
	v_mfma_f32_16x16x32_bf16 v[58:61], v[138:141], v[188:191], v[58:61]
	v_mfma_f32_16x16x32_bf16 v[42:45], v[138:141], v[196:199], v[42:45]
	v_mfma_f32_16x16x32_bf16 v[50:53], v[130:133], v[196:199], v[50:53]
	v_mfma_f32_16x16x32_bf16 v[34:37], v[130:133], v[204:207], v[34:37]
	v_mfma_f32_16x16x32_bf16 v[26:29], v[138:141], v[204:207], v[26:29]
	v_mfma_f32_16x16x32_bf16 v[10:13], v[138:141], v[218:221], v[10:13]
	v_mfma_f32_16x16x32_bf16 v[18:21], v[130:133], v[218:221], v[18:21]
	v_mfma_f32_16x16x32_bf16 v[62:65], v[134:137], v[192:195], v[62:65]
	v_mfma_f32_16x16x32_bf16 v[58:61], v[142:145], v[192:195], v[58:61]
	v_mfma_f32_16x16x32_bf16 v[42:45], v[142:145], v[200:203], v[42:45]
	v_mfma_f32_16x16x32_bf16 v[50:53], v[134:137], v[200:203], v[50:53]
	v_mfma_f32_16x16x32_bf16 v[34:37], v[134:137], v[214:217], v[34:37]
	v_mfma_f32_16x16x32_bf16 v[26:29], v[142:145], v[214:217], v[26:29]
	v_mfma_f32_16x16x32_bf16 v[10:13], v[142:145], v[222:225], v[10:13]
	v_mfma_f32_16x16x32_bf16 v[18:21], v[134:137], v[222:225], v[18:21]
	s_setprio 0
	s_setprio 1
	v_mfma_f32_16x16x32_bf16 v[54:57], v[146:149], v[188:191], v[54:57]
	v_mfma_f32_16x16x32_bf16 v[46:49], v[170:173], v[188:191], v[46:49]
	v_mfma_f32_16x16x32_bf16 v[30:33], v[170:173], v[196:199], v[30:33]
	v_mfma_f32_16x16x32_bf16 v[38:41], v[146:149], v[196:199], v[38:41]
	v_mfma_f32_16x16x32_bf16 v[22:25], v[146:149], v[204:207], v[22:25]
	v_mfma_f32_16x16x32_bf16 v[14:17], v[170:173], v[204:207], v[14:17]
	v_mfma_f32_16x16x32_bf16 v[2:5], v[170:173], v[218:221], v[2:5]
	v_mfma_f32_16x16x32_bf16 v[6:9], v[146:149], v[218:221], v[6:9]
	v_mfma_f32_16x16x32_bf16 v[54:57], v[150:153], v[192:195], v[54:57]
	v_mfma_f32_16x16x32_bf16 v[46:49], v[180:183], v[192:195], v[46:49]
	v_mfma_f32_16x16x32_bf16 v[30:33], v[180:183], v[200:203], v[30:33]
	v_mfma_f32_16x16x32_bf16 v[38:41], v[150:153], v[200:203], v[38:41]
	v_mfma_f32_16x16x32_bf16 v[22:25], v[150:153], v[214:217], v[22:25]
	v_mfma_f32_16x16x32_bf16 v[14:17], v[180:183], v[214:217], v[14:17]
	v_mfma_f32_16x16x32_bf16 v[2:5], v[180:183], v[222:225], v[2:5]
	v_mfma_f32_16x16x32_bf16 v[6:9], v[150:153], v[222:225], v[6:9]
	s_setprio 0
	s_barrier
; #define PG8_STAGE(bufoff, gbase, voff) do { _Pragma("unroll") for (int _i = 0; _i < 2; ++_i) \
;         __builtin_amdgcn_global_load_lds((const unsigned*)((const char*)(gbase) + (voff)[_i]), (PG8_LAS unsigned*)(lds + (bufoff) + ldsw + _i * 8192), 16, 0, 0); } while (0)
; #define PG8_LDA(dst, b, h) do { _Pragma("unroll") for (int m = 0; m < 4; ++m) _Pragma("unroll") for (int k = 0; k < 2; ++k) dst[m][k] = *(const PG8_LAS bf16x8*)(lds + PG8_SA(b, h) + aoff + m * 2048 + k * 1024); } while (0)
; #define PG8_LDB(dst, b, h) do { _Pragma("unroll") for (int n = 0; n < 2; ++n) _Pragma("unroll") for (int k = 0; k < 2; ++k) dst[n][k] = *(const PG8_LAS bf16x8*)(lds + PG8_SB(b, h) + boff + n * 2048 + k * 1024); } while (0)
; #define PG8_WAIT_V(n) asm volatile("s_waitcnt vmcnt(" #n ")" ::: "memory")
; #define PG8_WAIT_L(n) asm volatile("s_waitcnt lgkmcnt(" #n ")" ::: "memory")
; #define PG8_BAR __builtin_amdgcn_s_barrier()
; #define PG8_SCHED __builtin_amdgcn_sched_barrier(0)
; template <class Epi, class Sched, bool ALIGN_EPI = false, bool SP2 = false>
; __device__ __forceinline__ void gemm_phase(PG8_LAS unsigned char* lds, const Gemm g, const Sched& S, const Epi& E) {
;     ...
;             PG8_LDB(B0, 1, 0); PG8_LDB(B1, 1, 1); PG8_SCHED; PG8_LDA(At, 1, 0); PG8_STAGE(PG8_SA(0, 1), a2 + hstep, voffA);
;             PG8_WAIT_V(8); PG8_WAIT_L(0); PG8_BAR; PG8_MMA(0, 0, At, B0); PG8_MMA(0, 1, At, B1); PG8_BAR; PG8_SCHED;
;             PG8_LDA(At, 1, 1); PG8_STAGE(PG8_SB(1, 0), b3, voffB); PG8_STAGE(PG8_SB(1, 1), b3 + hstep, voffB); PG8_STAGE(PG8_SA(1, 0), a3, voffA);
;             PG8_WAIT_V(8); PG8_WAIT_L(0); PG8_BAR; PG8_MMA(1, 0, At, B0); PG8_MMA(1, 1, At, B1); PG8_BAR; PG8_SCHED;
	s_add_i32 s55, 0, 0x18000
	s_add_i32 s56, 0, 0x1c000
	ds_read_b128 v[130:133], v248
	ds_read_b128 v[134:137], v248 offset:1024
	ds_read_b128 v[138:141], v248 offset:2048
	ds_read_b128 v[142:145], v248 offset:3072
	ds_read_b128 v[146:149], v249
	ds_read_b128 v[150:153], v249 offset:1024
	ds_read_b128 v[170:173], v249 offset:2048
	ds_read_b128 v[180:183], v249 offset:3072
	s_add_u32 s24, s24, 0x80000
	s_addc_u32 s25, s25, 0
	s_mov_b32 m0, s31
	ds_read_b128 v[188:191], v178 offset:32768
	ds_read_b128 v[192:195], v178 offset:33792
	ds_read_b128 v[196:199], v178 offset:34816
	ds_read_b128 v[200:203], v178 offset:35840
	ds_read_b128 v[204:207], v178 offset:36864
	ds_read_b128 v[214:217], v178 offset:37888
	ds_read_b128 v[218:221], v178 offset:38912
	ds_read_b128 v[222:225], v178 offset:39936
	global_load_lds_dwordx4 v154, s[24:25]
	s_mov_b32 m0, s33
	s_nop 0
	global_load_lds_dwordx4 v158, s[24:25]
	s_waitcnt vmcnt(8)
	s_waitcnt lgkmcnt(0)
	s_barrier
	s_setprio 1
	s_waitcnt lgkmcnt(0)
	v_mfma_f32_16x16x32_bf16 v[126:129], v[130:133], v[188:191], v[126:129]
	v_mfma_f32_16x16x32_bf16 v[122:125], v[138:141], v[188:191], v[122:125]
	v_mfma_f32_16x16x32_bf16 v[106:109], v[138:141], v[196:199], v[106:109]
	v_mfma_f32_16x16x32_bf16 v[110:113], v[130:133], v[196:199], v[110:113]
	v_mfma_f32_16x16x32_bf16 v[98:101], v[130:133], v[204:207], v[98:101]
	v_mfma_f32_16x16x32_bf16 v[90:93], v[138:141], v[204:207], v[90:93]
	v_mfma_f32_16x16x32_bf16 v[74:77], v[138:141], v[218:221], v[74:77]
	v_mfma_f32_16x16x32_bf16 v[82:85], v[130:133], v[218:221], v[82:85]
	v_mfma_f32_16x16x32_bf16 v[126:129], v[134:137], v[192:195], v[126:129]
	v_mfma_f32_16x16x32_bf16 v[122:125], v[142:145], v[192:195], v[122:125]
	v_mfma_f32_16x16x32_bf16 v[106:109], v[142:145], v[200:203], v[106:109]
	v_mfma_f32_16x16x32_bf16 v[110:113], v[134:137], v[200:203], v[110:113]
	v_mfma_f32_16x16x32_bf16 v[98:101], v[134:137], v[214:217], v[98:101]
	v_mfma_f32_16x16x32_bf16 v[90:93], v[142:145], v[214:217], v[90:93]
	v_mfma_f32_16x16x32_bf16 v[74:77], v[142:145], v[222:225], v[74:77]
	v_mfma_f32_16x16x32_bf16 v[82:85], v[134:137], v[222:225], v[82:85]
	s_setprio 0
	s_setprio 1
	v_mfma_f32_16x16x32_bf16 v[118:121], v[146:149], v[188:191], v[118:121]
	v_mfma_f32_16x16x32_bf16 v[114:117], v[170:173], v[188:191], v[114:117]
	v_mfma_f32_16x16x32_bf16 v[94:97], v[170:173], v[196:199], v[94:97]
	v_mfma_f32_16x16x32_bf16 v[102:105], v[146:149], v[196:199], v[102:105]
	v_mfma_f32_16x16x32_bf16 v[86:89], v[146:149], v[204:207], v[86:89]
	v_mfma_f32_16x16x32_bf16 v[78:81], v[170:173], v[204:207], v[78:81]
	v_mfma_f32_16x16x32_bf16 v[66:69], v[170:173], v[218:221], v[66:69]
	v_mfma_f32_16x16x32_bf16 v[70:73], v[146:149], v[218:221], v[70:73]
	v_mfma_f32_16x16x32_bf16 v[118:121], v[150:153], v[192:195], v[118:121]
	v_mfma_f32_16x16x32_bf16 v[114:117], v[180:183], v[192:195], v[114:117]
	v_mfma_f32_16x16x32_bf16 v[94:97], v[180:183], v[200:203], v[94:97]
	v_mfma_f32_16x16x32_bf16 v[102:105], v[150:153], v[200:203], v[102:105]
	v_mfma_f32_16x16x32_bf16 v[86:89], v[150:153], v[214:217], v[86:89]
	v_mfma_f32_16x16x32_bf16 v[78:81], v[180:183], v[214:217], v[78:81]
	v_mfma_f32_16x16x32_bf16 v[66:69], v[180:183], v[222:225], v[66:69]
	v_mfma_f32_16x16x32_bf16 v[70:73], v[150:153], v[222:225], v[70:73]
	s_setprio 0
	s_barrier
	s_add_u32 s98, s22, 0x80
	s_addc_u32 s99, s23, 0
	s_add_u32 s100, s24, 0xfff80080
	s_addc_u32 s101, s25, -1
	s_add_i32 s24, s55, s29
	s_mov_b32 m0, s24
	ds_read_b128 v[188:191], v178 offset:49152
	ds_read_b128 v[192:195], v178 offset:50176
	ds_read_b128 v[196:199], v178 offset:51200
	ds_read_b128 v[200:203], v178 offset:52224
	ds_read_b128 v[204:207], v178 offset:53248
	ds_read_b128 v[214:217], v178 offset:54272
	ds_read_b128 v[218:221], v178 offset:55296
	ds_read_b128 v[222:225], v178 offset:56320
	global_load_lds_dwordx4 v156, s[98:99]
	s_add_i32 m0, s24, 0x2000
	s_add_u32 s22, s22, 0x80080
	s_addc_u32 s23, s23, 0
	s_add_i32 s24, s56, s29
	global_load_lds_dwordx4 v160, s[98:99]
	s_mov_b32 m0, s24
	s_nop 0
	global_load_lds_dwordx4 v156, s[22:23]
	s_add_i32 m0, s24, 0x2000
	s_nop 0
	global_load_lds_dwordx4 v160, s[22:23]
	s_mov_b32 m0, s38
	s_nop 0
	global_load_lds_dwordx4 v154, s[100:101]
	s_mov_b32 m0, s39
	s_nop 0
	global_load_lds_dwordx4 v158, s[100:101]
	s_waitcnt vmcnt(8)
	s_waitcnt lgkmcnt(0)
	s_barrier
	s_setprio 1
	s_waitcnt lgkmcnt(0)
	v_mfma_f32_16x16x32_bf16 v[62:65], v[130:133], v[188:191], v[62:65]
	v_mfma_f32_16x16x32_bf16 v[58:61], v[138:141], v[188:191], v[58:61]
	v_mfma_f32_16x16x32_bf16 v[42:45], v[138:141], v[196:199], v[42:45]
	v_mfma_f32_16x16x32_bf16 v[50:53], v[130:133], v[196:199], v[50:53]
	v_mfma_f32_16x16x32_bf16 v[34:37], v[130:133], v[204:207], v[34:37]
	v_mfma_f32_16x16x32_bf16 v[26:29], v[138:141], v[204:207], v[26:29]
	v_mfma_f32_16x16x32_bf16 v[10:13], v[138:141], v[218:221], v[10:13]
	v_mfma_f32_16x16x32_bf16 v[18:21], v[130:133], v[218:221], v[18:21]
	v_mfma_f32_16x16x32_bf16 v[62:65], v[134:137], v[192:195], v[62:65]
	v_mfma_f32_16x16x32_bf16 v[58:61], v[142:145], v[192:195], v[58:61]
	v_mfma_f32_16x16x32_bf16 v[42:45], v[142:145], v[200:203], v[42:45]
	v_mfma_f32_16x16x32_bf16 v[50:53], v[134:137], v[200:203], v[50:53]
	v_mfma_f32_16x16x32_bf16 v[34:37], v[134:137], v[214:217], v[34:37]
	v_mfma_f32_16x16x32_bf16 v[26:29], v[142:145], v[214:217], v[26:29]
	v_mfma_f32_16x16x32_bf16 v[10:13], v[142:145], v[222:225], v[10:13]
	v_mfma_f32_16x16x32_bf16 v[18:21], v[134:137], v[222:225], v[18:21]
	s_setprio 0
	s_setprio 1
	v_mfma_f32_16x16x32_bf16 v[54:57], v[146:149], v[188:191], v[54:57]
	v_mfma_f32_16x16x32_bf16 v[46:49], v[170:173], v[188:191], v[46:49]
	v_mfma_f32_16x16x32_bf16 v[30:33], v[170:173], v[196:199], v[30:33]
	v_mfma_f32_16x16x32_bf16 v[38:41], v[146:149], v[196:199], v[38:41]
	v_mfma_f32_16x16x32_bf16 v[22:25], v[146:149], v[204:207], v[22:25]
	v_mfma_f32_16x16x32_bf16 v[14:17], v[170:173], v[204:207], v[14:17]
	v_mfma_f32_16x16x32_bf16 v[2:5], v[170:173], v[218:221], v[2:5]
	v_mfma_f32_16x16x32_bf16 v[6:9], v[146:149], v[218:221], v[6:9]
	v_mfma_f32_16x16x32_bf16 v[54:57], v[150:153], v[192:195], v[54:57]
	v_mfma_f32_16x16x32_bf16 v[46:49], v[180:183], v[192:195], v[46:49]
	v_mfma_f32_16x16x32_bf16 v[30:33], v[180:183], v[200:203], v[30:33]
	v_mfma_f32_16x16x32_bf16 v[38:41], v[150:153], v[200:203], v[38:41]
	v_mfma_f32_16x16x32_bf16 v[22:25], v[150:153], v[214:217], v[22:25]
	v_mfma_f32_16x16x32_bf16 v[14:17], v[180:183], v[214:217], v[14:17]
	v_mfma_f32_16x16x32_bf16 v[2:5], v[180:183], v[222:225], v[2:5]
	v_mfma_f32_16x16x32_bf16 v[6:9], v[150:153], v[222:225], v[6:9]
	s_setprio 0
	s_barrier
	s_add_i32 s54, s54, 2
	s_add_u32 s20, s20, 0x100
	s_addc_u32 s21, s21, 0
	s_add_u32 s52, s52, 0x100
	s_addc_u32 s53, s53, 0
	s_cmp_gt_u32 s54, 29
	s_cbranch_scc0 .LBB0_1456
	s_and_b64 vcc, exec, s[8:9]
	s_cbranch_vccz .LBB0_1459
	s_barrier
